# fp8 MFMA segments reordered boustrophedon (consecutive MFMAs always share one operand tuple), on top of the int8 loop peel
# speedup vs baseline: 1.0108x; 1.0072x over previous
.LBB0_693:
	s_and_b32 s61, s35, 3
	s_lshl_b32 s5, s4, 13
	s_lshl_b32 s7, s61, 12
	s_add_u32 s48, s28, 0x80
	s_addc_u32 s49, s29, 0
	s_add_i32 s18, 0, 0x18000
	s_mov_b64 s[8:9], s[48:49]
	s_add_i32 s67, s18, s6
	v_mov_b32_e32 v2, v171
	s_waitcnt vmcnt(2)
	s_barrier
	s_mov_b32 m0, s67
	s_add_i32 s69, s67, 0x2000
	global_load_lds_dwordx4 v2, s[8:9]
	v_mov_b32_e32 v2, v173
	s_add_u32 s50, s28, 0x40080
	s_mov_b32 m0, s69
	s_addc_u32 s51, s29, 0
	s_add_i32 s19, 0, 0x1c000
	global_load_lds_dwordx4 v2, s[8:9]
	s_mov_b64 s[8:9], s[50:51]
	s_add_i32 s70, s19, s6
	v_mov_b32_e32 v2, v171
	s_mov_b32 m0, s70
	s_add_i32 s71, s70, 0x2000
	global_load_lds_dwordx4 v2, s[8:9]
	v_mov_b32_e32 v2, v173
	s_mov_b32 m0, s71
	v_lshlrev_b32_e32 v5, 6, v0
	global_load_lds_dwordx4 v2, s[8:9]
	v_and_b32_e32 v2, 48, v0
	v_and_b32_e32 v5, 0x3c0, v5
	v_and_b32_e32 v175, 15, v0
	v_and_b32_e32 v3, 32, v200
	v_or_b32_e32 v6, v5, v2
	v_lshl_or_b32 v176, v175, 6, v2
	v_bitop3_b32 v177, v5, v3, v2 bitop3:0x36
	v_bitop3_b32 v2, s7, v6, v3 bitop3:0xf6
	s_add_i32 s17, 0, 0x10000
	v_bitop3_b32 v4, v176, s5, v3 bitop3:0xde
	v_add_u32_e32 v162, s17, v2
	s_add_i32 s16, 0, 0x14000
	s_waitcnt vmcnt(6)
	s_barrier
	v_add_u32_e32 v163, s16, v2
	v_add_u32_e32 v164, 0, v4
	v_add_u32_e32 v165, s18, v2
	v_add_u32_e32 v166, s19, v2
	ds_read_b128 v[2:5], v162
	s_waitcnt lgkmcnt(0)
	ds_read_b128 v[6:9], v162 offset:1024
	s_waitcnt vmcnt(0)
	ds_read_b128 v[10:13], v162 offset:2048
	ds_read_b128 v[14:17], v162 offset:3072
	ds_read_b128 v[18:21], v163
	ds_read_b128 v[22:25], v163 offset:1024
	ds_read_b128 v[26:29], v163 offset:2048
	ds_read_b128 v[30:33], v163 offset:3072
	v_lshl_or_b32 v179, s4, 6, v175
	s_add_u32 s4, s0, 0x100
	s_addc_u32 s5, s1, 0
	s_add_u32 s44, s28, 0x100
	s_addc_u32 s45, s29, 0
	s_add_u32 s8, s0, 0x80
	s_addc_u32 s9, s1, 0
	v_mov_b32_e32 v66, v170
	s_add_i32 s72, s21, 0x8000
	ds_read_b128 v[34:37], v164
	ds_read_b128 v[38:41], v164 offset:1024
	ds_read_b128 v[42:45], v164 offset:2048
	ds_read_b128 v[46:49], v164 offset:3072
	ds_read_b128 v[50:53], v164 offset:4096
	ds_read_b128 v[54:57], v164 offset:5120
	ds_read_b128 v[58:61], v164 offset:6144
	ds_read_b128 v[62:65], v164 offset:7168
	s_mov_b32 m0, s72
	s_add_i32 s73, s21, 0xa000
	global_load_lds_dwordx4 v66, s[8:9]
	v_mov_b32_e32 v66, v172
	s_mov_b32 m0, s73
	s_nop 0
	global_load_lds_dwordx4 v66, s[8:9]
	s_add_u32 s8, s0, 0x40080
	s_addc_u32 s9, s1, 0
	v_mov_b32_e32 v66, v170
	s_add_i32 s74, s21, 0xc000
	s_mov_b32 m0, s74
	s_add_i32 s75, s21, 0xe000
	global_load_lds_dwordx4 v66, s[8:9]
	v_mov_b32_e32 v66, v172
	s_mov_b32 m0, s75
	s_add_u32 s42, s28, 0x180
	global_load_lds_dwordx4 v66, s[8:9]
	s_waitcnt vmcnt(8)
	s_waitcnt lgkmcnt(0)
	s_addc_u32 s43, s29, 0
	s_barrier
	s_setprio 1
	s_waitcnt lgkmcnt(0)
	v_mfma_f32_16x16x128_f8f6f4 v[158:161], v[2:9], v[34:41], 0
	v_mfma_f32_16x16x128_f8f6f4 v[154:157], v[10:17], v[34:41], 0
	v_mfma_f32_16x16x128_f8f6f4 v[150:153], v[18:25], v[34:41], 0
	v_mfma_f32_16x16x128_f8f6f4 v[146:149], v[26:33], v[34:41], 0
	v_mfma_f32_16x16x128_f8f6f4 v[122:125], v[26:33], v[42:49], 0
	v_mfma_f32_16x16x128_f8f6f4 v[102:105], v[18:25], v[42:49], 0
	v_mfma_f32_16x16x128_f8f6f4 v[114:117], v[10:17], v[42:49], 0
	v_mfma_f32_16x16x128_f8f6f4 v[110:113], v[2:9], v[42:49], 0
	v_mfma_f32_16x16x128_f8f6f4 v[134:137], v[2:9], v[50:57], 0
	v_mfma_f32_16x16x128_f8f6f4 v[138:141], v[10:17], v[50:57], 0
	v_mfma_f32_16x16x128_f8f6f4 v[130:133], v[18:25], v[50:57], 0
	v_mfma_f32_16x16x128_f8f6f4 v[142:145], v[26:33], v[50:57], 0
	v_mfma_f32_16x16x128_f8f6f4 v[98:101], v[26:33], v[58:65], 0
	v_mfma_f32_16x16x128_f8f6f4 v[106:109], v[18:25], v[58:65], 0
	v_mfma_f32_16x16x128_f8f6f4 v[118:121], v[10:17], v[58:65], 0
	v_mfma_f32_16x16x128_f8f6f4 v[126:129], v[2:9], v[58:65], 0
	s_setprio 0
	s_barrier
	s_mov_b64 s[8:9], s[44:45]
	v_mov_b32_e32 v50, v171
	s_add_i32 s76, s17, s6
	ds_read_b128 v[34:37], v164 offset:16384
	ds_read_b128 v[38:41], v164 offset:17408
	ds_read_b128 v[42:45], v164 offset:18432
	ds_read_b128 v[46:49], v164 offset:19456
	ds_read_b128 v[180:183], v164 offset:20480
	ds_read_b128 v[184:187], v164 offset:21504
	ds_read_b128 v[188:191], v164 offset:22528
	ds_read_b128 v[192:195], v164 offset:23552
	s_mov_b32 m0, s76
	s_add_i32 s77, s76, 0x2000
	global_load_lds_dwordx4 v50, s[8:9]
	v_mov_b32_e32 v50, v173
	s_add_u32 s52, s28, 0x40100
	s_mov_b32 m0, s77
	s_addc_u32 s53, s29, 0
	global_load_lds_dwordx4 v50, s[8:9]
	s_mov_b64 s[8:9], s[52:53]
	v_mov_b32_e32 v50, v171
	s_add_i32 s78, s16, s6
	s_mov_b32 m0, s78
	s_add_i32 s79, s78, 0x2000
	global_load_lds_dwordx4 v50, s[8:9]
	v_mov_b32_e32 v50, v173
	s_mov_b32 m0, s79
	s_nop 0
	global_load_lds_dwordx4 v50, s[8:9]
	s_waitcnt vmcnt(6)
	s_waitcnt lgkmcnt(0)
	s_barrier
	s_setprio 1
	s_waitcnt lgkmcnt(0)
	v_mfma_f32_16x16x128_f8f6f4 v[94:97], v[2:9], v[34:41], 0
	v_mfma_f32_16x16x128_f8f6f4 v[90:93], v[10:17], v[34:41], 0
	v_mfma_f32_16x16x128_f8f6f4 v[86:89], v[18:25], v[34:41], 0
	v_mfma_f32_16x16x128_f8f6f4 v[82:85], v[26:33], v[34:41], 0
	v_mfma_f32_16x16x128_f8f6f4 v[66:69], v[26:33], v[42:49], 0
	v_mfma_f32_16x16x128_f8f6f4 v[70:73], v[18:25], v[42:49], 0
	v_mfma_f32_16x16x128_f8f6f4 v[74:77], v[10:17], v[42:49], 0
	v_mfma_f32_16x16x128_f8f6f4 v[78:81], v[2:9], v[42:49], 0
	v_mfma_f32_16x16x128_f8f6f4 v[62:65], v[2:9], v[180:187], 0
	v_mfma_f32_16x16x128_f8f6f4 v[58:61], v[10:17], v[180:187], 0
	v_mfma_f32_16x16x128_f8f6f4 v[54:57], v[18:25], v[180:187], 0
	v_mfma_f32_16x16x128_f8f6f4 v[50:53], v[26:33], v[180:187], 0
	v_mfma_f32_16x16x128_f8f6f4 v[34:37], v[26:33], v[188:195], 0
	v_mfma_f32_16x16x128_f8f6f4 v[38:41], v[18:25], v[188:195], 0
	v_mfma_f32_16x16x128_f8f6f4 v[42:45], v[10:17], v[188:195], 0
	v_mfma_f32_16x16x128_f8f6f4 v[46:49], v[2:9], v[188:195], 0
	s_setprio 0
	s_barrier
	ds_read_b128 v[26:29], v165
	ds_read_b128 v[30:33], v165 offset:1024
	ds_read_b128 v[18:21], v165 offset:2048
	ds_read_b128 v[22:25], v165 offset:3072
	ds_read_b128 v[10:13], v166
	ds_read_b128 v[14:17], v166 offset:1024
	ds_read_b128 v[2:5], v166 offset:2048
	ds_read_b128 v[6:9], v166 offset:3072
	v_mov_b32_e32 v167, v170
	s_mov_b32 m0, s21
	ds_read_b128 v[180:183], v164 offset:32768
	ds_read_b128 v[184:187], v164 offset:33792
	ds_read_b128 v[188:191], v164 offset:34816
	ds_read_b128 v[192:195], v164 offset:35840
	ds_read_b128 v[202:205], v164 offset:36864
	ds_read_b128 v[206:209], v164 offset:37888
	ds_read_b128 v[210:213], v164 offset:38912
	ds_read_b128 v[214:217], v164 offset:39936
	s_nop 0
	global_load_lds_dwordx4 v167, s[4:5]
	v_mov_b32_e32 v167, v172
	s_mov_b32 m0, s60
	s_nop 0
	global_load_lds_dwordx4 v167, s[4:5]
	s_add_u32 s4, s0, 0x40100
	s_addc_u32 s5, s1, 0
	v_mov_b32_e32 v167, v170
	s_mov_b32 m0, s62
	s_nop 0
	global_load_lds_dwordx4 v167, s[4:5]
	v_mov_b32_e32 v167, v172
	s_mov_b32 m0, s63
	s_nop 0
	global_load_lds_dwordx4 v167, s[4:5]
	s_waitcnt vmcnt(8)
	s_waitcnt lgkmcnt(0)
	s_barrier
	s_setprio 1
	s_waitcnt lgkmcnt(0)
	v_mfma_f32_16x16x128_f8f6f4 v[158:161], v[26:33], v[180:187], v[158:161]
	v_mfma_f32_16x16x128_f8f6f4 v[154:157], v[18:25], v[180:187], v[154:157]
	v_mfma_f32_16x16x128_f8f6f4 v[150:153], v[10:17], v[180:187], v[150:153]
	v_mfma_f32_16x16x128_f8f6f4 v[146:149], v[2:9], v[180:187], v[146:149]
	v_mfma_f32_16x16x128_f8f6f4 v[122:125], v[2:9], v[188:195], v[122:125]
	v_mfma_f32_16x16x128_f8f6f4 v[102:105], v[10:17], v[188:195], v[102:105]
	v_mfma_f32_16x16x128_f8f6f4 v[114:117], v[18:25], v[188:195], v[114:117]
	v_mfma_f32_16x16x128_f8f6f4 v[110:113], v[26:33], v[188:195], v[110:113]
	v_mfma_f32_16x16x128_f8f6f4 v[134:137], v[26:33], v[202:209], v[134:137]
	v_mfma_f32_16x16x128_f8f6f4 v[138:141], v[18:25], v[202:209], v[138:141]
	v_mfma_f32_16x16x128_f8f6f4 v[130:133], v[10:17], v[202:209], v[130:133]
	v_mfma_f32_16x16x128_f8f6f4 v[142:145], v[2:9], v[202:209], v[142:145]
	v_mfma_f32_16x16x128_f8f6f4 v[98:101], v[2:9], v[210:217], v[98:101]
	v_mfma_f32_16x16x128_f8f6f4 v[106:109], v[10:17], v[210:217], v[106:109]
	v_mfma_f32_16x16x128_f8f6f4 v[118:121], v[18:25], v[210:217], v[118:121]
	v_mfma_f32_16x16x128_f8f6f4 v[126:129], v[26:33], v[210:217], v[126:129]
	s_setprio 0
	s_barrier
	s_mov_b64 s[4:5], s[42:43]
	v_mov_b32_e32 v167, v171
	s_mov_b32 m0, s67
	ds_read_b128 v[180:183], v164 offset:49152
	ds_read_b128 v[184:187], v164 offset:50176
	ds_read_b128 v[188:191], v164 offset:51200
	ds_read_b128 v[192:195], v164 offset:52224
	ds_read_b128 v[202:205], v164 offset:53248
	ds_read_b128 v[206:209], v164 offset:54272
	ds_read_b128 v[210:213], v164 offset:55296
	ds_read_b128 v[214:217], v164 offset:56320
	s_add_u32 s64, s28, 0x40180
	global_load_lds_dwordx4 v167, s[4:5]
	v_mov_b32_e32 v167, v173
	s_mov_b32 m0, s69
	s_addc_u32 s65, s29, 0
	global_load_lds_dwordx4 v167, s[4:5]
	s_mov_b64 s[4:5], s[64:65]
	v_mov_b32_e32 v167, v171
	s_mov_b32 m0, s70
	s_nop 0
	global_load_lds_dwordx4 v167, s[4:5]
	v_mov_b32_e32 v167, v173
	s_mov_b32 m0, s71
	s_nop 0
	global_load_lds_dwordx4 v167, s[4:5]
	s_waitcnt vmcnt(6)
	s_waitcnt lgkmcnt(0)
	s_barrier
	s_setprio 1
	s_waitcnt lgkmcnt(0)
	v_mfma_f32_16x16x128_f8f6f4 v[94:97], v[26:33], v[180:187], v[94:97]
	v_mfma_f32_16x16x128_f8f6f4 v[90:93], v[18:25], v[180:187], v[90:93]
	v_mfma_f32_16x16x128_f8f6f4 v[86:89], v[10:17], v[180:187], v[86:89]
	v_mfma_f32_16x16x128_f8f6f4 v[82:85], v[2:9], v[180:187], v[82:85]
	v_mfma_f32_16x16x128_f8f6f4 v[66:69], v[2:9], v[188:195], v[66:69]
	v_mfma_f32_16x16x128_f8f6f4 v[70:73], v[10:17], v[188:195], v[70:73]
	v_mfma_f32_16x16x128_f8f6f4 v[74:77], v[18:25], v[188:195], v[74:77]
	v_mfma_f32_16x16x128_f8f6f4 v[78:81], v[26:33], v[188:195], v[78:81]
	v_mfma_f32_16x16x128_f8f6f4 v[62:65], v[26:33], v[202:209], v[62:65]
	v_mfma_f32_16x16x128_f8f6f4 v[58:61], v[18:25], v[202:209], v[58:61]
	v_mfma_f32_16x16x128_f8f6f4 v[54:57], v[10:17], v[202:209], v[54:57]
	v_mfma_f32_16x16x128_f8f6f4 v[50:53], v[2:9], v[202:209], v[50:53]
	v_mfma_f32_16x16x128_f8f6f4 v[34:37], v[2:9], v[210:217], v[34:37]
	v_mfma_f32_16x16x128_f8f6f4 v[38:41], v[10:17], v[210:217], v[38:41]
	v_mfma_f32_16x16x128_f8f6f4 v[42:45], v[18:25], v[210:217], v[42:45]
	v_mfma_f32_16x16x128_f8f6f4 v[46:49], v[26:33], v[210:217], v[46:49]
	s_setprio 0
	s_barrier
	s_and_b32 s4, s12, 7
	s_lshl_b32 s4, s4, 22
	s_lshl_b32 s5, s11, 19
	s_or_b32 s4, s4, s5
	s_add_u32 s4, s56, s4
	s_addc_u32 s5, s57, 0
	s_add_u32 s8, s4, 0x3ab00100
	s_addc_u32 s9, s5, 0
	s_add_u32 s2, s56, s2
	s_addc_u32 s3, s57, s3
	s_add_u32 s30, s2, 0xf00200
	s_addc_u32 s31, s3, 0
	s_mov_b64 s[2:3], s[30:31]
.LBB0_694:
	ds_read_b128 v[10:13], v162
	ds_read_b128 v[14:17], v162 offset:1024
	ds_read_b128 v[2:5], v162 offset:2048
	ds_read_b128 v[6:9], v162 offset:3072
	ds_read_b128 v[26:29], v163
	ds_read_b128 v[30:33], v163 offset:1024
	ds_read_b128 v[18:21], v163 offset:2048
	ds_read_b128 v[22:25], v163 offset:3072
	s_add_u32 s4, s8, 0x100
	s_addc_u32 s5, s9, 0
	s_cmp_eq_u32 s66, 12
	s_cselect_b32 s7, s29, s3
	s_cselect_b32 s6, s28, s2
	s_cselect_b32 s15, s1, s5
	s_cselect_b32 s14, s0, s4
	s_add_u32 s80, s8, 0x80
	s_addc_u32 s81, s9, 0
	v_mov_b32_e32 v167, v170
	s_mov_b32 m0, s72
	ds_read_b128 v[180:183], v164
	ds_read_b128 v[184:187], v164 offset:1024
	ds_read_b128 v[188:191], v164 offset:2048
	ds_read_b128 v[192:195], v164 offset:3072
	ds_read_b128 v[202:205], v164 offset:4096
	ds_read_b128 v[206:209], v164 offset:5120
	ds_read_b128 v[210:213], v164 offset:6144
	ds_read_b128 v[214:217], v164 offset:7168
	s_add_u32 s8, s8, 0x40080
	global_load_lds_dwordx4 v167, s[80:81]
	v_mov_b32_e32 v167, v172
	s_mov_b32 m0, s73
	s_addc_u32 s9, s9, 0
	global_load_lds_dwordx4 v167, s[80:81]
	v_mov_b32_e32 v167, v170
	s_mov_b32 m0, s74
	s_nop 0
	global_load_lds_dwordx4 v167, s[8:9]
	v_mov_b32_e32 v167, v172
	s_mov_b32 m0, s75
	s_nop 0
	global_load_lds_dwordx4 v167, s[8:9]
	s_waitcnt vmcnt(8)
	s_waitcnt lgkmcnt(0)
	s_add_u32 s8, s6, 0x80
	s_addc_u32 s9, s7, 0
	s_barrier
	s_setprio 1
	s_waitcnt lgkmcnt(0)
	v_mfma_f32_16x16x128_f8f6f4 v[158:161], v[10:17], v[180:187], v[158:161]
	v_mfma_f32_16x16x128_f8f6f4 v[154:157], v[2:9], v[180:187], v[154:157]
	v_mfma_f32_16x16x128_f8f6f4 v[150:153], v[26:33], v[180:187], v[150:153]
	v_mfma_f32_16x16x128_f8f6f4 v[146:149], v[18:25], v[180:187], v[146:149]
	v_mfma_f32_16x16x128_f8f6f4 v[122:125], v[18:25], v[188:195], v[122:125]
	v_mfma_f32_16x16x128_f8f6f4 v[102:105], v[26:33], v[188:195], v[102:105]
	v_mfma_f32_16x16x128_f8f6f4 v[114:117], v[2:9], v[188:195], v[114:117]
	v_mfma_f32_16x16x128_f8f6f4 v[110:113], v[10:17], v[188:195], v[110:113]
	v_mfma_f32_16x16x128_f8f6f4 v[134:137], v[10:17], v[202:209], v[134:137]
	v_mfma_f32_16x16x128_f8f6f4 v[138:141], v[2:9], v[202:209], v[138:141]
	v_mfma_f32_16x16x128_f8f6f4 v[130:133], v[26:33], v[202:209], v[130:133]
	v_mfma_f32_16x16x128_f8f6f4 v[142:145], v[18:25], v[202:209], v[142:145]
	v_mfma_f32_16x16x128_f8f6f4 v[98:101], v[18:25], v[210:217], v[98:101]
	v_mfma_f32_16x16x128_f8f6f4 v[106:109], v[26:33], v[210:217], v[106:109]
	v_mfma_f32_16x16x128_f8f6f4 v[118:121], v[2:9], v[210:217], v[118:121]
	v_mfma_f32_16x16x128_f8f6f4 v[126:129], v[10:17], v[210:217], v[126:129]
	s_setprio 0
	s_barrier
	s_mov_b64 s[80:81], s[6:7]
	v_mov_b32_e32 v167, v171
	s_mov_b32 m0, s76
	ds_read_b128 v[180:183], v164 offset:16384
	ds_read_b128 v[184:187], v164 offset:17408
	ds_read_b128 v[188:191], v164 offset:18432
	ds_read_b128 v[192:195], v164 offset:19456
	ds_read_b128 v[202:205], v164 offset:20480
	ds_read_b128 v[206:209], v164 offset:21504
	ds_read_b128 v[210:213], v164 offset:22528
	ds_read_b128 v[214:217], v164 offset:23552
	s_nop 0
	global_load_lds_dwordx4 v167, s[80:81]
	v_mov_b32_e32 v167, v173
	s_mov_b32 m0, s77
	s_nop 0
	global_load_lds_dwordx4 v167, s[80:81]
	s_add_u32 s80, s6, 0x40000
	s_addc_u32 s81, s7, 0
	v_mov_b32_e32 v167, v171
	s_mov_b32 m0, s78
	s_nop 0
	global_load_lds_dwordx4 v167, s[80:81]
	v_mov_b32_e32 v167, v173
	s_mov_b32 m0, s79
	s_nop 0
	global_load_lds_dwordx4 v167, s[80:81]
	s_waitcnt vmcnt(6)
	s_waitcnt lgkmcnt(0)
	s_barrier
	s_setprio 1
	s_waitcnt lgkmcnt(0)
	v_mfma_f32_16x16x128_f8f6f4 v[94:97], v[10:17], v[180:187], v[94:97]
	v_mfma_f32_16x16x128_f8f6f4 v[90:93], v[2:9], v[180:187], v[90:93]
	v_mfma_f32_16x16x128_f8f6f4 v[86:89], v[26:33], v[180:187], v[86:89]
	v_mfma_f32_16x16x128_f8f6f4 v[82:85], v[18:25], v[180:187], v[82:85]
	v_mfma_f32_16x16x128_f8f6f4 v[66:69], v[18:25], v[188:195], v[66:69]
	v_mfma_f32_16x16x128_f8f6f4 v[70:73], v[26:33], v[188:195], v[70:73]
	v_mfma_f32_16x16x128_f8f6f4 v[74:77], v[2:9], v[188:195], v[74:77]
	v_mfma_f32_16x16x128_f8f6f4 v[78:81], v[10:17], v[188:195], v[78:81]
	v_mfma_f32_16x16x128_f8f6f4 v[62:65], v[10:17], v[202:209], v[62:65]
	v_mfma_f32_16x16x128_f8f6f4 v[58:61], v[2:9], v[202:209], v[58:61]
	v_mfma_f32_16x16x128_f8f6f4 v[54:57], v[26:33], v[202:209], v[54:57]
	v_mfma_f32_16x16x128_f8f6f4 v[50:53], v[18:25], v[202:209], v[50:53]
	v_mfma_f32_16x16x128_f8f6f4 v[34:37], v[18:25], v[210:217], v[34:37]
	v_mfma_f32_16x16x128_f8f6f4 v[38:41], v[26:33], v[210:217], v[38:41]
	v_mfma_f32_16x16x128_f8f6f4 v[42:45], v[2:9], v[210:217], v[42:45]
	v_mfma_f32_16x16x128_f8f6f4 v[46:49], v[10:17], v[210:217], v[46:49]
	s_setprio 0
	s_barrier
	ds_read_b128 v[26:29], v165
	ds_read_b128 v[30:33], v165 offset:1024
	ds_read_b128 v[18:21], v165 offset:2048
	ds_read_b128 v[22:25], v165 offset:3072
	ds_read_b128 v[10:13], v166
	ds_read_b128 v[14:17], v166 offset:1024
	ds_read_b128 v[2:5], v166 offset:2048
	ds_read_b128 v[6:9], v166 offset:3072
	s_mov_b64 s[80:81], s[14:15]
	v_mov_b32_e32 v167, v170
	s_mov_b32 m0, s21
	ds_read_b128 v[180:183], v164 offset:32768
	ds_read_b128 v[184:187], v164 offset:33792
	ds_read_b128 v[188:191], v164 offset:34816
	ds_read_b128 v[192:195], v164 offset:35840
	ds_read_b128 v[202:205], v164 offset:36864
	ds_read_b128 v[206:209], v164 offset:37888
	ds_read_b128 v[210:213], v164 offset:38912
	ds_read_b128 v[214:217], v164 offset:39936
	s_add_u32 s14, s14, 0x40000
	global_load_lds_dwordx4 v167, s[80:81]
	v_mov_b32_e32 v167, v172
	s_mov_b32 m0, s60
	s_addc_u32 s15, s15, 0
	global_load_lds_dwordx4 v167, s[80:81]
	v_mov_b32_e32 v167, v170
	s_mov_b32 m0, s62
	s_nop 0
	global_load_lds_dwordx4 v167, s[14:15]
	v_mov_b32_e32 v167, v172
	s_mov_b32 m0, s63
	s_nop 0
	global_load_lds_dwordx4 v167, s[14:15]
	s_waitcnt vmcnt(8)
	s_waitcnt lgkmcnt(0)
	s_barrier
	s_setprio 1
	s_waitcnt lgkmcnt(0)
	v_mfma_f32_16x16x128_f8f6f4 v[158:161], v[26:33], v[180:187], v[158:161]
	v_mfma_f32_16x16x128_f8f6f4 v[154:157], v[18:25], v[180:187], v[154:157]
	v_mfma_f32_16x16x128_f8f6f4 v[150:153], v[10:17], v[180:187], v[150:153]
	v_mfma_f32_16x16x128_f8f6f4 v[146:149], v[2:9], v[180:187], v[146:149]
	v_mfma_f32_16x16x128_f8f6f4 v[122:125], v[2:9], v[188:195], v[122:125]
	v_mfma_f32_16x16x128_f8f6f4 v[102:105], v[10:17], v[188:195], v[102:105]
	v_mfma_f32_16x16x128_f8f6f4 v[114:117], v[18:25], v[188:195], v[114:117]
	v_mfma_f32_16x16x128_f8f6f4 v[110:113], v[26:33], v[188:195], v[110:113]
	v_mfma_f32_16x16x128_f8f6f4 v[134:137], v[26:33], v[202:209], v[134:137]
	v_mfma_f32_16x16x128_f8f6f4 v[138:141], v[18:25], v[202:209], v[138:141]
	v_mfma_f32_16x16x128_f8f6f4 v[130:133], v[10:17], v[202:209], v[130:133]
	v_mfma_f32_16x16x128_f8f6f4 v[142:145], v[2:9], v[202:209], v[142:145]
	v_mfma_f32_16x16x128_f8f6f4 v[98:101], v[2:9], v[210:217], v[98:101]
	v_mfma_f32_16x16x128_f8f6f4 v[106:109], v[10:17], v[210:217], v[106:109]
	v_mfma_f32_16x16x128_f8f6f4 v[118:121], v[18:25], v[210:217], v[118:121]
	v_mfma_f32_16x16x128_f8f6f4 v[126:129], v[26:33], v[210:217], v[126:129]
	s_setprio 0
	s_barrier
	v_mov_b32_e32 v167, v171
	s_mov_b32 m0, s67
	ds_read_b128 v[180:183], v164 offset:49152
	ds_read_b128 v[184:187], v164 offset:50176
	ds_read_b128 v[188:191], v164 offset:51200
	ds_read_b128 v[192:195], v164 offset:52224
	ds_read_b128 v[202:205], v164 offset:53248
	ds_read_b128 v[206:209], v164 offset:54272
	ds_read_b128 v[210:213], v164 offset:55296
	ds_read_b128 v[214:217], v164 offset:56320
	s_add_u32 s6, s6, 0x40080
	global_load_lds_dwordx4 v167, s[8:9]
	v_mov_b32_e32 v167, v173
	s_mov_b32 m0, s69
	s_addc_u32 s7, s7, 0
	global_load_lds_dwordx4 v167, s[8:9]
	v_mov_b32_e32 v167, v171
	s_mov_b32 m0, s70
	s_nop 0
	global_load_lds_dwordx4 v167, s[6:7]
	v_mov_b32_e32 v167, v173
	s_mov_b32 m0, s71
	s_nop 0
	global_load_lds_dwordx4 v167, s[6:7]
	s_waitcnt vmcnt(6)
	s_waitcnt lgkmcnt(0)
	s_barrier
	s_setprio 1
	s_waitcnt lgkmcnt(0)
	v_mfma_f32_16x16x128_f8f6f4 v[94:97], v[26:33], v[180:187], v[94:97]
	v_mfma_f32_16x16x128_f8f6f4 v[90:93], v[18:25], v[180:187], v[90:93]
	v_mfma_f32_16x16x128_f8f6f4 v[86:89], v[10:17], v[180:187], v[86:89]
	v_mfma_f32_16x16x128_f8f6f4 v[82:85], v[2:9], v[180:187], v[82:85]
	v_mfma_f32_16x16x128_f8f6f4 v[66:69], v[2:9], v[188:195], v[66:69]
	v_mfma_f32_16x16x128_f8f6f4 v[70:73], v[10:17], v[188:195], v[70:73]
	v_mfma_f32_16x16x128_f8f6f4 v[74:77], v[18:25], v[188:195], v[74:77]
	v_mfma_f32_16x16x128_f8f6f4 v[78:81], v[26:33], v[188:195], v[78:81]
	v_mfma_f32_16x16x128_f8f6f4 v[62:65], v[26:33], v[202:209], v[62:65]
	v_mfma_f32_16x16x128_f8f6f4 v[58:61], v[18:25], v[202:209], v[58:61]
	v_mfma_f32_16x16x128_f8f6f4 v[54:57], v[10:17], v[202:209], v[54:57]
	v_mfma_f32_16x16x128_f8f6f4 v[50:53], v[2:9], v[202:209], v[50:53]
	v_mfma_f32_16x16x128_f8f6f4 v[34:37], v[2:9], v[210:217], v[34:37]
	v_mfma_f32_16x16x128_f8f6f4 v[38:41], v[10:17], v[210:217], v[38:41]
	v_mfma_f32_16x16x128_f8f6f4 v[42:45], v[18:25], v[210:217], v[42:45]
	v_mfma_f32_16x16x128_f8f6f4 v[46:49], v[26:33], v[210:217], v[46:49]
	s_setprio 0
	s_barrier
	s_add_i32 s66, s66, 2
	s_add_u32 s2, s2, 0x100
	s_addc_u32 s3, s3, 0
	s_cmp_gt_u32 s66, 13
	s_mov_b64 s[8:9], s[4:5]
	s_cbranch_scc0 .LBB0_694
	s_cmpk_lt_u32 s33, 0x100
	s_cbranch_scc0 .LBB0_697
	s_barrier

.LBB0_740:
	s_add_i32 s66, s18, s70
	v_mov_b32_e32 v2, v171
	s_waitcnt vmcnt(2)
	s_barrier
	s_mov_b32 m0, s66
	s_add_i32 s67, s66, 0x2000
	global_load_lds_dwordx4 v2, s[48:49]
	v_mov_b32_e32 v2, v173
	s_mov_b32 m0, s67
	s_and_b32 s20, s35, 3
	global_load_lds_dwordx4 v2, s[48:49]
	s_add_i32 s48, s19, s70
	v_mov_b32_e32 v2, v171
	s_mov_b32 m0, s48
	s_add_i32 s49, s48, 0x2000
	global_load_lds_dwordx4 v2, s[50:51]
	v_mov_b32_e32 v2, v173
	s_mov_b32 m0, s49
	v_lshl_or_b32 v179, s14, 6, v175
	global_load_lds_dwordx4 v2, s[50:51]
	v_lshlrev_b32_e32 v2, 2, v175
	s_lshl_b32 s14, s14, 13
	v_and_b32_e32 v2, 32, v2
	v_lshl_or_b32 v3, s20, 12, v177
	v_bitop3_b32 v2, v176, s14, v2 bitop3:0xde
	v_add_u32_e32 v162, s17, v3
	s_waitcnt vmcnt(6)
	s_barrier
	v_add_u32_e32 v163, s16, v3
	v_add_u32_e32 v164, 0, v2
	v_add_u32_e32 v165, s18, v3
	v_add_u32_e32 v166, s19, v3
	ds_read_b128 v[2:5], v162
	ds_read_b128 v[6:9], v162 offset:1024
	ds_read_b128 v[10:13], v162 offset:2048
	ds_read_b128 v[14:17], v162 offset:3072
	ds_read_b128 v[18:21], v163
	ds_read_b128 v[22:25], v163 offset:1024
	ds_read_b128 v[26:29], v163 offset:2048
	ds_read_b128 v[30:33], v163 offset:3072
	s_add_u32 s14, s0, 0x100
	s_addc_u32 s15, s1, 0
	s_add_u32 s40, s0, 0x80
	s_addc_u32 s41, s1, 0
	v_mov_b32_e32 v66, v170
	s_add_i32 s18, s61, 0x8000
	ds_read_b128 v[34:37], v164
	ds_read_b128 v[38:41], v164 offset:1024
	ds_read_b128 v[42:45], v164 offset:2048
	ds_read_b128 v[46:49], v164 offset:3072
	ds_read_b128 v[50:53], v164 offset:4096
	ds_read_b128 v[54:57], v164 offset:5120
	ds_read_b128 v[58:61], v164 offset:6144
	ds_read_b128 v[62:65], v164 offset:7168
	s_mov_b32 m0, s18
	s_add_i32 s19, s61, 0xa000
	global_load_lds_dwordx4 v66, s[40:41]
	v_mov_b32_e32 v66, v172
	s_mov_b32 m0, s19
	s_nop 0
	global_load_lds_dwordx4 v66, s[40:41]
	s_add_u32 s40, s0, 0x40080
	s_addc_u32 s41, s1, 0
	v_mov_b32_e32 v66, v170
	s_add_i32 s50, s61, 0xc000
	s_mov_b32 m0, s50
	s_add_i32 s51, s61, 0xe000
	global_load_lds_dwordx4 v66, s[40:41]
	v_mov_b32_e32 v66, v172
	s_mov_b32 m0, s51
	s_nop 0
	global_load_lds_dwordx4 v66, s[40:41]
	s_waitcnt vmcnt(8)
	s_waitcnt lgkmcnt(0)
	s_barrier
	s_setprio 1
	s_waitcnt lgkmcnt(0)
	v_mfma_f32_16x16x128_f8f6f4 v[158:161], v[2:9], v[34:41], 0
	v_mfma_f32_16x16x128_f8f6f4 v[154:157], v[10:17], v[34:41], 0
	v_mfma_f32_16x16x128_f8f6f4 v[150:153], v[18:25], v[34:41], 0
	v_mfma_f32_16x16x128_f8f6f4 v[146:149], v[26:33], v[34:41], 0
	v_mfma_f32_16x16x128_f8f6f4 v[118:121], v[26:33], v[42:49], 0
	v_mfma_f32_16x16x128_f8f6f4 v[102:105], v[18:25], v[42:49], 0
	v_mfma_f32_16x16x128_f8f6f4 v[110:113], v[10:17], v[42:49], 0
	v_mfma_f32_16x16x128_f8f6f4 v[106:109], v[2:9], v[42:49], 0
	v_mfma_f32_16x16x128_f8f6f4 v[134:137], v[2:9], v[50:57], 0
	v_mfma_f32_16x16x128_f8f6f4 v[138:141], v[10:17], v[50:57], 0
	v_mfma_f32_16x16x128_f8f6f4 v[126:129], v[18:25], v[50:57], 0
	v_mfma_f32_16x16x128_f8f6f4 v[142:145], v[26:33], v[50:57], 0
	v_mfma_f32_16x16x128_f8f6f4 v[98:101], v[26:33], v[58:65], 0
	v_mfma_f32_16x16x128_f8f6f4 v[114:117], v[18:25], v[58:65], 0
	v_mfma_f32_16x16x128_f8f6f4 v[122:125], v[10:17], v[58:65], 0
	v_mfma_f32_16x16x128_f8f6f4 v[130:133], v[2:9], v[58:65], 0
	s_setprio 0
	s_barrier
	v_mov_b32_e32 v50, v171
	s_add_i32 s17, s17, s70
	ds_read_b128 v[34:37], v164 offset:16384
	ds_read_b128 v[38:41], v164 offset:17408
	ds_read_b128 v[42:45], v164 offset:18432
	ds_read_b128 v[46:49], v164 offset:19456
	ds_read_b128 v[180:183], v164 offset:20480
	ds_read_b128 v[184:187], v164 offset:21504
	ds_read_b128 v[188:191], v164 offset:22528
	ds_read_b128 v[192:195], v164 offset:23552
	s_mov_b32 m0, s17
	s_add_i32 s69, s17, 0x2000
	global_load_lds_dwordx4 v50, s[44:45]
	v_mov_b32_e32 v50, v173
	s_mov_b32 m0, s69
	s_add_i32 s16, s16, s70
	global_load_lds_dwordx4 v50, s[44:45]
	v_mov_b32_e32 v50, v171
	s_mov_b32 m0, s16
	s_add_i32 s70, s16, 0x2000
	global_load_lds_dwordx4 v50, s[52:53]
	v_mov_b32_e32 v50, v173
	s_mov_b32 m0, s70
	s_nop 0
	global_load_lds_dwordx4 v50, s[52:53]
	s_waitcnt vmcnt(6)
	s_waitcnt lgkmcnt(0)
	s_barrier
	s_setprio 1
	s_waitcnt lgkmcnt(0)
	v_mfma_f32_16x16x128_f8f6f4 v[94:97], v[2:9], v[34:41], 0
	v_mfma_f32_16x16x128_f8f6f4 v[90:93], v[10:17], v[34:41], 0
	v_mfma_f32_16x16x128_f8f6f4 v[86:89], v[18:25], v[34:41], 0
	v_mfma_f32_16x16x128_f8f6f4 v[82:85], v[26:33], v[34:41], 0
	v_mfma_f32_16x16x128_f8f6f4 v[66:69], v[26:33], v[42:49], 0
	v_mfma_f32_16x16x128_f8f6f4 v[70:73], v[18:25], v[42:49], 0
	v_mfma_f32_16x16x128_f8f6f4 v[74:77], v[10:17], v[42:49], 0
	v_mfma_f32_16x16x128_f8f6f4 v[78:81], v[2:9], v[42:49], 0
	v_mfma_f32_16x16x128_f8f6f4 v[62:65], v[2:9], v[180:187], 0
	v_mfma_f32_16x16x128_f8f6f4 v[58:61], v[10:17], v[180:187], 0
	v_mfma_f32_16x16x128_f8f6f4 v[54:57], v[18:25], v[180:187], 0
	v_mfma_f32_16x16x128_f8f6f4 v[50:53], v[26:33], v[180:187], 0
	v_mfma_f32_16x16x128_f8f6f4 v[34:37], v[26:33], v[188:195], 0
	v_mfma_f32_16x16x128_f8f6f4 v[38:41], v[18:25], v[188:195], 0
	v_mfma_f32_16x16x128_f8f6f4 v[42:45], v[10:17], v[188:195], 0
	v_mfma_f32_16x16x128_f8f6f4 v[46:49], v[2:9], v[188:195], 0
	s_setprio 0
	s_barrier
	ds_read_b128 v[26:29], v165
	ds_read_b128 v[30:33], v165 offset:1024
	ds_read_b128 v[18:21], v165 offset:2048
	ds_read_b128 v[22:25], v165 offset:3072
	ds_read_b128 v[10:13], v166
	ds_read_b128 v[14:17], v166 offset:1024
	ds_read_b128 v[2:5], v166 offset:2048
	ds_read_b128 v[6:9], v166 offset:3072
	v_mov_b32_e32 v167, v170
	s_mov_b32 m0, s61
	ds_read_b128 v[180:183], v164 offset:32768
	ds_read_b128 v[184:187], v164 offset:33792
	ds_read_b128 v[188:191], v164 offset:34816
	ds_read_b128 v[192:195], v164 offset:35840
	ds_read_b128 v[202:205], v164 offset:36864
	ds_read_b128 v[206:209], v164 offset:37888
	ds_read_b128 v[210:213], v164 offset:38912
	ds_read_b128 v[214:217], v164 offset:39936
	s_nop 0
	global_load_lds_dwordx4 v167, s[14:15]
	v_mov_b32_e32 v167, v172
	s_mov_b32 m0, s46
	s_nop 0
	global_load_lds_dwordx4 v167, s[14:15]
	s_add_u32 s14, s0, 0x40100
	s_addc_u32 s15, s1, 0
	v_mov_b32_e32 v167, v170
	s_mov_b32 m0, s47
	s_nop 0
	global_load_lds_dwordx4 v167, s[14:15]
	v_mov_b32_e32 v167, v172
	s_mov_b32 m0, s62
	s_nop 0
	global_load_lds_dwordx4 v167, s[14:15]
	s_waitcnt vmcnt(8)
	s_waitcnt lgkmcnt(0)
	s_barrier
	s_setprio 1
	s_waitcnt lgkmcnt(0)
	v_mfma_f32_16x16x128_f8f6f4 v[158:161], v[26:33], v[180:187], v[158:161]
	v_mfma_f32_16x16x128_f8f6f4 v[154:157], v[18:25], v[180:187], v[154:157]
	v_mfma_f32_16x16x128_f8f6f4 v[150:153], v[10:17], v[180:187], v[150:153]
	v_mfma_f32_16x16x128_f8f6f4 v[146:149], v[2:9], v[180:187], v[146:149]
	v_mfma_f32_16x16x128_f8f6f4 v[118:121], v[2:9], v[188:195], v[118:121]
	v_mfma_f32_16x16x128_f8f6f4 v[102:105], v[10:17], v[188:195], v[102:105]
	v_mfma_f32_16x16x128_f8f6f4 v[110:113], v[18:25], v[188:195], v[110:113]
	v_mfma_f32_16x16x128_f8f6f4 v[106:109], v[26:33], v[188:195], v[106:109]
	v_mfma_f32_16x16x128_f8f6f4 v[134:137], v[26:33], v[202:209], v[134:137]
	v_mfma_f32_16x16x128_f8f6f4 v[138:141], v[18:25], v[202:209], v[138:141]
	v_mfma_f32_16x16x128_f8f6f4 v[126:129], v[10:17], v[202:209], v[126:129]
	v_mfma_f32_16x16x128_f8f6f4 v[142:145], v[2:9], v[202:209], v[142:145]
	v_mfma_f32_16x16x128_f8f6f4 v[98:101], v[2:9], v[210:217], v[98:101]
	v_mfma_f32_16x16x128_f8f6f4 v[114:117], v[10:17], v[210:217], v[114:117]
	v_mfma_f32_16x16x128_f8f6f4 v[122:125], v[18:25], v[210:217], v[122:125]
	v_mfma_f32_16x16x128_f8f6f4 v[130:133], v[26:33], v[210:217], v[130:133]
	s_setprio 0
	s_barrier
	v_mov_b32_e32 v167, v171
	s_mov_b32 m0, s66
	ds_read_b128 v[180:183], v164 offset:49152
	ds_read_b128 v[184:187], v164 offset:50176
	ds_read_b128 v[188:191], v164 offset:51200
	ds_read_b128 v[192:195], v164 offset:52224
	ds_read_b128 v[202:205], v164 offset:53248
	ds_read_b128 v[206:209], v164 offset:54272
	ds_read_b128 v[210:213], v164 offset:55296
	ds_read_b128 v[214:217], v164 offset:56320
	s_nop 0
	global_load_lds_dwordx4 v167, s[42:43]
	v_mov_b32_e32 v167, v173
	s_mov_b32 m0, s67
	s_nop 0
	global_load_lds_dwordx4 v167, s[42:43]
	v_mov_b32_e32 v167, v171
	s_mov_b32 m0, s48
	s_nop 0
	global_load_lds_dwordx4 v167, s[64:65]
	v_mov_b32_e32 v167, v173
	s_mov_b32 m0, s49
	s_nop 0
	global_load_lds_dwordx4 v167, s[64:65]
	s_waitcnt vmcnt(6)
	s_waitcnt lgkmcnt(0)
	s_barrier
	s_setprio 1
	s_waitcnt lgkmcnt(0)
	v_mfma_f32_16x16x128_f8f6f4 v[94:97], v[26:33], v[180:187], v[94:97]
	v_mfma_f32_16x16x128_f8f6f4 v[90:93], v[18:25], v[180:187], v[90:93]
	v_mfma_f32_16x16x128_f8f6f4 v[86:89], v[10:17], v[180:187], v[86:89]
	v_mfma_f32_16x16x128_f8f6f4 v[82:85], v[2:9], v[180:187], v[82:85]
	v_mfma_f32_16x16x128_f8f6f4 v[66:69], v[2:9], v[188:195], v[66:69]
	v_mfma_f32_16x16x128_f8f6f4 v[70:73], v[10:17], v[188:195], v[70:73]
	v_mfma_f32_16x16x128_f8f6f4 v[74:77], v[18:25], v[188:195], v[74:77]
	v_mfma_f32_16x16x128_f8f6f4 v[78:81], v[26:33], v[188:195], v[78:81]
	v_mfma_f32_16x16x128_f8f6f4 v[62:65], v[26:33], v[202:209], v[62:65]
	v_mfma_f32_16x16x128_f8f6f4 v[58:61], v[18:25], v[202:209], v[58:61]
	v_mfma_f32_16x16x128_f8f6f4 v[54:57], v[10:17], v[202:209], v[54:57]
	v_mfma_f32_16x16x128_f8f6f4 v[50:53], v[2:9], v[202:209], v[50:53]
	v_mfma_f32_16x16x128_f8f6f4 v[34:37], v[2:9], v[210:217], v[34:37]
	v_mfma_f32_16x16x128_f8f6f4 v[38:41], v[10:17], v[210:217], v[38:41]
	v_mfma_f32_16x16x128_f8f6f4 v[42:45], v[18:25], v[210:217], v[42:45]
	v_mfma_f32_16x16x128_f8f6f4 v[46:49], v[26:33], v[210:217], v[46:49]
	s_setprio 0
	s_barrier
	s_add_i32 s10, s10, s11
	s_lshl_b32 s10, s10, 19
	s_add_i32 s10, s10, 0x200000
	s_add_u32 s10, s56, s10
	s_addc_u32 s11, s57, 0
	s_add_u32 s42, s10, 0x3ab00100
	s_addc_u32 s43, s11, 0
.LBB0_741:
	ds_read_b128 v[10:13], v162
	ds_read_b128 v[14:17], v162 offset:1024
	ds_read_b128 v[2:5], v162 offset:2048
	ds_read_b128 v[6:9], v162 offset:3072
	ds_read_b128 v[26:29], v163
	ds_read_b128 v[30:33], v163 offset:1024
	ds_read_b128 v[18:21], v163 offset:2048
	ds_read_b128 v[22:25], v163 offset:3072
	s_add_u32 s14, s42, 0x100
	s_addc_u32 s15, s43, 0
	s_cmp_eq_u32 s63, 12
	s_cselect_b32 s41, s29, s31
	s_cselect_b32 s40, s28, s30
	s_cselect_b32 s45, s1, s15
	s_cselect_b32 s44, s0, s14
	s_add_u32 s10, s42, 0x80
	s_addc_u32 s11, s43, 0
	v_mov_b32_e32 v167, v170
	s_mov_b32 m0, s18
	ds_read_b128 v[180:183], v164
	ds_read_b128 v[184:187], v164 offset:1024
	ds_read_b128 v[188:191], v164 offset:2048
	ds_read_b128 v[192:195], v164 offset:3072
	ds_read_b128 v[202:205], v164 offset:4096
	ds_read_b128 v[206:209], v164 offset:5120
	ds_read_b128 v[210:213], v164 offset:6144
	ds_read_b128 v[214:217], v164 offset:7168
	s_nop 0
	global_load_lds_dwordx4 v167, s[10:11]
	v_mov_b32_e32 v167, v172
	s_mov_b32 m0, s19
	s_nop 0
	global_load_lds_dwordx4 v167, s[10:11]
	s_add_u32 s10, s42, 0x40080
	s_addc_u32 s11, s43, 0
	v_mov_b32_e32 v167, v170
	s_mov_b32 m0, s50
	s_add_u32 s42, s40, 0x80
	global_load_lds_dwordx4 v167, s[10:11]
	v_mov_b32_e32 v167, v172
	s_mov_b32 m0, s51
	s_addc_u32 s43, s41, 0
	global_load_lds_dwordx4 v167, s[10:11]
	s_waitcnt vmcnt(8)
	s_waitcnt lgkmcnt(0)
	s_barrier
	s_setprio 1
	s_waitcnt lgkmcnt(0)
	v_mfma_f32_16x16x128_f8f6f4 v[158:161], v[10:17], v[180:187], v[158:161]
	v_mfma_f32_16x16x128_f8f6f4 v[154:157], v[2:9], v[180:187], v[154:157]
	v_mfma_f32_16x16x128_f8f6f4 v[150:153], v[26:33], v[180:187], v[150:153]
	v_mfma_f32_16x16x128_f8f6f4 v[146:149], v[18:25], v[180:187], v[146:149]
	v_mfma_f32_16x16x128_f8f6f4 v[118:121], v[18:25], v[188:195], v[118:121]
	v_mfma_f32_16x16x128_f8f6f4 v[102:105], v[26:33], v[188:195], v[102:105]
	v_mfma_f32_16x16x128_f8f6f4 v[110:113], v[2:9], v[188:195], v[110:113]
	v_mfma_f32_16x16x128_f8f6f4 v[106:109], v[10:17], v[188:195], v[106:109]
	v_mfma_f32_16x16x128_f8f6f4 v[134:137], v[10:17], v[202:209], v[134:137]
	v_mfma_f32_16x16x128_f8f6f4 v[138:141], v[2:9], v[202:209], v[138:141]
	v_mfma_f32_16x16x128_f8f6f4 v[126:129], v[26:33], v[202:209], v[126:129]
	v_mfma_f32_16x16x128_f8f6f4 v[142:145], v[18:25], v[202:209], v[142:145]
	v_mfma_f32_16x16x128_f8f6f4 v[98:101], v[18:25], v[210:217], v[98:101]
	v_mfma_f32_16x16x128_f8f6f4 v[114:117], v[26:33], v[210:217], v[114:117]
	v_mfma_f32_16x16x128_f8f6f4 v[122:125], v[2:9], v[210:217], v[122:125]
	v_mfma_f32_16x16x128_f8f6f4 v[130:133], v[10:17], v[210:217], v[130:133]
	s_setprio 0
	s_barrier
	s_mov_b64 s[10:11], s[40:41]
	v_mov_b32_e32 v167, v171
	s_mov_b32 m0, s17
	ds_read_b128 v[180:183], v164 offset:16384
	ds_read_b128 v[184:187], v164 offset:17408
	ds_read_b128 v[188:191], v164 offset:18432
	ds_read_b128 v[192:195], v164 offset:19456
	ds_read_b128 v[202:205], v164 offset:20480
	ds_read_b128 v[206:209], v164 offset:21504
	ds_read_b128 v[210:213], v164 offset:22528
	ds_read_b128 v[214:217], v164 offset:23552
	s_nop 0
	global_load_lds_dwordx4 v167, s[10:11]
	v_mov_b32_e32 v167, v173
	s_mov_b32 m0, s69
	s_nop 0
	global_load_lds_dwordx4 v167, s[10:11]
	s_add_u32 s10, s40, 0x40000
	s_addc_u32 s11, s41, 0
	v_mov_b32_e32 v167, v171
	s_mov_b32 m0, s16
	s_nop 0
	global_load_lds_dwordx4 v167, s[10:11]
	v_mov_b32_e32 v167, v173
	s_mov_b32 m0, s70
	s_nop 0
	global_load_lds_dwordx4 v167, s[10:11]
	s_waitcnt vmcnt(6)
	s_waitcnt lgkmcnt(0)
	s_barrier
	s_setprio 1
	s_waitcnt lgkmcnt(0)
	v_mfma_f32_16x16x128_f8f6f4 v[94:97], v[10:17], v[180:187], v[94:97]
	v_mfma_f32_16x16x128_f8f6f4 v[90:93], v[2:9], v[180:187], v[90:93]
	v_mfma_f32_16x16x128_f8f6f4 v[86:89], v[26:33], v[180:187], v[86:89]
	v_mfma_f32_16x16x128_f8f6f4 v[82:85], v[18:25], v[180:187], v[82:85]
	v_mfma_f32_16x16x128_f8f6f4 v[66:69], v[18:25], v[188:195], v[66:69]
	v_mfma_f32_16x16x128_f8f6f4 v[70:73], v[26:33], v[188:195], v[70:73]
	v_mfma_f32_16x16x128_f8f6f4 v[74:77], v[2:9], v[188:195], v[74:77]
	v_mfma_f32_16x16x128_f8f6f4 v[78:81], v[10:17], v[188:195], v[78:81]
	v_mfma_f32_16x16x128_f8f6f4 v[62:65], v[10:17], v[202:209], v[62:65]
	v_mfma_f32_16x16x128_f8f6f4 v[58:61], v[2:9], v[202:209], v[58:61]
	v_mfma_f32_16x16x128_f8f6f4 v[54:57], v[26:33], v[202:209], v[54:57]
	v_mfma_f32_16x16x128_f8f6f4 v[50:53], v[18:25], v[202:209], v[50:53]
	v_mfma_f32_16x16x128_f8f6f4 v[34:37], v[18:25], v[210:217], v[34:37]
	v_mfma_f32_16x16x128_f8f6f4 v[38:41], v[26:33], v[210:217], v[38:41]
	v_mfma_f32_16x16x128_f8f6f4 v[42:45], v[2:9], v[210:217], v[42:45]
	v_mfma_f32_16x16x128_f8f6f4 v[46:49], v[10:17], v[210:217], v[46:49]
	s_setprio 0
	s_barrier
	ds_read_b128 v[26:29], v165
	ds_read_b128 v[30:33], v165 offset:1024
	ds_read_b128 v[18:21], v165 offset:2048
	ds_read_b128 v[22:25], v165 offset:3072
	ds_read_b128 v[10:13], v166
	ds_read_b128 v[14:17], v166 offset:1024
	ds_read_b128 v[2:5], v166 offset:2048
	ds_read_b128 v[6:9], v166 offset:3072
	s_mov_b64 s[10:11], s[44:45]
	v_mov_b32_e32 v167, v170
	s_mov_b32 m0, s61
	ds_read_b128 v[180:183], v164 offset:32768
	ds_read_b128 v[184:187], v164 offset:33792
	ds_read_b128 v[188:191], v164 offset:34816
	ds_read_b128 v[192:195], v164 offset:35840
	ds_read_b128 v[202:205], v164 offset:36864
	ds_read_b128 v[206:209], v164 offset:37888
	ds_read_b128 v[210:213], v164 offset:38912
	ds_read_b128 v[214:217], v164 offset:39936
	s_nop 0
	global_load_lds_dwordx4 v167, s[10:11]
	v_mov_b32_e32 v167, v172
	s_mov_b32 m0, s46
	s_nop 0
	global_load_lds_dwordx4 v167, s[10:11]
	s_add_u32 s10, s44, 0x40000
	s_addc_u32 s11, s45, 0
	v_mov_b32_e32 v167, v170
	s_mov_b32 m0, s47
	s_nop 0
	global_load_lds_dwordx4 v167, s[10:11]
	v_mov_b32_e32 v167, v172
	s_mov_b32 m0, s62
	s_nop 0
	global_load_lds_dwordx4 v167, s[10:11]
	s_waitcnt vmcnt(8)
	s_waitcnt lgkmcnt(0)
	s_barrier
	s_setprio 1
	s_waitcnt lgkmcnt(0)
	v_mfma_f32_16x16x128_f8f6f4 v[158:161], v[26:33], v[180:187], v[158:161]
	v_mfma_f32_16x16x128_f8f6f4 v[154:157], v[18:25], v[180:187], v[154:157]
	v_mfma_f32_16x16x128_f8f6f4 v[150:153], v[10:17], v[180:187], v[150:153]
	v_mfma_f32_16x16x128_f8f6f4 v[146:149], v[2:9], v[180:187], v[146:149]
	v_mfma_f32_16x16x128_f8f6f4 v[118:121], v[2:9], v[188:195], v[118:121]
	v_mfma_f32_16x16x128_f8f6f4 v[102:105], v[10:17], v[188:195], v[102:105]
	v_mfma_f32_16x16x128_f8f6f4 v[110:113], v[18:25], v[188:195], v[110:113]
	v_mfma_f32_16x16x128_f8f6f4 v[106:109], v[26:33], v[188:195], v[106:109]
	v_mfma_f32_16x16x128_f8f6f4 v[134:137], v[26:33], v[202:209], v[134:137]
	v_mfma_f32_16x16x128_f8f6f4 v[138:141], v[18:25], v[202:209], v[138:141]
	v_mfma_f32_16x16x128_f8f6f4 v[126:129], v[10:17], v[202:209], v[126:129]
	v_mfma_f32_16x16x128_f8f6f4 v[142:145], v[2:9], v[202:209], v[142:145]
	v_mfma_f32_16x16x128_f8f6f4 v[98:101], v[2:9], v[210:217], v[98:101]
	v_mfma_f32_16x16x128_f8f6f4 v[114:117], v[10:17], v[210:217], v[114:117]
	v_mfma_f32_16x16x128_f8f6f4 v[122:125], v[18:25], v[210:217], v[122:125]
	v_mfma_f32_16x16x128_f8f6f4 v[130:133], v[26:33], v[210:217], v[130:133]
	s_setprio 0
	s_barrier
	v_mov_b32_e32 v167, v171
	s_mov_b32 m0, s66
	ds_read_b128 v[180:183], v164 offset:49152
	ds_read_b128 v[184:187], v164 offset:50176
	ds_read_b128 v[188:191], v164 offset:51200
	ds_read_b128 v[192:195], v164 offset:52224
	ds_read_b128 v[202:205], v164 offset:53248
	ds_read_b128 v[206:209], v164 offset:54272
	ds_read_b128 v[210:213], v164 offset:55296
	ds_read_b128 v[214:217], v164 offset:56320
	s_add_u32 s10, s40, 0x40080
	global_load_lds_dwordx4 v167, s[42:43]
	v_mov_b32_e32 v167, v173
	s_mov_b32 m0, s67
	s_addc_u32 s11, s41, 0
	global_load_lds_dwordx4 v167, s[42:43]
	v_mov_b32_e32 v167, v171
	s_mov_b32 m0, s48
	s_nop 0
	global_load_lds_dwordx4 v167, s[10:11]
	v_mov_b32_e32 v167, v173
	s_mov_b32 m0, s49
	s_nop 0
	global_load_lds_dwordx4 v167, s[10:11]
	s_waitcnt vmcnt(6)
	s_waitcnt lgkmcnt(0)
	s_barrier
	s_setprio 1
	s_waitcnt lgkmcnt(0)
	v_mfma_f32_16x16x128_f8f6f4 v[94:97], v[26:33], v[180:187], v[94:97]
	v_mfma_f32_16x16x128_f8f6f4 v[90:93], v[18:25], v[180:187], v[90:93]
	v_mfma_f32_16x16x128_f8f6f4 v[86:89], v[10:17], v[180:187], v[86:89]
	v_mfma_f32_16x16x128_f8f6f4 v[82:85], v[2:9], v[180:187], v[82:85]
	v_mfma_f32_16x16x128_f8f6f4 v[66:69], v[2:9], v[188:195], v[66:69]
	v_mfma_f32_16x16x128_f8f6f4 v[70:73], v[10:17], v[188:195], v[70:73]
	v_mfma_f32_16x16x128_f8f6f4 v[74:77], v[18:25], v[188:195], v[74:77]
	v_mfma_f32_16x16x128_f8f6f4 v[78:81], v[26:33], v[188:195], v[78:81]
	v_mfma_f32_16x16x128_f8f6f4 v[62:65], v[26:33], v[202:209], v[62:65]
	v_mfma_f32_16x16x128_f8f6f4 v[58:61], v[18:25], v[202:209], v[58:61]
	v_mfma_f32_16x16x128_f8f6f4 v[54:57], v[10:17], v[202:209], v[54:57]
	v_mfma_f32_16x16x128_f8f6f4 v[50:53], v[2:9], v[202:209], v[50:53]
	v_mfma_f32_16x16x128_f8f6f4 v[34:37], v[2:9], v[210:217], v[34:37]
	v_mfma_f32_16x16x128_f8f6f4 v[38:41], v[10:17], v[210:217], v[38:41]
	v_mfma_f32_16x16x128_f8f6f4 v[42:45], v[18:25], v[210:217], v[42:45]
	v_mfma_f32_16x16x128_f8f6f4 v[46:49], v[26:33], v[210:217], v[46:49]
	s_setprio 0
	s_barrier
	s_add_i32 s63, s63, 2
	s_add_u32 s30, s30, 0x100
	s_addc_u32 s31, s31, 0
	s_cmp_gt_u32 s63, 13
	s_mov_b64 s[42:43], s[14:15]
	s_cbranch_scc0 .LBB0_741
	s_cmpk_lt_u32 s33, 0x100
	s_cbranch_scc0 .LBB0_744
	s_barrier

.LBB0_930:
	s_and_b32 s64, s63, 3
	s_lshl_b32 s3, s2, 13
	s_lshl_b32 s7, s64, 12
	s_add_u32 s46, s28, 0x4000
	s_addc_u32 s47, s29, 0
	s_add_i32 s33, 0, 0x18000
	s_mov_b64 s[8:9], s[46:47]
	s_add_i32 s67, s33, s6
	v_mov_b32_e32 v2, v170
	s_waitcnt vmcnt(2)
	s_barrier
	s_mov_b32 m0, s67
	s_add_i32 s69, s67, 0x2000
	global_load_lds_dwordx4 v2, s[8:9]
	v_mov_b32_e32 v2, v171
	s_add_u32 s48, s28, 0xb4000
	s_mov_b32 m0, s69
	s_addc_u32 s49, s29, 0
	s_add_i32 s60, 0, 0x1c000
	global_load_lds_dwordx4 v2, s[8:9]
	s_mov_b64 s[8:9], s[48:49]
	s_add_i32 s70, s60, s6
	v_mov_b32_e32 v2, v170
	s_mov_b32 m0, s70
	s_add_i32 s71, s70, 0x2000
	global_load_lds_dwordx4 v2, s[8:9]
	v_mov_b32_e32 v2, v171
	s_mov_b32 m0, s71
	v_lshlrev_b32_e32 v5, 6, v0
	global_load_lds_dwordx4 v2, s[8:9]
	v_and_b32_e32 v2, 48, v0
	v_and_b32_e32 v5, 0x3c0, v5
	v_and_b32_e32 v172, 15, v0
	v_and_b32_e32 v3, 32, v200
	s_waitcnt vmcnt(0)
	v_or_b32_e32 v6, v5, v2
	v_lshl_or_b32 v173, v172, 6, v2
	v_bitop3_b32 v174, v5, v3, v2 bitop3:0x36
	v_bitop3_b32 v2, s7, v6, v3 bitop3:0xf6
	s_add_i32 s21, 0, 0x10000
	v_bitop3_b32 v4, v173, s3, v3 bitop3:0xde
	v_add_u32_e32 v162, s21, v2
	s_add_i32 s20, 0, 0x14000
	s_waitcnt vmcnt(6)
	s_barrier
	v_add_u32_e32 v163, s20, v2
	v_add_u32_e32 v164, 0, v4
	v_add_u32_e32 v165, s33, v2
	v_add_u32_e32 v166, s60, v2
	ds_read_b128 v[2:5], v162
	s_waitcnt lgkmcnt(0)
	ds_read_b128 v[6:9], v162 offset:1024
	ds_read_b128 v[10:13], v162 offset:2048
	ds_read_b128 v[14:17], v162 offset:3072
	ds_read_b128 v[18:21], v163
	ds_read_b128 v[22:25], v163 offset:1024
	ds_read_b128 v[26:29], v163 offset:2048
	ds_read_b128 v[30:33], v163 offset:3072
	v_lshl_or_b32 v177, s2, 6, v172
	s_add_u32 s2, s0, 0x8000
	s_addc_u32 s3, s1, 0
	s_add_u32 s42, s28, 0x8000
	s_addc_u32 s43, s29, 0
	s_add_u32 s8, s0, 0x4000
	s_addc_u32 s9, s1, 0
	v_mov_b32_e32 v66, v170
	s_add_i32 s72, s18, 0x8000
	ds_read_b128 v[34:37], v164
	ds_read_b128 v[38:41], v164 offset:1024
	ds_read_b128 v[42:45], v164 offset:2048
	ds_read_b128 v[46:49], v164 offset:3072
	ds_read_b128 v[50:53], v164 offset:4096
	ds_read_b128 v[54:57], v164 offset:5120
	ds_read_b128 v[58:61], v164 offset:6144
	ds_read_b128 v[62:65], v164 offset:7168
	s_mov_b32 m0, s72
	s_add_i32 s73, s18, 0xa000
	global_load_lds_dwordx4 v66, s[8:9]
	v_mov_b32_e32 v66, v171
	s_mov_b32 m0, s73
	s_nop 0
	global_load_lds_dwordx4 v66, s[8:9]
	s_add_u32 s8, s0, 0xb4000
	s_addc_u32 s9, s1, 0
	v_mov_b32_e32 v66, v170
	s_add_i32 s74, s18, 0xc000
	s_mov_b32 m0, s74
	s_add_i32 s75, s18, 0xe000
	global_load_lds_dwordx4 v66, s[8:9]
	v_mov_b32_e32 v66, v171
	s_mov_b32 m0, s75
	s_add_u32 s40, s28, 0xc000
	global_load_lds_dwordx4 v66, s[8:9]
	s_waitcnt vmcnt(8)
	s_waitcnt lgkmcnt(0)
	s_addc_u32 s41, s29, 0
	s_barrier
	s_setprio 1
	s_waitcnt lgkmcnt(0)
	v_mfma_f32_16x16x128_f8f6f4 v[150:153], v[2:9], v[34:41], 0
	v_mfma_f32_16x16x128_f8f6f4 v[154:157], v[10:17], v[34:41], 0
	v_mfma_f32_16x16x128_f8f6f4 v[158:161], v[18:25], v[34:41], 0
	v_mfma_f32_16x16x128_f8f6f4 v[146:149], v[26:33], v[34:41], 0
	v_mfma_f32_16x16x128_f8f6f4 v[98:101], v[26:33], v[42:49], 0
	v_mfma_f32_16x16x128_f8f6f4 v[102:105], v[18:25], v[42:49], 0
	v_mfma_f32_16x16x128_f8f6f4 v[122:125], v[10:17], v[42:49], 0
	v_mfma_f32_16x16x128_f8f6f4 v[126:129], v[2:9], v[42:49], 0
	v_mfma_f32_16x16x128_f8f6f4 v[142:145], v[2:9], v[50:57], 0
	v_mfma_f32_16x16x128_f8f6f4 v[138:141], v[10:17], v[50:57], 0
	v_mfma_f32_16x16x128_f8f6f4 v[134:137], v[18:25], v[50:57], 0
	v_mfma_f32_16x16x128_f8f6f4 v[130:133], v[26:33], v[50:57], 0
	v_mfma_f32_16x16x128_f8f6f4 v[106:109], v[26:33], v[58:65], 0
	v_mfma_f32_16x16x128_f8f6f4 v[110:113], v[18:25], v[58:65], 0
	v_mfma_f32_16x16x128_f8f6f4 v[114:117], v[10:17], v[58:65], 0
	v_mfma_f32_16x16x128_f8f6f4 v[118:121], v[2:9], v[58:65], 0
	s_setprio 0
	s_barrier
	s_mov_b64 s[8:9], s[42:43]
	v_mov_b32_e32 v50, v170
	s_add_i32 s76, s21, s6
	ds_read_b128 v[34:37], v164 offset:16384
	ds_read_b128 v[38:41], v164 offset:17408
	ds_read_b128 v[42:45], v164 offset:18432
	ds_read_b128 v[46:49], v164 offset:19456
	ds_read_b128 v[178:181], v164 offset:20480
	ds_read_b128 v[182:185], v164 offset:21504
	ds_read_b128 v[186:189], v164 offset:22528
	ds_read_b128 v[190:193], v164 offset:23552
	s_mov_b32 m0, s76
	s_add_i32 s77, s76, 0x2000
	global_load_lds_dwordx4 v50, s[8:9]
	v_mov_b32_e32 v50, v171
	s_add_u32 s50, s28, 0xb8000
	s_mov_b32 m0, s77
	s_addc_u32 s51, s29, 0
	global_load_lds_dwordx4 v50, s[8:9]
	s_mov_b64 s[8:9], s[50:51]
	v_mov_b32_e32 v50, v170
	s_add_i32 s78, s20, s6
	s_mov_b32 m0, s78
	s_add_i32 s79, s78, 0x2000
	global_load_lds_dwordx4 v50, s[8:9]
	v_mov_b32_e32 v50, v171
	s_mov_b32 m0, s79
	s_nop 0
	global_load_lds_dwordx4 v50, s[8:9]
	s_waitcnt vmcnt(6)
	s_waitcnt lgkmcnt(0)
	s_barrier
	s_setprio 1
	s_waitcnt lgkmcnt(0)
	v_mfma_f32_16x16x128_f8f6f4 v[94:97], v[2:9], v[34:41], 0
	v_mfma_f32_16x16x128_f8f6f4 v[90:93], v[10:17], v[34:41], 0
	v_mfma_f32_16x16x128_f8f6f4 v[86:89], v[18:25], v[34:41], 0
	v_mfma_f32_16x16x128_f8f6f4 v[82:85], v[26:33], v[34:41], 0
	v_mfma_f32_16x16x128_f8f6f4 v[66:69], v[26:33], v[42:49], 0
	v_mfma_f32_16x16x128_f8f6f4 v[70:73], v[18:25], v[42:49], 0
	v_mfma_f32_16x16x128_f8f6f4 v[74:77], v[10:17], v[42:49], 0
	v_mfma_f32_16x16x128_f8f6f4 v[78:81], v[2:9], v[42:49], 0
	v_mfma_f32_16x16x128_f8f6f4 v[62:65], v[2:9], v[178:185], 0
	v_mfma_f32_16x16x128_f8f6f4 v[58:61], v[10:17], v[178:185], 0
	v_mfma_f32_16x16x128_f8f6f4 v[54:57], v[18:25], v[178:185], 0
	v_mfma_f32_16x16x128_f8f6f4 v[50:53], v[26:33], v[178:185], 0
	v_mfma_f32_16x16x128_f8f6f4 v[34:37], v[26:33], v[186:193], 0
	v_mfma_f32_16x16x128_f8f6f4 v[38:41], v[18:25], v[186:193], 0
	v_mfma_f32_16x16x128_f8f6f4 v[42:45], v[10:17], v[186:193], 0
	v_mfma_f32_16x16x128_f8f6f4 v[46:49], v[2:9], v[186:193], 0
	s_setprio 0
	s_barrier
	ds_read_b128 v[26:29], v165
	ds_read_b128 v[30:33], v165 offset:1024
	ds_read_b128 v[18:21], v165 offset:2048
	ds_read_b128 v[22:25], v165 offset:3072
	ds_read_b128 v[10:13], v166
	ds_read_b128 v[14:17], v166 offset:1024
	ds_read_b128 v[2:5], v166 offset:2048
	ds_read_b128 v[6:9], v166 offset:3072
	v_mov_b32_e32 v167, v170
	s_mov_b32 m0, s18
	ds_read_b128 v[178:181], v164 offset:32768
	ds_read_b128 v[182:185], v164 offset:33792
	ds_read_b128 v[186:189], v164 offset:34816
	ds_read_b128 v[190:193], v164 offset:35840
	ds_read_b128 v[202:205], v164 offset:36864
	ds_read_b128 v[206:209], v164 offset:37888
	ds_read_b128 v[210:213], v164 offset:38912
	ds_read_b128 v[214:217], v164 offset:39936
	s_nop 0
	global_load_lds_dwordx4 v167, s[2:3]
	v_mov_b32_e32 v167, v171
	s_mov_b32 m0, s19
	s_nop 0
	global_load_lds_dwordx4 v167, s[2:3]
	s_add_u32 s2, s0, 0xb8000
	s_addc_u32 s3, s1, 0
	v_mov_b32_e32 v167, v170
	s_mov_b32 m0, s61
	s_nop 0
	global_load_lds_dwordx4 v167, s[2:3]
	v_mov_b32_e32 v167, v171
	s_mov_b32 m0, s65
	s_nop 0
	global_load_lds_dwordx4 v167, s[2:3]
	s_waitcnt vmcnt(8)
	s_waitcnt lgkmcnt(0)
	s_barrier
	s_setprio 1
	s_waitcnt lgkmcnt(0)
	v_mfma_f32_16x16x128_f8f6f4 v[150:153], v[26:33], v[178:185], v[150:153]
	v_mfma_f32_16x16x128_f8f6f4 v[154:157], v[18:25], v[178:185], v[154:157]
	v_mfma_f32_16x16x128_f8f6f4 v[158:161], v[10:17], v[178:185], v[158:161]
	v_mfma_f32_16x16x128_f8f6f4 v[146:149], v[2:9], v[178:185], v[146:149]
	v_mfma_f32_16x16x128_f8f6f4 v[98:101], v[2:9], v[186:193], v[98:101]
	v_mfma_f32_16x16x128_f8f6f4 v[102:105], v[10:17], v[186:193], v[102:105]
	v_mfma_f32_16x16x128_f8f6f4 v[122:125], v[18:25], v[186:193], v[122:125]
	v_mfma_f32_16x16x128_f8f6f4 v[126:129], v[26:33], v[186:193], v[126:129]
	v_mfma_f32_16x16x128_f8f6f4 v[142:145], v[26:33], v[202:209], v[142:145]
	v_mfma_f32_16x16x128_f8f6f4 v[138:141], v[18:25], v[202:209], v[138:141]
	v_mfma_f32_16x16x128_f8f6f4 v[134:137], v[10:17], v[202:209], v[134:137]
	v_mfma_f32_16x16x128_f8f6f4 v[130:133], v[2:9], v[202:209], v[130:133]
	v_mfma_f32_16x16x128_f8f6f4 v[106:109], v[2:9], v[210:217], v[106:109]
	v_mfma_f32_16x16x128_f8f6f4 v[110:113], v[10:17], v[210:217], v[110:113]
	v_mfma_f32_16x16x128_f8f6f4 v[114:117], v[18:25], v[210:217], v[114:117]
	v_mfma_f32_16x16x128_f8f6f4 v[118:121], v[26:33], v[210:217], v[118:121]
	s_setprio 0
	s_barrier
	s_mov_b64 s[2:3], s[40:41]
	v_mov_b32_e32 v167, v170
	s_mov_b32 m0, s67
	ds_read_b128 v[178:181], v164 offset:49152
	ds_read_b128 v[182:185], v164 offset:50176
	ds_read_b128 v[186:189], v164 offset:51200
	ds_read_b128 v[190:193], v164 offset:52224
	ds_read_b128 v[202:205], v164 offset:53248
	ds_read_b128 v[206:209], v164 offset:54272
	ds_read_b128 v[210:213], v164 offset:55296
	ds_read_b128 v[214:217], v164 offset:56320
	s_add_u32 s52, s28, 0xbc000
	global_load_lds_dwordx4 v167, s[2:3]
	v_mov_b32_e32 v167, v171
	s_mov_b32 m0, s69
	s_addc_u32 s53, s29, 0
	global_load_lds_dwordx4 v167, s[2:3]
	s_mov_b64 s[2:3], s[52:53]
	v_mov_b32_e32 v167, v170
	s_mov_b32 m0, s70
	s_nop 0
	global_load_lds_dwordx4 v167, s[2:3]
	v_mov_b32_e32 v167, v171
	s_mov_b32 m0, s71
	s_nop 0
	global_load_lds_dwordx4 v167, s[2:3]
	s_waitcnt vmcnt(6)
	s_waitcnt lgkmcnt(0)
	s_barrier
	s_setprio 1
	s_waitcnt lgkmcnt(0)
	v_mfma_f32_16x16x128_f8f6f4 v[94:97], v[26:33], v[178:185], v[94:97]
	v_mfma_f32_16x16x128_f8f6f4 v[90:93], v[18:25], v[178:185], v[90:93]
	v_mfma_f32_16x16x128_f8f6f4 v[86:89], v[10:17], v[178:185], v[86:89]
	v_mfma_f32_16x16x128_f8f6f4 v[82:85], v[2:9], v[178:185], v[82:85]
	v_mfma_f32_16x16x128_f8f6f4 v[66:69], v[2:9], v[186:193], v[66:69]
	v_mfma_f32_16x16x128_f8f6f4 v[70:73], v[10:17], v[186:193], v[70:73]
	v_mfma_f32_16x16x128_f8f6f4 v[74:77], v[18:25], v[186:193], v[74:77]
	v_mfma_f32_16x16x128_f8f6f4 v[78:81], v[26:33], v[186:193], v[78:81]
	v_mfma_f32_16x16x128_f8f6f4 v[62:65], v[26:33], v[202:209], v[62:65]
	v_mfma_f32_16x16x128_f8f6f4 v[58:61], v[18:25], v[202:209], v[58:61]
	v_mfma_f32_16x16x128_f8f6f4 v[54:57], v[10:17], v[202:209], v[54:57]
	v_mfma_f32_16x16x128_f8f6f4 v[50:53], v[2:9], v[202:209], v[50:53]
	v_mfma_f32_16x16x128_f8f6f4 v[34:37], v[2:9], v[210:217], v[34:37]
	v_mfma_f32_16x16x128_f8f6f4 v[38:41], v[10:17], v[210:217], v[38:41]
	v_mfma_f32_16x16x128_f8f6f4 v[42:45], v[18:25], v[210:217], v[42:45]
	v_mfma_f32_16x16x128_f8f6f4 v[46:49], v[26:33], v[210:217], v[46:49]
	s_setprio 0
	s_barrier
	s_and_b32 s2, s12, 7
	s_mul_i32 s2, s2, 0xb00000
	s_mul_i32 s3, s11, 0x160000
	s_add_i32 s2, s2, s3
	s_add_u32 s2, s56, s2
	s_addc_u32 s3, s57, 0
	s_add_u32 s8, s2, 0x3eb08000
	s_addc_u32 s9, s3, 0
	s_add_u32 s2, s56, s5
	s_addc_u32 s3, s57, s4
	s_add_u32 s30, s2, 0x4310000
	s_addc_u32 s31, s3, 0
	s_mov_b64 s[2:3], s[30:31]
.LBB0_931:
	ds_read_b128 v[10:13], v162
	ds_read_b128 v[14:17], v162 offset:1024
	ds_read_b128 v[2:5], v162 offset:2048
	ds_read_b128 v[6:9], v162 offset:3072
	ds_read_b128 v[26:29], v163
	ds_read_b128 v[30:33], v163 offset:1024
	ds_read_b128 v[18:21], v163 offset:2048
	ds_read_b128 v[22:25], v163 offset:3072
	s_add_u32 s4, s8, 0x8000
	s_addc_u32 s5, s9, 0
	s_cmp_eq_u32 s66, 40
	s_cselect_b32 s7, s29, s3
	s_cselect_b32 s6, s28, s2
	s_cselect_b32 s15, s1, s5
	s_cselect_b32 s14, s0, s4
	s_add_u32 s80, s8, 0x4000
	s_addc_u32 s81, s9, 0
	v_mov_b32_e32 v167, v170
	s_mov_b32 m0, s72
	ds_read_b128 v[178:181], v164
	ds_read_b128 v[182:185], v164 offset:1024
	ds_read_b128 v[186:189], v164 offset:2048
	ds_read_b128 v[190:193], v164 offset:3072
	ds_read_b128 v[202:205], v164 offset:4096
	ds_read_b128 v[206:209], v164 offset:5120
	ds_read_b128 v[210:213], v164 offset:6144
	ds_read_b128 v[214:217], v164 offset:7168
	s_add_u32 s8, s8, 0xb4000
	global_load_lds_dwordx4 v167, s[80:81]
	v_mov_b32_e32 v167, v171
	s_mov_b32 m0, s73
	s_addc_u32 s9, s9, 0
	global_load_lds_dwordx4 v167, s[80:81]
	v_mov_b32_e32 v167, v170
	s_mov_b32 m0, s74
	s_nop 0
	global_load_lds_dwordx4 v167, s[8:9]
	v_mov_b32_e32 v167, v171
	s_mov_b32 m0, s75
	s_nop 0
	global_load_lds_dwordx4 v167, s[8:9]
	s_waitcnt vmcnt(8)
	s_waitcnt lgkmcnt(0)
	s_add_u32 s8, s6, 0x4000
	s_addc_u32 s9, s7, 0
	s_barrier
	s_setprio 1
	s_waitcnt lgkmcnt(0)
	v_mfma_f32_16x16x128_f8f6f4 v[150:153], v[10:17], v[178:185], v[150:153]
	v_mfma_f32_16x16x128_f8f6f4 v[154:157], v[2:9], v[178:185], v[154:157]
	v_mfma_f32_16x16x128_f8f6f4 v[158:161], v[26:33], v[178:185], v[158:161]
	v_mfma_f32_16x16x128_f8f6f4 v[146:149], v[18:25], v[178:185], v[146:149]
	v_mfma_f32_16x16x128_f8f6f4 v[98:101], v[18:25], v[186:193], v[98:101]
	v_mfma_f32_16x16x128_f8f6f4 v[102:105], v[26:33], v[186:193], v[102:105]
	v_mfma_f32_16x16x128_f8f6f4 v[122:125], v[2:9], v[186:193], v[122:125]
	v_mfma_f32_16x16x128_f8f6f4 v[126:129], v[10:17], v[186:193], v[126:129]
	v_mfma_f32_16x16x128_f8f6f4 v[142:145], v[10:17], v[202:209], v[142:145]
	v_mfma_f32_16x16x128_f8f6f4 v[138:141], v[2:9], v[202:209], v[138:141]
	v_mfma_f32_16x16x128_f8f6f4 v[134:137], v[26:33], v[202:209], v[134:137]
	v_mfma_f32_16x16x128_f8f6f4 v[130:133], v[18:25], v[202:209], v[130:133]
	v_mfma_f32_16x16x128_f8f6f4 v[106:109], v[18:25], v[210:217], v[106:109]
	v_mfma_f32_16x16x128_f8f6f4 v[110:113], v[26:33], v[210:217], v[110:113]
	v_mfma_f32_16x16x128_f8f6f4 v[114:117], v[2:9], v[210:217], v[114:117]
	v_mfma_f32_16x16x128_f8f6f4 v[118:121], v[10:17], v[210:217], v[118:121]
	s_setprio 0
	s_barrier
	s_mov_b64 s[80:81], s[6:7]
	v_mov_b32_e32 v167, v170
	s_mov_b32 m0, s76
	ds_read_b128 v[178:181], v164 offset:16384
	ds_read_b128 v[182:185], v164 offset:17408
	ds_read_b128 v[186:189], v164 offset:18432
	ds_read_b128 v[190:193], v164 offset:19456
	ds_read_b128 v[202:205], v164 offset:20480
	ds_read_b128 v[206:209], v164 offset:21504
	ds_read_b128 v[210:213], v164 offset:22528
	ds_read_b128 v[214:217], v164 offset:23552
	s_nop 0
	global_load_lds_dwordx4 v167, s[80:81]
	v_mov_b32_e32 v167, v171
	s_mov_b32 m0, s77
	s_nop 0
	global_load_lds_dwordx4 v167, s[80:81]
	s_add_u32 s80, s6, 0xb0000
	s_addc_u32 s81, s7, 0
	v_mov_b32_e32 v167, v170
	s_mov_b32 m0, s78
	s_nop 0
	global_load_lds_dwordx4 v167, s[80:81]
	v_mov_b32_e32 v167, v171
	s_mov_b32 m0, s79
	s_nop 0
	global_load_lds_dwordx4 v167, s[80:81]
	s_waitcnt vmcnt(6)
	s_waitcnt lgkmcnt(0)
	s_barrier
	s_setprio 1
	s_waitcnt lgkmcnt(0)
	v_mfma_f32_16x16x128_f8f6f4 v[94:97], v[10:17], v[178:185], v[94:97]
	v_mfma_f32_16x16x128_f8f6f4 v[90:93], v[2:9], v[178:185], v[90:93]
	v_mfma_f32_16x16x128_f8f6f4 v[86:89], v[26:33], v[178:185], v[86:89]
	v_mfma_f32_16x16x128_f8f6f4 v[82:85], v[18:25], v[178:185], v[82:85]
	v_mfma_f32_16x16x128_f8f6f4 v[66:69], v[18:25], v[186:193], v[66:69]
	v_mfma_f32_16x16x128_f8f6f4 v[70:73], v[26:33], v[186:193], v[70:73]
	v_mfma_f32_16x16x128_f8f6f4 v[74:77], v[2:9], v[186:193], v[74:77]
	v_mfma_f32_16x16x128_f8f6f4 v[78:81], v[10:17], v[186:193], v[78:81]
	v_mfma_f32_16x16x128_f8f6f4 v[62:65], v[10:17], v[202:209], v[62:65]
	v_mfma_f32_16x16x128_f8f6f4 v[58:61], v[2:9], v[202:209], v[58:61]
	v_mfma_f32_16x16x128_f8f6f4 v[54:57], v[26:33], v[202:209], v[54:57]
	v_mfma_f32_16x16x128_f8f6f4 v[50:53], v[18:25], v[202:209], v[50:53]
	v_mfma_f32_16x16x128_f8f6f4 v[34:37], v[18:25], v[210:217], v[34:37]
	v_mfma_f32_16x16x128_f8f6f4 v[38:41], v[26:33], v[210:217], v[38:41]
	v_mfma_f32_16x16x128_f8f6f4 v[42:45], v[2:9], v[210:217], v[42:45]
	v_mfma_f32_16x16x128_f8f6f4 v[46:49], v[10:17], v[210:217], v[46:49]
	s_setprio 0
	s_barrier
	ds_read_b128 v[26:29], v165
	ds_read_b128 v[30:33], v165 offset:1024
	ds_read_b128 v[18:21], v165 offset:2048
	ds_read_b128 v[22:25], v165 offset:3072
	ds_read_b128 v[10:13], v166
	ds_read_b128 v[14:17], v166 offset:1024
	ds_read_b128 v[2:5], v166 offset:2048
	ds_read_b128 v[6:9], v166 offset:3072
	s_mov_b64 s[80:81], s[14:15]
	v_mov_b32_e32 v167, v170
	s_mov_b32 m0, s18
	ds_read_b128 v[178:181], v164 offset:32768
	ds_read_b128 v[182:185], v164 offset:33792
	ds_read_b128 v[186:189], v164 offset:34816
	ds_read_b128 v[190:193], v164 offset:35840
	ds_read_b128 v[202:205], v164 offset:36864
	ds_read_b128 v[206:209], v164 offset:37888
	ds_read_b128 v[210:213], v164 offset:38912
	ds_read_b128 v[214:217], v164 offset:39936
	s_add_u32 s14, s14, 0xb0000
	global_load_lds_dwordx4 v167, s[80:81]
	v_mov_b32_e32 v167, v171
	s_mov_b32 m0, s19
	s_addc_u32 s15, s15, 0
	global_load_lds_dwordx4 v167, s[80:81]
	v_mov_b32_e32 v167, v170
	s_mov_b32 m0, s61
	s_nop 0
	global_load_lds_dwordx4 v167, s[14:15]
	v_mov_b32_e32 v167, v171
	s_mov_b32 m0, s65
	s_nop 0
	global_load_lds_dwordx4 v167, s[14:15]
	s_waitcnt vmcnt(8)
	s_waitcnt lgkmcnt(0)
	s_barrier
	s_setprio 1
	s_waitcnt lgkmcnt(0)
	v_mfma_f32_16x16x128_f8f6f4 v[150:153], v[26:33], v[178:185], v[150:153]
	v_mfma_f32_16x16x128_f8f6f4 v[154:157], v[18:25], v[178:185], v[154:157]
	v_mfma_f32_16x16x128_f8f6f4 v[158:161], v[10:17], v[178:185], v[158:161]
	v_mfma_f32_16x16x128_f8f6f4 v[146:149], v[2:9], v[178:185], v[146:149]
	v_mfma_f32_16x16x128_f8f6f4 v[98:101], v[2:9], v[186:193], v[98:101]
	v_mfma_f32_16x16x128_f8f6f4 v[102:105], v[10:17], v[186:193], v[102:105]
	v_mfma_f32_16x16x128_f8f6f4 v[122:125], v[18:25], v[186:193], v[122:125]
	v_mfma_f32_16x16x128_f8f6f4 v[126:129], v[26:33], v[186:193], v[126:129]
	v_mfma_f32_16x16x128_f8f6f4 v[142:145], v[26:33], v[202:209], v[142:145]
	v_mfma_f32_16x16x128_f8f6f4 v[138:141], v[18:25], v[202:209], v[138:141]
	v_mfma_f32_16x16x128_f8f6f4 v[134:137], v[10:17], v[202:209], v[134:137]
	v_mfma_f32_16x16x128_f8f6f4 v[130:133], v[2:9], v[202:209], v[130:133]
	v_mfma_f32_16x16x128_f8f6f4 v[106:109], v[2:9], v[210:217], v[106:109]
	v_mfma_f32_16x16x128_f8f6f4 v[110:113], v[10:17], v[210:217], v[110:113]
	v_mfma_f32_16x16x128_f8f6f4 v[114:117], v[18:25], v[210:217], v[114:117]
	v_mfma_f32_16x16x128_f8f6f4 v[118:121], v[26:33], v[210:217], v[118:121]
	s_setprio 0
	s_barrier
	v_mov_b32_e32 v167, v170
	s_mov_b32 m0, s67
	ds_read_b128 v[178:181], v164 offset:49152
	ds_read_b128 v[182:185], v164 offset:50176
	ds_read_b128 v[186:189], v164 offset:51200
	ds_read_b128 v[190:193], v164 offset:52224
	ds_read_b128 v[202:205], v164 offset:53248
	ds_read_b128 v[206:209], v164 offset:54272
	ds_read_b128 v[210:213], v164 offset:55296
	ds_read_b128 v[214:217], v164 offset:56320
	s_add_u32 s6, s6, 0xb4000
	global_load_lds_dwordx4 v167, s[8:9]
	v_mov_b32_e32 v167, v171
	s_mov_b32 m0, s69
	s_addc_u32 s7, s7, 0
	global_load_lds_dwordx4 v167, s[8:9]
	v_mov_b32_e32 v167, v170
	s_mov_b32 m0, s70
	s_nop 0
	global_load_lds_dwordx4 v167, s[6:7]
	v_mov_b32_e32 v167, v171
	s_mov_b32 m0, s71
	s_nop 0
	global_load_lds_dwordx4 v167, s[6:7]
	s_waitcnt vmcnt(6)
	s_waitcnt lgkmcnt(0)
	s_barrier
	s_setprio 1
	s_waitcnt lgkmcnt(0)
	v_mfma_f32_16x16x128_f8f6f4 v[94:97], v[26:33], v[178:185], v[94:97]
	v_mfma_f32_16x16x128_f8f6f4 v[90:93], v[18:25], v[178:185], v[90:93]
	v_mfma_f32_16x16x128_f8f6f4 v[86:89], v[10:17], v[178:185], v[86:89]
	v_mfma_f32_16x16x128_f8f6f4 v[82:85], v[2:9], v[178:185], v[82:85]
	v_mfma_f32_16x16x128_f8f6f4 v[66:69], v[2:9], v[186:193], v[66:69]
	v_mfma_f32_16x16x128_f8f6f4 v[70:73], v[10:17], v[186:193], v[70:73]
	v_mfma_f32_16x16x128_f8f6f4 v[74:77], v[18:25], v[186:193], v[74:77]
	v_mfma_f32_16x16x128_f8f6f4 v[78:81], v[26:33], v[186:193], v[78:81]
	v_mfma_f32_16x16x128_f8f6f4 v[62:65], v[26:33], v[202:209], v[62:65]
	v_mfma_f32_16x16x128_f8f6f4 v[58:61], v[18:25], v[202:209], v[58:61]
	v_mfma_f32_16x16x128_f8f6f4 v[54:57], v[10:17], v[202:209], v[54:57]
	v_mfma_f32_16x16x128_f8f6f4 v[50:53], v[2:9], v[202:209], v[50:53]
	v_mfma_f32_16x16x128_f8f6f4 v[34:37], v[2:9], v[210:217], v[34:37]
	v_mfma_f32_16x16x128_f8f6f4 v[38:41], v[10:17], v[210:217], v[38:41]
	v_mfma_f32_16x16x128_f8f6f4 v[42:45], v[18:25], v[210:217], v[42:45]
	v_mfma_f32_16x16x128_f8f6f4 v[46:49], v[26:33], v[210:217], v[46:49]
	s_setprio 0
	s_barrier
	s_add_i32 s66, s66, 2
	s_add_u32 s2, s2, 0x8000
	s_addc_u32 s3, s3, 0
	s_cmp_gt_u32 s66, 41
	s_mov_b64 s[8:9], s[4:5]
	s_cbranch_scc0 .LBB0_931
	s_cmpk_lt_u32 s62, 0x100
	s_cbranch_scc0 .LBB0_934
	s_barrier

.LBB0_977:
	s_add_i32 s69, s33, s72
	v_mov_b32_e32 v2, v170
	s_waitcnt vmcnt(2)
	s_barrier
	s_mov_b32 m0, s69
	s_add_i32 s70, s69, 0x2000
	global_load_lds_dwordx4 v2, s[46:47]
	v_mov_b32_e32 v2, v171
	s_mov_b32 m0, s70
	s_and_b32 s44, s63, 3
	global_load_lds_dwordx4 v2, s[46:47]
	s_add_i32 s46, s60, s72
	v_mov_b32_e32 v2, v170
	s_mov_b32 m0, s46
	s_add_i32 s47, s46, 0x2000
	global_load_lds_dwordx4 v2, s[48:49]
	v_mov_b32_e32 v2, v171
	s_mov_b32 m0, s47
	v_lshl_or_b32 v177, s14, 6, v172
	global_load_lds_dwordx4 v2, s[48:49]
	v_lshlrev_b32_e32 v2, 2, v172
	s_lshl_b32 s14, s14, 13
	v_and_b32_e32 v2, 32, v2
	v_lshl_or_b32 v3, s44, 12, v174
	v_bitop3_b32 v2, v173, s14, v2 bitop3:0xde
	v_add_u32_e32 v162, s21, v3
	s_waitcnt vmcnt(6)
	s_barrier
	v_add_u32_e32 v163, s20, v3
	v_add_u32_e32 v164, 0, v2
	v_add_u32_e32 v165, s33, v3
	v_add_u32_e32 v166, s60, v3
	ds_read_b128 v[2:5], v162
	ds_read_b128 v[6:9], v162 offset:1024
	ds_read_b128 v[10:13], v162 offset:2048
	ds_read_b128 v[14:17], v162 offset:3072
	ds_read_b128 v[18:21], v163
	ds_read_b128 v[22:25], v163 offset:1024
	ds_read_b128 v[26:29], v163 offset:2048
	ds_read_b128 v[30:33], v163 offset:3072
	s_add_u32 s14, s0, 0x8000
	s_addc_u32 s15, s1, 0
	s_add_u32 s16, s0, 0x4000
	s_addc_u32 s17, s1, 0
	v_mov_b32_e32 v66, v170
	s_add_i32 s33, s64, 0x8000
	ds_read_b128 v[34:37], v164
	ds_read_b128 v[38:41], v164 offset:1024
	ds_read_b128 v[42:45], v164 offset:2048
	ds_read_b128 v[46:49], v164 offset:3072
	ds_read_b128 v[50:53], v164 offset:4096
	ds_read_b128 v[54:57], v164 offset:5120
	ds_read_b128 v[58:61], v164 offset:6144
	ds_read_b128 v[62:65], v164 offset:7168
	s_mov_b32 m0, s33
	s_add_i32 s48, s64, 0xa000
	global_load_lds_dwordx4 v66, s[16:17]
	v_mov_b32_e32 v66, v171
	s_mov_b32 m0, s48
	s_nop 0
	global_load_lds_dwordx4 v66, s[16:17]
	s_add_u32 s16, s0, 0xb4000
	s_addc_u32 s17, s1, 0
	v_mov_b32_e32 v66, v170
	s_add_i32 s49, s64, 0xc000
	s_mov_b32 m0, s49
	s_add_i32 s60, s64, 0xe000
	global_load_lds_dwordx4 v66, s[16:17]
	v_mov_b32_e32 v66, v171
	s_mov_b32 m0, s60
	s_nop 0
	global_load_lds_dwordx4 v66, s[16:17]
	s_waitcnt vmcnt(8)
	s_waitcnt lgkmcnt(0)
	s_barrier
	s_setprio 1
	s_waitcnt lgkmcnt(0)
	v_mfma_f32_16x16x128_f8f6f4 v[146:149], v[2:9], v[34:41], 0
	v_mfma_f32_16x16x128_f8f6f4 v[150:153], v[10:17], v[34:41], 0
	v_mfma_f32_16x16x128_f8f6f4 v[154:157], v[18:25], v[34:41], 0
	v_mfma_f32_16x16x128_f8f6f4 v[158:161], v[26:33], v[34:41], 0
	v_mfma_f32_16x16x128_f8f6f4 v[98:101], v[26:33], v[42:49], 0
	v_mfma_f32_16x16x128_f8f6f4 v[102:105], v[18:25], v[42:49], 0
	v_mfma_f32_16x16x128_f8f6f4 v[106:109], v[10:17], v[42:49], 0
	v_mfma_f32_16x16x128_f8f6f4 v[110:113], v[2:9], v[42:49], 0
	v_mfma_f32_16x16x128_f8f6f4 v[142:145], v[2:9], v[50:57], 0
	v_mfma_f32_16x16x128_f8f6f4 v[138:141], v[10:17], v[50:57], 0
	v_mfma_f32_16x16x128_f8f6f4 v[134:137], v[18:25], v[50:57], 0
	v_mfma_f32_16x16x128_f8f6f4 v[130:133], v[26:33], v[50:57], 0
	v_mfma_f32_16x16x128_f8f6f4 v[114:117], v[26:33], v[58:65], 0
	v_mfma_f32_16x16x128_f8f6f4 v[118:121], v[18:25], v[58:65], 0
	v_mfma_f32_16x16x128_f8f6f4 v[122:125], v[10:17], v[58:65], 0
	v_mfma_f32_16x16x128_f8f6f4 v[126:129], v[2:9], v[58:65], 0
	s_setprio 0
	s_barrier
	v_mov_b32_e32 v50, v170
	s_add_i32 s21, s21, s72
	ds_read_b128 v[34:37], v164 offset:16384
	ds_read_b128 v[38:41], v164 offset:17408
	ds_read_b128 v[42:45], v164 offset:18432
	ds_read_b128 v[46:49], v164 offset:19456
	ds_read_b128 v[178:181], v164 offset:20480
	ds_read_b128 v[182:185], v164 offset:21504
	ds_read_b128 v[186:189], v164 offset:22528
	ds_read_b128 v[190:193], v164 offset:23552
	s_mov_b32 m0, s21
	s_add_i32 s71, s21, 0x2000
	global_load_lds_dwordx4 v50, s[42:43]
	v_mov_b32_e32 v50, v171
	s_mov_b32 m0, s71
	s_add_i32 s20, s20, s72
	global_load_lds_dwordx4 v50, s[42:43]
	v_mov_b32_e32 v50, v170
	s_mov_b32 m0, s20
	s_add_i32 s72, s20, 0x2000
	global_load_lds_dwordx4 v50, s[50:51]
	v_mov_b32_e32 v50, v171
	s_mov_b32 m0, s72
	s_nop 0
	global_load_lds_dwordx4 v50, s[50:51]
	s_waitcnt vmcnt(6)
	s_waitcnt lgkmcnt(0)
	s_barrier
	s_setprio 1
	s_waitcnt lgkmcnt(0)
	v_mfma_f32_16x16x128_f8f6f4 v[94:97], v[2:9], v[34:41], 0
	v_mfma_f32_16x16x128_f8f6f4 v[90:93], v[10:17], v[34:41], 0
	v_mfma_f32_16x16x128_f8f6f4 v[86:89], v[18:25], v[34:41], 0
	v_mfma_f32_16x16x128_f8f6f4 v[82:85], v[26:33], v[34:41], 0
	v_mfma_f32_16x16x128_f8f6f4 v[66:69], v[26:33], v[42:49], 0
	v_mfma_f32_16x16x128_f8f6f4 v[70:73], v[18:25], v[42:49], 0
	v_mfma_f32_16x16x128_f8f6f4 v[74:77], v[10:17], v[42:49], 0
	v_mfma_f32_16x16x128_f8f6f4 v[78:81], v[2:9], v[42:49], 0
	v_mfma_f32_16x16x128_f8f6f4 v[62:65], v[2:9], v[178:185], 0
	v_mfma_f32_16x16x128_f8f6f4 v[58:61], v[10:17], v[178:185], 0
	v_mfma_f32_16x16x128_f8f6f4 v[54:57], v[18:25], v[178:185], 0
	v_mfma_f32_16x16x128_f8f6f4 v[50:53], v[26:33], v[178:185], 0
	v_mfma_f32_16x16x128_f8f6f4 v[34:37], v[26:33], v[186:193], 0
	v_mfma_f32_16x16x128_f8f6f4 v[38:41], v[18:25], v[186:193], 0
	v_mfma_f32_16x16x128_f8f6f4 v[42:45], v[10:17], v[186:193], 0
	v_mfma_f32_16x16x128_f8f6f4 v[46:49], v[2:9], v[186:193], 0
	s_setprio 0
	s_barrier
	ds_read_b128 v[26:29], v165
	ds_read_b128 v[30:33], v165 offset:1024
	ds_read_b128 v[18:21], v165 offset:2048
	ds_read_b128 v[22:25], v165 offset:3072
	ds_read_b128 v[10:13], v166
	ds_read_b128 v[14:17], v166 offset:1024
	ds_read_b128 v[2:5], v166 offset:2048
	ds_read_b128 v[6:9], v166 offset:3072
	v_mov_b32_e32 v167, v170
	s_mov_b32 m0, s64
	ds_read_b128 v[178:181], v164 offset:32768
	ds_read_b128 v[182:185], v164 offset:33792
	ds_read_b128 v[186:189], v164 offset:34816
	ds_read_b128 v[190:193], v164 offset:35840
	ds_read_b128 v[202:205], v164 offset:36864
	ds_read_b128 v[206:209], v164 offset:37888
	ds_read_b128 v[210:213], v164 offset:38912
	ds_read_b128 v[214:217], v164 offset:39936
	s_nop 0
	global_load_lds_dwordx4 v167, s[14:15]
	v_mov_b32_e32 v167, v171
	s_mov_b32 m0, s45
	s_nop 0
	global_load_lds_dwordx4 v167, s[14:15]
	s_add_u32 s14, s0, 0xb8000
	s_addc_u32 s15, s1, 0
	v_mov_b32_e32 v167, v170
	s_mov_b32 m0, s65
	s_nop 0
	global_load_lds_dwordx4 v167, s[14:15]
	v_mov_b32_e32 v167, v171
	s_mov_b32 m0, s66
	s_nop 0
	global_load_lds_dwordx4 v167, s[14:15]
	s_waitcnt vmcnt(8)
	s_waitcnt lgkmcnt(0)
	s_barrier
	s_setprio 1
	s_waitcnt lgkmcnt(0)
	v_mfma_f32_16x16x128_f8f6f4 v[146:149], v[26:33], v[178:185], v[146:149]
	v_mfma_f32_16x16x128_f8f6f4 v[150:153], v[18:25], v[178:185], v[150:153]
	v_mfma_f32_16x16x128_f8f6f4 v[154:157], v[10:17], v[178:185], v[154:157]
	v_mfma_f32_16x16x128_f8f6f4 v[158:161], v[2:9], v[178:185], v[158:161]
	v_mfma_f32_16x16x128_f8f6f4 v[98:101], v[2:9], v[186:193], v[98:101]
	v_mfma_f32_16x16x128_f8f6f4 v[102:105], v[10:17], v[186:193], v[102:105]
	v_mfma_f32_16x16x128_f8f6f4 v[106:109], v[18:25], v[186:193], v[106:109]
	v_mfma_f32_16x16x128_f8f6f4 v[110:113], v[26:33], v[186:193], v[110:113]
	v_mfma_f32_16x16x128_f8f6f4 v[142:145], v[26:33], v[202:209], v[142:145]
	v_mfma_f32_16x16x128_f8f6f4 v[138:141], v[18:25], v[202:209], v[138:141]
	v_mfma_f32_16x16x128_f8f6f4 v[134:137], v[10:17], v[202:209], v[134:137]
	v_mfma_f32_16x16x128_f8f6f4 v[130:133], v[2:9], v[202:209], v[130:133]
	v_mfma_f32_16x16x128_f8f6f4 v[114:117], v[2:9], v[210:217], v[114:117]
	v_mfma_f32_16x16x128_f8f6f4 v[118:121], v[10:17], v[210:217], v[118:121]
	v_mfma_f32_16x16x128_f8f6f4 v[122:125], v[18:25], v[210:217], v[122:125]
	v_mfma_f32_16x16x128_f8f6f4 v[126:129], v[26:33], v[210:217], v[126:129]
	s_setprio 0
	s_barrier
	v_mov_b32_e32 v167, v170
	s_mov_b32 m0, s69
	ds_read_b128 v[178:181], v164 offset:49152
	ds_read_b128 v[182:185], v164 offset:50176
	ds_read_b128 v[186:189], v164 offset:51200
	ds_read_b128 v[190:193], v164 offset:52224
	ds_read_b128 v[202:205], v164 offset:53248
	ds_read_b128 v[206:209], v164 offset:54272
	ds_read_b128 v[210:213], v164 offset:55296
	ds_read_b128 v[214:217], v164 offset:56320
	s_nop 0
	global_load_lds_dwordx4 v167, s[40:41]
	v_mov_b32_e32 v167, v171
	s_mov_b32 m0, s70
	s_nop 0
	global_load_lds_dwordx4 v167, s[40:41]
	v_mov_b32_e32 v167, v170
	s_mov_b32 m0, s46
	s_nop 0
	global_load_lds_dwordx4 v167, s[52:53]
	v_mov_b32_e32 v167, v171
	s_mov_b32 m0, s47
	s_nop 0
	global_load_lds_dwordx4 v167, s[52:53]
	s_waitcnt vmcnt(6)
	s_waitcnt lgkmcnt(0)
	s_barrier
	s_setprio 1
	s_waitcnt lgkmcnt(0)
	v_mfma_f32_16x16x128_f8f6f4 v[94:97], v[26:33], v[178:185], v[94:97]
	v_mfma_f32_16x16x128_f8f6f4 v[90:93], v[18:25], v[178:185], v[90:93]
	v_mfma_f32_16x16x128_f8f6f4 v[86:89], v[10:17], v[178:185], v[86:89]
	v_mfma_f32_16x16x128_f8f6f4 v[82:85], v[2:9], v[178:185], v[82:85]
	v_mfma_f32_16x16x128_f8f6f4 v[66:69], v[2:9], v[186:193], v[66:69]
	v_mfma_f32_16x16x128_f8f6f4 v[70:73], v[10:17], v[186:193], v[70:73]
	v_mfma_f32_16x16x128_f8f6f4 v[74:77], v[18:25], v[186:193], v[74:77]
	v_mfma_f32_16x16x128_f8f6f4 v[78:81], v[26:33], v[186:193], v[78:81]
	v_mfma_f32_16x16x128_f8f6f4 v[62:65], v[26:33], v[202:209], v[62:65]
	v_mfma_f32_16x16x128_f8f6f4 v[58:61], v[18:25], v[202:209], v[58:61]
	v_mfma_f32_16x16x128_f8f6f4 v[54:57], v[10:17], v[202:209], v[54:57]
	v_mfma_f32_16x16x128_f8f6f4 v[50:53], v[2:9], v[202:209], v[50:53]
	v_mfma_f32_16x16x128_f8f6f4 v[34:37], v[2:9], v[210:217], v[34:37]
	v_mfma_f32_16x16x128_f8f6f4 v[38:41], v[10:17], v[210:217], v[38:41]
	v_mfma_f32_16x16x128_f8f6f4 v[42:45], v[18:25], v[210:217], v[42:45]
	v_mfma_f32_16x16x128_f8f6f4 v[46:49], v[26:33], v[210:217], v[46:49]
	s_setprio 0
	s_barrier
	s_add_i32 s10, s10, s11
	s_mul_i32 s10, s10, 0x160000
	s_add_i32 s10, s10, 0x580000
	s_add_u32 s10, s56, s10
	s_addc_u32 s11, s57, 0
	s_add_u32 s40, s10, 0x3eb08000
	s_addc_u32 s41, s11, 0
.LBB0_978:
	ds_read_b128 v[10:13], v162
	ds_read_b128 v[14:17], v162 offset:1024
	ds_read_b128 v[2:5], v162 offset:2048
	ds_read_b128 v[6:9], v162 offset:3072
	ds_read_b128 v[26:29], v163
	ds_read_b128 v[30:33], v163 offset:1024
	ds_read_b128 v[18:21], v163 offset:2048
	ds_read_b128 v[22:25], v163 offset:3072
	s_add_u32 s14, s40, 0x8000
	s_addc_u32 s15, s41, 0
	s_cmp_eq_u32 s67, 40
	s_cselect_b32 s17, s29, s31
	s_cselect_b32 s16, s28, s30
	s_cselect_b32 s43, s1, s15
	s_cselect_b32 s42, s0, s14
	s_add_u32 s10, s40, 0x4000
	s_addc_u32 s11, s41, 0
	v_mov_b32_e32 v167, v170
	s_mov_b32 m0, s33
	ds_read_b128 v[178:181], v164
	ds_read_b128 v[182:185], v164 offset:1024
	ds_read_b128 v[186:189], v164 offset:2048
	ds_read_b128 v[190:193], v164 offset:3072
	ds_read_b128 v[202:205], v164 offset:4096
	ds_read_b128 v[206:209], v164 offset:5120
	ds_read_b128 v[210:213], v164 offset:6144
	ds_read_b128 v[214:217], v164 offset:7168
	s_nop 0
	global_load_lds_dwordx4 v167, s[10:11]
	v_mov_b32_e32 v167, v171
	s_mov_b32 m0, s48
	s_nop 0
	global_load_lds_dwordx4 v167, s[10:11]
	s_add_u32 s10, s40, 0xb4000
	s_addc_u32 s11, s41, 0
	v_mov_b32_e32 v167, v170
	s_mov_b32 m0, s49
	s_add_u32 s40, s16, 0x4000
	global_load_lds_dwordx4 v167, s[10:11]
	v_mov_b32_e32 v167, v171
	s_mov_b32 m0, s60
	s_addc_u32 s41, s17, 0
	global_load_lds_dwordx4 v167, s[10:11]
	s_waitcnt vmcnt(8)
	s_waitcnt lgkmcnt(0)
	s_barrier
	s_setprio 1
	s_waitcnt lgkmcnt(0)
	v_mfma_f32_16x16x128_f8f6f4 v[146:149], v[10:17], v[178:185], v[146:149]
	v_mfma_f32_16x16x128_f8f6f4 v[150:153], v[2:9], v[178:185], v[150:153]
	v_mfma_f32_16x16x128_f8f6f4 v[154:157], v[26:33], v[178:185], v[154:157]
	v_mfma_f32_16x16x128_f8f6f4 v[158:161], v[18:25], v[178:185], v[158:161]
	v_mfma_f32_16x16x128_f8f6f4 v[98:101], v[18:25], v[186:193], v[98:101]
	v_mfma_f32_16x16x128_f8f6f4 v[102:105], v[26:33], v[186:193], v[102:105]
	v_mfma_f32_16x16x128_f8f6f4 v[106:109], v[2:9], v[186:193], v[106:109]
	v_mfma_f32_16x16x128_f8f6f4 v[110:113], v[10:17], v[186:193], v[110:113]
	v_mfma_f32_16x16x128_f8f6f4 v[142:145], v[10:17], v[202:209], v[142:145]
	v_mfma_f32_16x16x128_f8f6f4 v[138:141], v[2:9], v[202:209], v[138:141]
	v_mfma_f32_16x16x128_f8f6f4 v[134:137], v[26:33], v[202:209], v[134:137]
	v_mfma_f32_16x16x128_f8f6f4 v[130:133], v[18:25], v[202:209], v[130:133]
	v_mfma_f32_16x16x128_f8f6f4 v[114:117], v[18:25], v[210:217], v[114:117]
	v_mfma_f32_16x16x128_f8f6f4 v[118:121], v[26:33], v[210:217], v[118:121]
	v_mfma_f32_16x16x128_f8f6f4 v[122:125], v[2:9], v[210:217], v[122:125]
	v_mfma_f32_16x16x128_f8f6f4 v[126:129], v[10:17], v[210:217], v[126:129]
	s_setprio 0
	s_barrier
	s_mov_b64 s[10:11], s[16:17]
	v_mov_b32_e32 v167, v170
	s_mov_b32 m0, s21
	ds_read_b128 v[178:181], v164 offset:16384
	ds_read_b128 v[182:185], v164 offset:17408
	ds_read_b128 v[186:189], v164 offset:18432
	ds_read_b128 v[190:193], v164 offset:19456
	ds_read_b128 v[202:205], v164 offset:20480
	ds_read_b128 v[206:209], v164 offset:21504
	ds_read_b128 v[210:213], v164 offset:22528
	ds_read_b128 v[214:217], v164 offset:23552
	s_nop 0
	global_load_lds_dwordx4 v167, s[10:11]
	v_mov_b32_e32 v167, v171
	s_mov_b32 m0, s71
	s_nop 0
	global_load_lds_dwordx4 v167, s[10:11]
	s_add_u32 s10, s16, 0xb0000
	s_addc_u32 s11, s17, 0
	v_mov_b32_e32 v167, v170
	s_mov_b32 m0, s20
	s_nop 0
	global_load_lds_dwordx4 v167, s[10:11]
	v_mov_b32_e32 v167, v171
	s_mov_b32 m0, s72
	s_nop 0
	global_load_lds_dwordx4 v167, s[10:11]
	s_waitcnt vmcnt(6)
	s_waitcnt lgkmcnt(0)
	s_barrier
	s_setprio 1
	s_waitcnt lgkmcnt(0)
	v_mfma_f32_16x16x128_f8f6f4 v[94:97], v[10:17], v[178:185], v[94:97]
	v_mfma_f32_16x16x128_f8f6f4 v[90:93], v[2:9], v[178:185], v[90:93]
	v_mfma_f32_16x16x128_f8f6f4 v[86:89], v[26:33], v[178:185], v[86:89]
	v_mfma_f32_16x16x128_f8f6f4 v[82:85], v[18:25], v[178:185], v[82:85]
	v_mfma_f32_16x16x128_f8f6f4 v[66:69], v[18:25], v[186:193], v[66:69]
	v_mfma_f32_16x16x128_f8f6f4 v[70:73], v[26:33], v[186:193], v[70:73]
	v_mfma_f32_16x16x128_f8f6f4 v[74:77], v[2:9], v[186:193], v[74:77]
	v_mfma_f32_16x16x128_f8f6f4 v[78:81], v[10:17], v[186:193], v[78:81]
	v_mfma_f32_16x16x128_f8f6f4 v[62:65], v[10:17], v[202:209], v[62:65]
	v_mfma_f32_16x16x128_f8f6f4 v[58:61], v[2:9], v[202:209], v[58:61]
	v_mfma_f32_16x16x128_f8f6f4 v[54:57], v[26:33], v[202:209], v[54:57]
	v_mfma_f32_16x16x128_f8f6f4 v[50:53], v[18:25], v[202:209], v[50:53]
	v_mfma_f32_16x16x128_f8f6f4 v[34:37], v[18:25], v[210:217], v[34:37]
	v_mfma_f32_16x16x128_f8f6f4 v[38:41], v[26:33], v[210:217], v[38:41]
	v_mfma_f32_16x16x128_f8f6f4 v[42:45], v[2:9], v[210:217], v[42:45]
	v_mfma_f32_16x16x128_f8f6f4 v[46:49], v[10:17], v[210:217], v[46:49]
	s_setprio 0
	s_barrier
	ds_read_b128 v[26:29], v165
	ds_read_b128 v[30:33], v165 offset:1024
	ds_read_b128 v[18:21], v165 offset:2048
	ds_read_b128 v[22:25], v165 offset:3072
	ds_read_b128 v[10:13], v166
	ds_read_b128 v[14:17], v166 offset:1024
	ds_read_b128 v[2:5], v166 offset:2048
	ds_read_b128 v[6:9], v166 offset:3072
	s_mov_b64 s[10:11], s[42:43]
	v_mov_b32_e32 v167, v170
	s_mov_b32 m0, s64
	ds_read_b128 v[178:181], v164 offset:32768
	ds_read_b128 v[182:185], v164 offset:33792
	ds_read_b128 v[186:189], v164 offset:34816
	ds_read_b128 v[190:193], v164 offset:35840
	ds_read_b128 v[202:205], v164 offset:36864
	ds_read_b128 v[206:209], v164 offset:37888
	ds_read_b128 v[210:213], v164 offset:38912
	ds_read_b128 v[214:217], v164 offset:39936
	s_nop 0
	global_load_lds_dwordx4 v167, s[10:11]
	v_mov_b32_e32 v167, v171
	s_mov_b32 m0, s45
	s_nop 0
	global_load_lds_dwordx4 v167, s[10:11]
	s_add_u32 s10, s42, 0xb0000
	s_addc_u32 s11, s43, 0
	v_mov_b32_e32 v167, v170
	s_mov_b32 m0, s65
	s_nop 0
	global_load_lds_dwordx4 v167, s[10:11]
	v_mov_b32_e32 v167, v171
	s_mov_b32 m0, s66
	s_nop 0
	global_load_lds_dwordx4 v167, s[10:11]
	s_waitcnt vmcnt(8)
	s_waitcnt lgkmcnt(0)
	s_barrier
	s_setprio 1
	s_waitcnt lgkmcnt(0)
	v_mfma_f32_16x16x128_f8f6f4 v[146:149], v[26:33], v[178:185], v[146:149]
	v_mfma_f32_16x16x128_f8f6f4 v[150:153], v[18:25], v[178:185], v[150:153]
	v_mfma_f32_16x16x128_f8f6f4 v[154:157], v[10:17], v[178:185], v[154:157]
	v_mfma_f32_16x16x128_f8f6f4 v[158:161], v[2:9], v[178:185], v[158:161]
	v_mfma_f32_16x16x128_f8f6f4 v[98:101], v[2:9], v[186:193], v[98:101]
	v_mfma_f32_16x16x128_f8f6f4 v[102:105], v[10:17], v[186:193], v[102:105]
	v_mfma_f32_16x16x128_f8f6f4 v[106:109], v[18:25], v[186:193], v[106:109]
	v_mfma_f32_16x16x128_f8f6f4 v[110:113], v[26:33], v[186:193], v[110:113]
	v_mfma_f32_16x16x128_f8f6f4 v[142:145], v[26:33], v[202:209], v[142:145]
	v_mfma_f32_16x16x128_f8f6f4 v[138:141], v[18:25], v[202:209], v[138:141]
	v_mfma_f32_16x16x128_f8f6f4 v[134:137], v[10:17], v[202:209], v[134:137]
	v_mfma_f32_16x16x128_f8f6f4 v[130:133], v[2:9], v[202:209], v[130:133]
	v_mfma_f32_16x16x128_f8f6f4 v[114:117], v[2:9], v[210:217], v[114:117]
	v_mfma_f32_16x16x128_f8f6f4 v[118:121], v[10:17], v[210:217], v[118:121]
	v_mfma_f32_16x16x128_f8f6f4 v[122:125], v[18:25], v[210:217], v[122:125]
	v_mfma_f32_16x16x128_f8f6f4 v[126:129], v[26:33], v[210:217], v[126:129]
	s_setprio 0
	s_barrier
	v_mov_b32_e32 v167, v170
	s_mov_b32 m0, s69
	ds_read_b128 v[178:181], v164 offset:49152
	ds_read_b128 v[182:185], v164 offset:50176
	ds_read_b128 v[186:189], v164 offset:51200
	ds_read_b128 v[190:193], v164 offset:52224
	ds_read_b128 v[202:205], v164 offset:53248
	ds_read_b128 v[206:209], v164 offset:54272
	ds_read_b128 v[210:213], v164 offset:55296
	ds_read_b128 v[214:217], v164 offset:56320
	s_add_u32 s10, s16, 0xb4000
	global_load_lds_dwordx4 v167, s[40:41]
	v_mov_b32_e32 v167, v171
	s_mov_b32 m0, s70
	s_addc_u32 s11, s17, 0
	global_load_lds_dwordx4 v167, s[40:41]
	v_mov_b32_e32 v167, v170
	s_mov_b32 m0, s46
	s_nop 0
	global_load_lds_dwordx4 v167, s[10:11]
	v_mov_b32_e32 v167, v171
	s_mov_b32 m0, s47
	s_nop 0
	global_load_lds_dwordx4 v167, s[10:11]
	s_waitcnt vmcnt(6)
	s_waitcnt lgkmcnt(0)
	s_barrier
	s_setprio 1
	s_waitcnt lgkmcnt(0)
	v_mfma_f32_16x16x128_f8f6f4 v[94:97], v[26:33], v[178:185], v[94:97]
	v_mfma_f32_16x16x128_f8f6f4 v[90:93], v[18:25], v[178:185], v[90:93]
	v_mfma_f32_16x16x128_f8f6f4 v[86:89], v[10:17], v[178:185], v[86:89]
	v_mfma_f32_16x16x128_f8f6f4 v[82:85], v[2:9], v[178:185], v[82:85]
	v_mfma_f32_16x16x128_f8f6f4 v[66:69], v[2:9], v[186:193], v[66:69]
	v_mfma_f32_16x16x128_f8f6f4 v[70:73], v[10:17], v[186:193], v[70:73]
	v_mfma_f32_16x16x128_f8f6f4 v[74:77], v[18:25], v[186:193], v[74:77]
	v_mfma_f32_16x16x128_f8f6f4 v[78:81], v[26:33], v[186:193], v[78:81]
	v_mfma_f32_16x16x128_f8f6f4 v[62:65], v[26:33], v[202:209], v[62:65]
	v_mfma_f32_16x16x128_f8f6f4 v[58:61], v[18:25], v[202:209], v[58:61]
	v_mfma_f32_16x16x128_f8f6f4 v[54:57], v[10:17], v[202:209], v[54:57]
	v_mfma_f32_16x16x128_f8f6f4 v[50:53], v[2:9], v[202:209], v[50:53]
	v_mfma_f32_16x16x128_f8f6f4 v[34:37], v[2:9], v[210:217], v[34:37]
	v_mfma_f32_16x16x128_f8f6f4 v[38:41], v[10:17], v[210:217], v[38:41]
	v_mfma_f32_16x16x128_f8f6f4 v[42:45], v[18:25], v[210:217], v[42:45]
	v_mfma_f32_16x16x128_f8f6f4 v[46:49], v[26:33], v[210:217], v[46:49]
	s_setprio 0
	s_barrier
	s_add_i32 s67, s67, 2
	s_add_u32 s30, s30, 0x8000
	s_addc_u32 s31, s31, 0
	s_cmp_gt_u32 s67, 41
	s_mov_b64 s[40:41], s[14:15]
	s_cbranch_scc0 .LBB0_978
	s_cmpk_lt_u32 s62, 0x100
	s_cbranch_scc0 .LBB0_981
	s_barrier

.LBB0_1525:
	s_add_u32 s46, s40, 0x100
	s_addc_u32 s47, s41, 0
	s_add_u32 s48, s42, 0x100
	s_waitcnt vmcnt(8)
	s_addc_u32 s49, s43, 0
	s_waitcnt lgkmcnt(0)
	s_add_u32 s44, s42, 0x180
	s_addc_u32 s45, s43, 0
	s_barrier
	s_setprio 1
	s_waitcnt lgkmcnt(0)
	v_mfma_f32_16x16x128_f8f6f4 v[154:157], v[2:9], v[58:65], 0
	v_mfma_f32_16x16x128_f8f6f4 v[146:149], v[10:17], v[58:65], 0
	v_mfma_f32_16x16x128_f8f6f4 v[158:161], v[18:25], v[58:65], 0
	v_mfma_f32_16x16x128_f8f6f4 v[150:153], v[26:33], v[58:65], 0
	v_mfma_f32_16x16x128_f8f6f4 v[134:137], v[26:33], v[50:57], 0
	v_mfma_f32_16x16x128_f8f6f4 v[142:145], v[18:25], v[50:57], 0
	v_mfma_f32_16x16x128_f8f6f4 v[130:133], v[10:17], v[50:57], 0
	v_mfma_f32_16x16x128_f8f6f4 v[138:141], v[2:9], v[50:57], 0
	v_mfma_f32_16x16x128_f8f6f4 v[122:125], v[2:9], v[42:49], 0
	v_mfma_f32_16x16x128_f8f6f4 v[114:117], v[10:17], v[42:49], 0
	v_mfma_f32_16x16x128_f8f6f4 v[126:129], v[18:25], v[42:49], 0
	v_mfma_f32_16x16x128_f8f6f4 v[118:121], v[26:33], v[42:49], 0
	v_mfma_f32_16x16x128_f8f6f4 v[102:105], v[26:33], v[34:41], 0
	v_mfma_f32_16x16x128_f8f6f4 v[110:113], v[18:25], v[34:41], 0
	v_mfma_f32_16x16x128_f8f6f4 v[98:101], v[10:17], v[34:41], 0
	v_mfma_f32_16x16x128_f8f6f4 v[106:109], v[2:9], v[34:41], 0
	s_setprio 0
	s_barrier
	v_mov_b32_e32 v50, v167
	s_mov_b32 m0, s35
	ds_read_b128 v[34:37], v173 offset:16384
	ds_read_b128 v[38:41], v173 offset:17408
	ds_read_b128 v[42:45], v173 offset:18432
	ds_read_b128 v[46:49], v173 offset:19456
	ds_read_b128 v[176:179], v173 offset:20480
	ds_read_b128 v[180:183], v173 offset:21504
	ds_read_b128 v[184:187], v173 offset:22528
	ds_read_b128 v[188:191], v173 offset:23552
	s_nop 0
	global_load_lds_dwordx4 v50, s[48:49]
	v_mov_b32_e32 v50, v169
	s_mov_b32 m0, s50
	s_nop 0
	global_load_lds_dwordx4 v50, s[48:49]
	s_add_u32 s48, s42, 0x40100
	s_addc_u32 s49, s43, 0
	v_mov_b32_e32 v50, v167
	s_mov_b32 m0, s51
	s_nop 0
	global_load_lds_dwordx4 v50, s[48:49]
	v_mov_b32_e32 v50, v169
	s_mov_b32 m0, s52
	s_nop 0
	global_load_lds_dwordx4 v50, s[48:49]
	s_waitcnt vmcnt(6)
	s_waitcnt lgkmcnt(0)
	s_barrier
	s_setprio 1
	s_waitcnt lgkmcnt(0)
	v_mfma_f32_16x16x128_f8f6f4 v[90:93], v[2:9], v[34:41], 0
	v_mfma_f32_16x16x128_f8f6f4 v[82:85], v[10:17], v[34:41], 0
	v_mfma_f32_16x16x128_f8f6f4 v[94:97], v[18:25], v[34:41], 0
	v_mfma_f32_16x16x128_f8f6f4 v[86:89], v[26:33], v[34:41], 0
	v_mfma_f32_16x16x128_f8f6f4 v[70:73], v[26:33], v[42:49], 0
	v_mfma_f32_16x16x128_f8f6f4 v[78:81], v[18:25], v[42:49], 0
	v_mfma_f32_16x16x128_f8f6f4 v[66:69], v[10:17], v[42:49], 0
	v_mfma_f32_16x16x128_f8f6f4 v[74:77], v[2:9], v[42:49], 0
	v_mfma_f32_16x16x128_f8f6f4 v[58:61], v[2:9], v[176:183], 0
	v_mfma_f32_16x16x128_f8f6f4 v[50:53], v[10:17], v[176:183], 0
	v_mfma_f32_16x16x128_f8f6f4 v[62:65], v[18:25], v[176:183], 0
	v_mfma_f32_16x16x128_f8f6f4 v[54:57], v[26:33], v[176:183], 0
	v_mfma_f32_16x16x128_f8f6f4 v[38:41], v[26:33], v[184:191], 0
	v_mfma_f32_16x16x128_f8f6f4 v[46:49], v[18:25], v[184:191], 0
	v_mfma_f32_16x16x128_f8f6f4 v[34:37], v[10:17], v[184:191], 0
	v_mfma_f32_16x16x128_f8f6f4 v[42:45], v[2:9], v[184:191], 0
	s_setprio 0
	s_barrier
	s_add_i32 s15, 0, 0x18000
	s_add_i32 s48, 0, 0x1c000
	v_add_u32_e32 v175, s15, v170
	v_add_u32_e32 v176, s48, v170
	ds_read_b128 v[26:29], v175
	ds_read_b128 v[30:33], v175 offset:1024
	ds_read_b128 v[18:21], v175 offset:2048
	ds_read_b128 v[22:25], v175 offset:3072
	ds_read_b128 v[10:13], v176
	ds_read_b128 v[14:17], v176 offset:1024
	ds_read_b128 v[2:5], v176 offset:2048
	ds_read_b128 v[6:9], v176 offset:3072
	v_mov_b32_e32 v177, v166
	s_mov_b32 m0, s33
	ds_read_b128 v[178:181], v173 offset:32768
	ds_read_b128 v[182:185], v173 offset:33792
	ds_read_b128 v[186:189], v173 offset:34816
	ds_read_b128 v[190:193], v173 offset:35840
	ds_read_b128 v[202:205], v173 offset:36864
	ds_read_b128 v[206:209], v173 offset:37888
	ds_read_b128 v[210:213], v173 offset:38912
	ds_read_b128 v[214:217], v173 offset:39936
	s_nop 0
	global_load_lds_dwordx4 v177, s[46:47]
	v_mov_b32_e32 v177, v168
	s_mov_b32 m0, s53
	s_nop 0
	global_load_lds_dwordx4 v177, s[46:47]
	s_add_u32 s46, s40, 0x40100
	s_addc_u32 s47, s41, 0
	v_mov_b32_e32 v177, v166
	s_mov_b32 m0, s60
	s_nop 0
	global_load_lds_dwordx4 v177, s[46:47]
	v_mov_b32_e32 v177, v168
	s_mov_b32 m0, s61
	s_nop 0
	global_load_lds_dwordx4 v177, s[46:47]
	s_waitcnt vmcnt(8)
	s_waitcnt lgkmcnt(0)
	s_barrier
	s_setprio 1
	s_waitcnt lgkmcnt(0)
	v_mfma_f32_16x16x128_f8f6f4 v[154:157], v[26:33], v[178:185], v[154:157]
	v_mfma_f32_16x16x128_f8f6f4 v[146:149], v[18:25], v[178:185], v[146:149]
	v_mfma_f32_16x16x128_f8f6f4 v[158:161], v[10:17], v[178:185], v[158:161]
	v_mfma_f32_16x16x128_f8f6f4 v[150:153], v[2:9], v[178:185], v[150:153]
	v_mfma_f32_16x16x128_f8f6f4 v[134:137], v[2:9], v[186:193], v[134:137]
	v_mfma_f32_16x16x128_f8f6f4 v[142:145], v[10:17], v[186:193], v[142:145]
	v_mfma_f32_16x16x128_f8f6f4 v[130:133], v[18:25], v[186:193], v[130:133]
	v_mfma_f32_16x16x128_f8f6f4 v[138:141], v[26:33], v[186:193], v[138:141]
	v_mfma_f32_16x16x128_f8f6f4 v[122:125], v[26:33], v[202:209], v[122:125]
	v_mfma_f32_16x16x128_f8f6f4 v[114:117], v[18:25], v[202:209], v[114:117]
	v_mfma_f32_16x16x128_f8f6f4 v[126:129], v[10:17], v[202:209], v[126:129]
	v_mfma_f32_16x16x128_f8f6f4 v[118:121], v[2:9], v[202:209], v[118:121]
	v_mfma_f32_16x16x128_f8f6f4 v[102:105], v[2:9], v[210:217], v[102:105]
	v_mfma_f32_16x16x128_f8f6f4 v[110:113], v[10:17], v[210:217], v[110:113]
	v_mfma_f32_16x16x128_f8f6f4 v[98:101], v[18:25], v[210:217], v[98:101]
	v_mfma_f32_16x16x128_f8f6f4 v[106:109], v[26:33], v[210:217], v[106:109]
	s_setprio 0
	s_barrier
	v_mov_b32_e32 v177, v167
	s_add_i32 s15, s15, s10
	ds_read_b128 v[178:181], v173 offset:49152
	ds_read_b128 v[182:185], v173 offset:50176
	ds_read_b128 v[186:189], v173 offset:51200
	ds_read_b128 v[190:193], v173 offset:52224
	ds_read_b128 v[202:205], v173 offset:53248
	ds_read_b128 v[206:209], v173 offset:54272
	ds_read_b128 v[210:213], v173 offset:55296
	ds_read_b128 v[214:217], v173 offset:56320
	s_mov_b32 m0, s15
	s_add_i32 s17, s15, 0x2000
	global_load_lds_dwordx4 v177, s[44:45]
	v_mov_b32_e32 v177, v169
	s_mov_b32 m0, s17
	s_nop 0
	global_load_lds_dwordx4 v177, s[44:45]
	s_add_u32 s44, s42, 0x40180
	s_addc_u32 s45, s43, 0
	v_mov_b32_e32 v177, v167
	s_add_i32 s48, s48, s10
	s_mov_b32 m0, s48
	s_add_i32 s49, s48, 0x2000
	global_load_lds_dwordx4 v177, s[44:45]
	v_mov_b32_e32 v177, v169
	s_mov_b32 m0, s49
	s_nop 0
	global_load_lds_dwordx4 v177, s[44:45]
	s_waitcnt vmcnt(6)
	s_waitcnt lgkmcnt(0)
	s_barrier
	s_setprio 1
	s_waitcnt lgkmcnt(0)
	v_mfma_f32_16x16x128_f8f6f4 v[90:93], v[26:33], v[178:185], v[90:93]
	v_mfma_f32_16x16x128_f8f6f4 v[82:85], v[18:25], v[178:185], v[82:85]
	v_mfma_f32_16x16x128_f8f6f4 v[94:97], v[10:17], v[178:185], v[94:97]
	v_mfma_f32_16x16x128_f8f6f4 v[86:89], v[2:9], v[178:185], v[86:89]
	v_mfma_f32_16x16x128_f8f6f4 v[70:73], v[2:9], v[186:193], v[70:73]
	v_mfma_f32_16x16x128_f8f6f4 v[78:81], v[10:17], v[186:193], v[78:81]
	v_mfma_f32_16x16x128_f8f6f4 v[66:69], v[18:25], v[186:193], v[66:69]
	v_mfma_f32_16x16x128_f8f6f4 v[74:77], v[26:33], v[186:193], v[74:77]
	v_mfma_f32_16x16x128_f8f6f4 v[58:61], v[26:33], v[202:209], v[58:61]
	v_mfma_f32_16x16x128_f8f6f4 v[50:53], v[18:25], v[202:209], v[50:53]
	v_mfma_f32_16x16x128_f8f6f4 v[62:65], v[10:17], v[202:209], v[62:65]
	v_mfma_f32_16x16x128_f8f6f4 v[54:57], v[2:9], v[202:209], v[54:57]
	v_mfma_f32_16x16x128_f8f6f4 v[38:41], v[2:9], v[210:217], v[38:41]
	v_mfma_f32_16x16x128_f8f6f4 v[46:49], v[10:17], v[210:217], v[46:49]
	v_mfma_f32_16x16x128_f8f6f4 v[34:37], v[18:25], v[210:217], v[34:37]
	v_mfma_f32_16x16x128_f8f6f4 v[42:45], v[26:33], v[210:217], v[42:45]
	s_setprio 0
	s_barrier
	s_add_u32 s44, s40, 0x100
	s_addc_u32 s45, s41, 0
	s_add_u32 s71, s42, 0x200
	s_addc_u32 s72, s43, 0
	s_mov_b32 s73, 0
.LBB0_1526:
	s_add_u32 s40, s44, 0x100
	s_addc_u32 s41, s45, 0
	s_add_i32 s76, 0, 0x10000
	s_cmp_eq_u32 s73, 12
	s_cselect_b32 s43, s25, s72
	s_cselect_b32 s42, s24, s71
	s_cselect_b32 s47, s19, s41
	s_cselect_b32 s46, s18, s40
	s_add_i32 s77, 0, 0x14000
	v_add_u32_e32 v6, s76, v170
	v_add_u32_e32 v22, s77, v170
	ds_read_b128 v[10:13], v6
	ds_read_b128 v[14:17], v6 offset:1024
	ds_read_b128 v[2:5], v6 offset:2048
	ds_read_b128 v[6:9], v6 offset:3072
	ds_read_b128 v[26:29], v22
	ds_read_b128 v[30:33], v22 offset:1024
	ds_read_b128 v[18:21], v22 offset:2048
	ds_read_b128 v[22:25], v22 offset:3072
	s_add_u32 s74, s44, 0x80
	s_addc_u32 s75, s45, 0
	v_mov_b32_e32 v177, v166
	s_mov_b32 m0, s64
	ds_read_b128 v[178:181], v173
	ds_read_b128 v[182:185], v173 offset:1024
	ds_read_b128 v[186:189], v173 offset:2048
	ds_read_b128 v[190:193], v173 offset:3072
	ds_read_b128 v[202:205], v173 offset:4096
	ds_read_b128 v[206:209], v173 offset:5120
	ds_read_b128 v[210:213], v173 offset:6144
	ds_read_b128 v[214:217], v173 offset:7168
	s_add_u32 s44, s44, 0x40080
	global_load_lds_dwordx4 v177, s[74:75]
	v_mov_b32_e32 v177, v168
	s_mov_b32 m0, s65
	s_addc_u32 s45, s45, 0
	global_load_lds_dwordx4 v177, s[74:75]
	v_mov_b32_e32 v177, v166
	s_mov_b32 m0, s66
	s_nop 0
	global_load_lds_dwordx4 v177, s[44:45]
	v_mov_b32_e32 v177, v168
	s_mov_b32 m0, s67
	s_nop 0
	global_load_lds_dwordx4 v177, s[44:45]
	s_waitcnt vmcnt(8)
	s_waitcnt lgkmcnt(0)
	s_add_u32 s44, s42, 0x80
	s_addc_u32 s45, s43, 0
	s_barrier
	s_setprio 1
	s_waitcnt lgkmcnt(0)
	v_mfma_f32_16x16x128_f8f6f4 v[154:157], v[10:17], v[178:185], v[154:157]
	v_mfma_f32_16x16x128_f8f6f4 v[146:149], v[2:9], v[178:185], v[146:149]
	v_mfma_f32_16x16x128_f8f6f4 v[158:161], v[26:33], v[178:185], v[158:161]
	v_mfma_f32_16x16x128_f8f6f4 v[150:153], v[18:25], v[178:185], v[150:153]
	v_mfma_f32_16x16x128_f8f6f4 v[134:137], v[18:25], v[186:193], v[134:137]
	v_mfma_f32_16x16x128_f8f6f4 v[142:145], v[26:33], v[186:193], v[142:145]
	v_mfma_f32_16x16x128_f8f6f4 v[130:133], v[2:9], v[186:193], v[130:133]
	v_mfma_f32_16x16x128_f8f6f4 v[138:141], v[10:17], v[186:193], v[138:141]
	v_mfma_f32_16x16x128_f8f6f4 v[122:125], v[10:17], v[202:209], v[122:125]
	v_mfma_f32_16x16x128_f8f6f4 v[114:117], v[2:9], v[202:209], v[114:117]
	v_mfma_f32_16x16x128_f8f6f4 v[126:129], v[26:33], v[202:209], v[126:129]
	v_mfma_f32_16x16x128_f8f6f4 v[118:121], v[18:25], v[202:209], v[118:121]
	v_mfma_f32_16x16x128_f8f6f4 v[102:105], v[18:25], v[210:217], v[102:105]
	v_mfma_f32_16x16x128_f8f6f4 v[110:113], v[26:33], v[210:217], v[110:113]
	v_mfma_f32_16x16x128_f8f6f4 v[98:101], v[2:9], v[210:217], v[98:101]
	v_mfma_f32_16x16x128_f8f6f4 v[106:109], v[10:17], v[210:217], v[106:109]
	s_setprio 0
	s_barrier
	s_mov_b64 s[74:75], s[42:43]
	v_mov_b32_e32 v177, v167
	s_add_i32 s76, s76, s10
	ds_read_b128 v[178:181], v173 offset:16384
	ds_read_b128 v[182:185], v173 offset:17408
	ds_read_b128 v[186:189], v173 offset:18432
	ds_read_b128 v[190:193], v173 offset:19456
	ds_read_b128 v[202:205], v173 offset:20480
	ds_read_b128 v[206:209], v173 offset:21504
	ds_read_b128 v[210:213], v173 offset:22528
	ds_read_b128 v[214:217], v173 offset:23552
	s_mov_b32 m0, s76
	s_nop 0
	global_load_lds_dwordx4 v177, s[74:75]
	v_mov_b32_e32 v177, v169
	s_add_i32 m0, s76, 0x2000
	s_nop 0
	global_load_lds_dwordx4 v177, s[74:75]
	s_add_u32 s74, s42, 0x40000
	s_addc_u32 s75, s43, 0
	v_mov_b32_e32 v177, v167
	s_add_i32 s76, s77, s10
	s_mov_b32 m0, s76
	s_nop 0
	global_load_lds_dwordx4 v177, s[74:75]
	v_mov_b32_e32 v177, v169
	s_add_i32 m0, s76, 0x2000
	s_nop 0
	global_load_lds_dwordx4 v177, s[74:75]
	s_waitcnt vmcnt(6)
	s_waitcnt lgkmcnt(0)
	s_barrier
	s_setprio 1
	s_waitcnt lgkmcnt(0)
	v_mfma_f32_16x16x128_f8f6f4 v[90:93], v[10:17], v[178:185], v[90:93]
	v_mfma_f32_16x16x128_f8f6f4 v[82:85], v[2:9], v[178:185], v[82:85]
	v_mfma_f32_16x16x128_f8f6f4 v[94:97], v[26:33], v[178:185], v[94:97]
	v_mfma_f32_16x16x128_f8f6f4 v[86:89], v[18:25], v[178:185], v[86:89]
	v_mfma_f32_16x16x128_f8f6f4 v[70:73], v[18:25], v[186:193], v[70:73]
	v_mfma_f32_16x16x128_f8f6f4 v[78:81], v[26:33], v[186:193], v[78:81]
	v_mfma_f32_16x16x128_f8f6f4 v[66:69], v[2:9], v[186:193], v[66:69]
	v_mfma_f32_16x16x128_f8f6f4 v[74:77], v[10:17], v[186:193], v[74:77]
	v_mfma_f32_16x16x128_f8f6f4 v[58:61], v[10:17], v[202:209], v[58:61]
	v_mfma_f32_16x16x128_f8f6f4 v[50:53], v[2:9], v[202:209], v[50:53]
	v_mfma_f32_16x16x128_f8f6f4 v[62:65], v[26:33], v[202:209], v[62:65]
	v_mfma_f32_16x16x128_f8f6f4 v[54:57], v[18:25], v[202:209], v[54:57]
	v_mfma_f32_16x16x128_f8f6f4 v[38:41], v[18:25], v[210:217], v[38:41]
	v_mfma_f32_16x16x128_f8f6f4 v[46:49], v[26:33], v[210:217], v[46:49]
	v_mfma_f32_16x16x128_f8f6f4 v[34:37], v[2:9], v[210:217], v[34:37]
	v_mfma_f32_16x16x128_f8f6f4 v[42:45], v[10:17], v[210:217], v[42:45]
	s_setprio 0
	s_barrier
	ds_read_b128 v[26:29], v175
	ds_read_b128 v[30:33], v175 offset:1024
	ds_read_b128 v[18:21], v175 offset:2048
	ds_read_b128 v[22:25], v175 offset:3072
	ds_read_b128 v[10:13], v176
	ds_read_b128 v[14:17], v176 offset:1024
	ds_read_b128 v[2:5], v176 offset:2048
	ds_read_b128 v[6:9], v176 offset:3072
	s_mov_b64 s[74:75], s[46:47]
	v_mov_b32_e32 v177, v166
	s_mov_b32 m0, s33
	ds_read_b128 v[178:181], v173 offset:32768
	ds_read_b128 v[182:185], v173 offset:33792
	ds_read_b128 v[186:189], v173 offset:34816
	ds_read_b128 v[190:193], v173 offset:35840
	ds_read_b128 v[202:205], v173 offset:36864
	ds_read_b128 v[206:209], v173 offset:37888
	ds_read_b128 v[210:213], v173 offset:38912
	ds_read_b128 v[214:217], v173 offset:39936
	s_add_u32 s46, s46, 0x40000
	global_load_lds_dwordx4 v177, s[74:75]
	v_mov_b32_e32 v177, v168
	s_mov_b32 m0, s53
	s_addc_u32 s47, s47, 0
	global_load_lds_dwordx4 v177, s[74:75]
	v_mov_b32_e32 v177, v166
	s_mov_b32 m0, s60
	s_nop 0
	global_load_lds_dwordx4 v177, s[46:47]
	v_mov_b32_e32 v177, v168
	s_mov_b32 m0, s61
	s_nop 0
	global_load_lds_dwordx4 v177, s[46:47]
	s_waitcnt vmcnt(8)
	s_waitcnt lgkmcnt(0)
	s_barrier
	s_setprio 1
	s_waitcnt lgkmcnt(0)
	v_mfma_f32_16x16x128_f8f6f4 v[154:157], v[26:33], v[178:185], v[154:157]
	v_mfma_f32_16x16x128_f8f6f4 v[146:149], v[18:25], v[178:185], v[146:149]
	v_mfma_f32_16x16x128_f8f6f4 v[158:161], v[10:17], v[178:185], v[158:161]
	v_mfma_f32_16x16x128_f8f6f4 v[150:153], v[2:9], v[178:185], v[150:153]
	v_mfma_f32_16x16x128_f8f6f4 v[134:137], v[2:9], v[186:193], v[134:137]
	v_mfma_f32_16x16x128_f8f6f4 v[142:145], v[10:17], v[186:193], v[142:145]
	v_mfma_f32_16x16x128_f8f6f4 v[130:133], v[18:25], v[186:193], v[130:133]
	v_mfma_f32_16x16x128_f8f6f4 v[138:141], v[26:33], v[186:193], v[138:141]
	v_mfma_f32_16x16x128_f8f6f4 v[122:125], v[26:33], v[202:209], v[122:125]
	v_mfma_f32_16x16x128_f8f6f4 v[114:117], v[18:25], v[202:209], v[114:117]
	v_mfma_f32_16x16x128_f8f6f4 v[126:129], v[10:17], v[202:209], v[126:129]
	v_mfma_f32_16x16x128_f8f6f4 v[118:121], v[2:9], v[202:209], v[118:121]
	v_mfma_f32_16x16x128_f8f6f4 v[102:105], v[2:9], v[210:217], v[102:105]
	v_mfma_f32_16x16x128_f8f6f4 v[110:113], v[10:17], v[210:217], v[110:113]
	v_mfma_f32_16x16x128_f8f6f4 v[98:101], v[18:25], v[210:217], v[98:101]
	v_mfma_f32_16x16x128_f8f6f4 v[106:109], v[26:33], v[210:217], v[106:109]
	s_setprio 0
	s_barrier
	v_mov_b32_e32 v177, v167
	s_mov_b32 m0, s15
	ds_read_b128 v[178:181], v173 offset:49152
	ds_read_b128 v[182:185], v173 offset:50176
	ds_read_b128 v[186:189], v173 offset:51200
	ds_read_b128 v[190:193], v173 offset:52224
	ds_read_b128 v[202:205], v173 offset:53248
	ds_read_b128 v[206:209], v173 offset:54272
	ds_read_b128 v[210:213], v173 offset:55296
	ds_read_b128 v[214:217], v173 offset:56320
	s_add_u32 s42, s42, 0x40080
	global_load_lds_dwordx4 v177, s[44:45]
	v_mov_b32_e32 v177, v169
	s_mov_b32 m0, s17
	s_addc_u32 s43, s43, 0
	global_load_lds_dwordx4 v177, s[44:45]
	v_mov_b32_e32 v177, v167
	s_mov_b32 m0, s48
	s_nop 0
	global_load_lds_dwordx4 v177, s[42:43]
	v_mov_b32_e32 v177, v169
	s_mov_b32 m0, s49
	s_nop 0
	global_load_lds_dwordx4 v177, s[42:43]
	s_waitcnt vmcnt(6)
	s_waitcnt lgkmcnt(0)
	s_barrier
	s_setprio 1
	s_waitcnt lgkmcnt(0)
	v_mfma_f32_16x16x128_f8f6f4 v[90:93], v[26:33], v[178:185], v[90:93]
	v_mfma_f32_16x16x128_f8f6f4 v[82:85], v[18:25], v[178:185], v[82:85]
	v_mfma_f32_16x16x128_f8f6f4 v[94:97], v[10:17], v[178:185], v[94:97]
	v_mfma_f32_16x16x128_f8f6f4 v[86:89], v[2:9], v[178:185], v[86:89]
	v_mfma_f32_16x16x128_f8f6f4 v[70:73], v[2:9], v[186:193], v[70:73]
	v_mfma_f32_16x16x128_f8f6f4 v[78:81], v[10:17], v[186:193], v[78:81]
	v_mfma_f32_16x16x128_f8f6f4 v[66:69], v[18:25], v[186:193], v[66:69]
	v_mfma_f32_16x16x128_f8f6f4 v[74:77], v[26:33], v[186:193], v[74:77]
	v_mfma_f32_16x16x128_f8f6f4 v[58:61], v[26:33], v[202:209], v[58:61]
	v_mfma_f32_16x16x128_f8f6f4 v[50:53], v[18:25], v[202:209], v[50:53]
	v_mfma_f32_16x16x128_f8f6f4 v[62:65], v[10:17], v[202:209], v[62:65]
	v_mfma_f32_16x16x128_f8f6f4 v[54:57], v[2:9], v[202:209], v[54:57]
	v_mfma_f32_16x16x128_f8f6f4 v[38:41], v[2:9], v[210:217], v[38:41]
	v_mfma_f32_16x16x128_f8f6f4 v[46:49], v[10:17], v[210:217], v[46:49]
	v_mfma_f32_16x16x128_f8f6f4 v[34:37], v[18:25], v[210:217], v[34:37]
	v_mfma_f32_16x16x128_f8f6f4 v[42:45], v[26:33], v[210:217], v[42:45]
	s_setprio 0
	s_barrier
	s_add_i32 s73, s73, 2
	s_add_u32 s71, s71, 0x100
	s_addc_u32 s72, s72, 0
	s_cmp_gt_u32 s73, 13
	s_mov_b64 s[44:45], s[40:41]
	s_cbranch_scc0 .LBB0_1526
	s_and_b64 vcc, exec, s[6:7]
	s_cbranch_vccz .LBB0_1529
	s_barrier

.LBB0_1598:
	s_add_u32 s44, s0, 0x8000
	s_addc_u32 s45, s1, 0
	s_add_u32 s46, s40, 0x8000
	s_waitcnt vmcnt(8)
	s_addc_u32 s47, s41, 0
	s_waitcnt lgkmcnt(0)
	s_add_u32 s42, s40, 0xc000
	s_addc_u32 s43, s41, 0
	s_barrier
	s_setprio 1
	s_waitcnt lgkmcnt(0)
	v_mfma_f32_16x16x128_f8f6f4 v[146:149], v[2:9], v[58:65], 0
	v_mfma_f32_16x16x128_f8f6f4 v[150:153], v[10:17], v[58:65], 0
	v_mfma_f32_16x16x128_f8f6f4 v[154:157], v[18:25], v[58:65], 0
	v_mfma_f32_16x16x128_f8f6f4 v[158:161], v[26:33], v[58:65], 0
	v_mfma_f32_16x16x128_f8f6f4 v[130:133], v[26:33], v[50:57], 0
	v_mfma_f32_16x16x128_f8f6f4 v[134:137], v[18:25], v[50:57], 0
	v_mfma_f32_16x16x128_f8f6f4 v[138:141], v[10:17], v[50:57], 0
	v_mfma_f32_16x16x128_f8f6f4 v[142:145], v[2:9], v[50:57], 0
	v_mfma_f32_16x16x128_f8f6f4 v[126:129], v[2:9], v[42:49], 0
	v_mfma_f32_16x16x128_f8f6f4 v[122:125], v[10:17], v[42:49], 0
	v_mfma_f32_16x16x128_f8f6f4 v[118:121], v[18:25], v[42:49], 0
	v_mfma_f32_16x16x128_f8f6f4 v[114:117], v[26:33], v[42:49], 0
	v_mfma_f32_16x16x128_f8f6f4 v[82:85], v[26:33], v[34:41], 0
	v_mfma_f32_16x16x128_f8f6f4 v[90:93], v[18:25], v[34:41], 0
	v_mfma_f32_16x16x128_f8f6f4 v[106:109], v[10:17], v[34:41], 0
	v_mfma_f32_16x16x128_f8f6f4 v[110:113], v[2:9], v[34:41], 0
	s_setprio 0
	s_barrier
	v_mov_b32_e32 v50, v180
	s_mov_b32 m0, s50
	ds_read_b128 v[34:37], v173 offset:16384
	ds_read_b128 v[38:41], v173 offset:17408
	ds_read_b128 v[42:45], v173 offset:18432
	ds_read_b128 v[46:49], v173 offset:19456
	ds_read_b128 v[182:185], v173 offset:20480
	ds_read_b128 v[186:189], v173 offset:21504
	ds_read_b128 v[190:193], v173 offset:22528
	ds_read_b128 v[194:197], v173 offset:23552
	s_nop 0
	global_load_lds_dwordx4 v50, s[46:47]
	v_mov_b32_e32 v50, v181
	s_mov_b32 m0, s51
	s_nop 0
	global_load_lds_dwordx4 v50, s[46:47]
	s_add_u32 s46, s40, 0xe8000
	s_addc_u32 s47, s41, 0
	v_mov_b32_e32 v50, v180
	s_mov_b32 m0, s52
	s_nop 0
	global_load_lds_dwordx4 v50, s[46:47]
	v_mov_b32_e32 v50, v181
	s_mov_b32 m0, s53
	s_nop 0
	global_load_lds_dwordx4 v50, s[46:47]
	s_waitcnt vmcnt(6)
	s_waitcnt lgkmcnt(0)
	s_barrier
	s_setprio 1
	s_waitcnt lgkmcnt(0)
	v_mfma_f32_16x16x128_f8f6f4 v[102:105], v[2:9], v[34:41], 0
	v_mfma_f32_16x16x128_f8f6f4 v[98:101], v[10:17], v[34:41], 0
	v_mfma_f32_16x16x128_f8f6f4 v[94:97], v[18:25], v[34:41], 0
	v_mfma_f32_16x16x128_f8f6f4 v[86:89], v[26:33], v[34:41], 0
	v_mfma_f32_16x16x128_f8f6f4 v[66:69], v[26:33], v[42:49], 0
	v_mfma_f32_16x16x128_f8f6f4 v[70:73], v[18:25], v[42:49], 0
	v_mfma_f32_16x16x128_f8f6f4 v[74:77], v[10:17], v[42:49], 0
	v_mfma_f32_16x16x128_f8f6f4 v[78:81], v[2:9], v[42:49], 0
	v_mfma_f32_16x16x128_f8f6f4 v[62:65], v[2:9], v[182:189], 0
	v_mfma_f32_16x16x128_f8f6f4 v[58:61], v[10:17], v[182:189], 0
	v_mfma_f32_16x16x128_f8f6f4 v[54:57], v[18:25], v[182:189], 0
	v_mfma_f32_16x16x128_f8f6f4 v[50:53], v[26:33], v[182:189], 0
	v_mfma_f32_16x16x128_f8f6f4 v[34:37], v[26:33], v[190:197], 0
	v_mfma_f32_16x16x128_f8f6f4 v[38:41], v[18:25], v[190:197], 0
	v_mfma_f32_16x16x128_f8f6f4 v[42:45], v[10:17], v[190:197], 0
	v_mfma_f32_16x16x128_f8f6f4 v[46:49], v[2:9], v[190:197], 0
	s_setprio 0
	s_barrier
	s_add_i32 s46, 0, 0x18000
	s_add_i32 s76, 0, 0x1c000
	v_add_u32_e32 v174, s46, v169
	v_add_u32_e32 v175, s76, v169
	ds_read_b128 v[26:29], v174
	ds_read_b128 v[30:33], v174 offset:1024
	ds_read_b128 v[18:21], v174 offset:2048
	ds_read_b128 v[22:25], v174 offset:3072
	ds_read_b128 v[10:13], v175
	ds_read_b128 v[14:17], v175 offset:1024
	ds_read_b128 v[2:5], v175 offset:2048
	ds_read_b128 v[6:9], v175 offset:3072
	v_mov_b32_e32 v176, v180
	s_mov_b32 m0, s49
	ds_read_b128 v[182:185], v173 offset:32768
	ds_read_b128 v[186:189], v173 offset:33792
	ds_read_b128 v[190:193], v173 offset:34816
	ds_read_b128 v[194:197], v173 offset:35840
	ds_read_b128 v[198:201], v173 offset:36864
	ds_read_b128 v[202:205], v173 offset:37888
	ds_read_b128 v[206:209], v173 offset:38912
	ds_read_b128 v[210:213], v173 offset:39936
	s_nop 0
	global_load_lds_dwordx4 v176, s[44:45]
	v_mov_b32_e32 v176, v181
	s_mov_b32 m0, s60
	s_nop 0
	global_load_lds_dwordx4 v176, s[44:45]
	s_add_u32 s44, s0, 0xe8000
	s_addc_u32 s45, s1, 0
	v_mov_b32_e32 v176, v180
	s_mov_b32 m0, s61
	s_nop 0
	global_load_lds_dwordx4 v176, s[44:45]
	v_mov_b32_e32 v176, v181
	s_mov_b32 m0, s62
	s_nop 0
	global_load_lds_dwordx4 v176, s[44:45]
	s_waitcnt vmcnt(8)
	s_waitcnt lgkmcnt(0)
	s_barrier
	s_setprio 1
	s_waitcnt lgkmcnt(0)
	v_mfma_f32_16x16x128_f8f6f4 v[146:149], v[26:33], v[182:189], v[146:149]
	v_mfma_f32_16x16x128_f8f6f4 v[150:153], v[18:25], v[182:189], v[150:153]
	v_mfma_f32_16x16x128_f8f6f4 v[154:157], v[10:17], v[182:189], v[154:157]
	v_mfma_f32_16x16x128_f8f6f4 v[158:161], v[2:9], v[182:189], v[158:161]
	v_mfma_f32_16x16x128_f8f6f4 v[130:133], v[2:9], v[190:197], v[130:133]
	v_mfma_f32_16x16x128_f8f6f4 v[134:137], v[10:17], v[190:197], v[134:137]
	v_mfma_f32_16x16x128_f8f6f4 v[138:141], v[18:25], v[190:197], v[138:141]
	v_mfma_f32_16x16x128_f8f6f4 v[142:145], v[26:33], v[190:197], v[142:145]
	v_mfma_f32_16x16x128_f8f6f4 v[126:129], v[26:33], v[198:205], v[126:129]
	v_mfma_f32_16x16x128_f8f6f4 v[122:125], v[18:25], v[198:205], v[122:125]
	v_mfma_f32_16x16x128_f8f6f4 v[118:121], v[10:17], v[198:205], v[118:121]
	v_mfma_f32_16x16x128_f8f6f4 v[114:117], v[2:9], v[198:205], v[114:117]
	v_mfma_f32_16x16x128_f8f6f4 v[82:85], v[2:9], v[206:213], v[82:85]
	v_mfma_f32_16x16x128_f8f6f4 v[90:93], v[10:17], v[206:213], v[90:93]
	v_mfma_f32_16x16x128_f8f6f4 v[106:109], v[18:25], v[206:213], v[106:109]
	v_mfma_f32_16x16x128_f8f6f4 v[110:113], v[26:33], v[206:213], v[110:113]
	s_setprio 0
	s_barrier
	v_mov_b32_e32 v176, v180
	s_add_i32 s46, s46, s33
	ds_read_b128 v[182:185], v173 offset:49152
	ds_read_b128 v[186:189], v173 offset:50176
	ds_read_b128 v[190:193], v173 offset:51200
	ds_read_b128 v[194:197], v173 offset:52224
	ds_read_b128 v[198:201], v173 offset:53248
	ds_read_b128 v[202:205], v173 offset:54272
	ds_read_b128 v[206:209], v173 offset:55296
	ds_read_b128 v[210:213], v173 offset:56320
	s_mov_b32 m0, s46
	s_add_i32 s47, s46, 0x2000
	global_load_lds_dwordx4 v176, s[42:43]
	v_mov_b32_e32 v176, v181
	s_mov_b32 m0, s47
	s_nop 0
	global_load_lds_dwordx4 v176, s[42:43]
	s_add_u32 s42, s40, 0xec000
	s_addc_u32 s43, s41, 0
	v_mov_b32_e32 v176, v180
	s_add_i32 s76, s76, s33
	s_mov_b32 m0, s76
	s_add_i32 s77, s76, 0x2000
	global_load_lds_dwordx4 v176, s[42:43]
	v_mov_b32_e32 v176, v181
	s_mov_b32 m0, s77
	s_nop 0
	global_load_lds_dwordx4 v176, s[42:43]
	s_waitcnt vmcnt(6)
	s_waitcnt lgkmcnt(0)
	s_barrier
	s_setprio 1
	s_waitcnt lgkmcnt(0)
	v_mfma_f32_16x16x128_f8f6f4 v[102:105], v[26:33], v[182:189], v[102:105]
	v_mfma_f32_16x16x128_f8f6f4 v[98:101], v[18:25], v[182:189], v[98:101]
	v_mfma_f32_16x16x128_f8f6f4 v[94:97], v[10:17], v[182:189], v[94:97]
	v_mfma_f32_16x16x128_f8f6f4 v[86:89], v[2:9], v[182:189], v[86:89]
	v_mfma_f32_16x16x128_f8f6f4 v[66:69], v[2:9], v[190:197], v[66:69]
	v_mfma_f32_16x16x128_f8f6f4 v[70:73], v[10:17], v[190:197], v[70:73]
	v_mfma_f32_16x16x128_f8f6f4 v[74:77], v[18:25], v[190:197], v[74:77]
	v_mfma_f32_16x16x128_f8f6f4 v[78:81], v[26:33], v[190:197], v[78:81]
	v_mfma_f32_16x16x128_f8f6f4 v[62:65], v[26:33], v[198:205], v[62:65]
	v_mfma_f32_16x16x128_f8f6f4 v[58:61], v[18:25], v[198:205], v[58:61]
	v_mfma_f32_16x16x128_f8f6f4 v[54:57], v[10:17], v[198:205], v[54:57]
	v_mfma_f32_16x16x128_f8f6f4 v[50:53], v[2:9], v[198:205], v[50:53]
	v_mfma_f32_16x16x128_f8f6f4 v[34:37], v[2:9], v[206:213], v[34:37]
	v_mfma_f32_16x16x128_f8f6f4 v[38:41], v[10:17], v[206:213], v[38:41]
	v_mfma_f32_16x16x128_f8f6f4 v[42:45], v[18:25], v[206:213], v[42:45]
	v_mfma_f32_16x16x128_f8f6f4 v[46:49], v[26:33], v[206:213], v[46:49]
	s_setprio 0
	s_barrier
	s_add_u32 s42, s0, 0x8000
	s_addc_u32 s43, s1, 0
	s_add_u32 s78, s40, 0x10000
	s_addc_u32 s79, s41, 0
	s_mov_b32 s80, 0
.LBB0_1599:
	s_add_u32 s0, s42, 0x8000
	s_addc_u32 s1, s43, 0
	s_add_i32 s81, 0, 0x10000
	s_cmp_eq_u32 s80, 52
	s_cselect_b32 s41, s39, s79
	s_cselect_b32 s40, s38, s78
	s_cselect_b32 s45, s31, s1
	s_cselect_b32 s44, s30, s0
	s_add_i32 s84, 0, 0x14000
	v_add_u32_e32 v6, s81, v169
	v_add_u32_e32 v22, s84, v169
	ds_read_b128 v[10:13], v6
	ds_read_b128 v[14:17], v6 offset:1024
	ds_read_b128 v[2:5], v6 offset:2048
	ds_read_b128 v[6:9], v6 offset:3072
	ds_read_b128 v[26:29], v22
	ds_read_b128 v[30:33], v22 offset:1024
	ds_read_b128 v[18:21], v22 offset:2048
	ds_read_b128 v[22:25], v22 offset:3072
	s_add_u32 s82, s42, 0x4000
	s_addc_u32 s83, s43, 0
	v_mov_b32_e32 v176, v180
	s_mov_b32 m0, s64
	ds_read_b128 v[182:185], v173
	ds_read_b128 v[186:189], v173 offset:1024
	ds_read_b128 v[190:193], v173 offset:2048
	ds_read_b128 v[194:197], v173 offset:3072
	ds_read_b128 v[198:201], v173 offset:4096
	ds_read_b128 v[202:205], v173 offset:5120
	ds_read_b128 v[206:209], v173 offset:6144
	ds_read_b128 v[210:213], v173 offset:7168
	s_add_u32 s42, s42, 0xe4000
	global_load_lds_dwordx4 v176, s[82:83]
	v_mov_b32_e32 v176, v181
	s_mov_b32 m0, s65
	s_addc_u32 s43, s43, 0
	global_load_lds_dwordx4 v176, s[82:83]
	v_mov_b32_e32 v176, v180
	s_mov_b32 m0, s66
	s_nop 0
	global_load_lds_dwordx4 v176, s[42:43]
	v_mov_b32_e32 v176, v181
	s_mov_b32 m0, s67
	s_nop 0
	global_load_lds_dwordx4 v176, s[42:43]
	s_waitcnt vmcnt(8)
	s_waitcnt lgkmcnt(0)
	s_add_u32 s42, s40, 0x4000
	s_addc_u32 s43, s41, 0
	s_barrier
	s_setprio 1
	s_waitcnt lgkmcnt(0)
	v_mfma_f32_16x16x128_f8f6f4 v[146:149], v[10:17], v[182:189], v[146:149]
	v_mfma_f32_16x16x128_f8f6f4 v[150:153], v[2:9], v[182:189], v[150:153]
	v_mfma_f32_16x16x128_f8f6f4 v[154:157], v[26:33], v[182:189], v[154:157]
	v_mfma_f32_16x16x128_f8f6f4 v[158:161], v[18:25], v[182:189], v[158:161]
	v_mfma_f32_16x16x128_f8f6f4 v[130:133], v[18:25], v[190:197], v[130:133]
	v_mfma_f32_16x16x128_f8f6f4 v[134:137], v[26:33], v[190:197], v[134:137]
	v_mfma_f32_16x16x128_f8f6f4 v[138:141], v[2:9], v[190:197], v[138:141]
	v_mfma_f32_16x16x128_f8f6f4 v[142:145], v[10:17], v[190:197], v[142:145]
	v_mfma_f32_16x16x128_f8f6f4 v[126:129], v[10:17], v[198:205], v[126:129]
	v_mfma_f32_16x16x128_f8f6f4 v[122:125], v[2:9], v[198:205], v[122:125]
	v_mfma_f32_16x16x128_f8f6f4 v[118:121], v[26:33], v[198:205], v[118:121]
	v_mfma_f32_16x16x128_f8f6f4 v[114:117], v[18:25], v[198:205], v[114:117]
	v_mfma_f32_16x16x128_f8f6f4 v[82:85], v[18:25], v[206:213], v[82:85]
	v_mfma_f32_16x16x128_f8f6f4 v[90:93], v[26:33], v[206:213], v[90:93]
	v_mfma_f32_16x16x128_f8f6f4 v[106:109], v[2:9], v[206:213], v[106:109]
	v_mfma_f32_16x16x128_f8f6f4 v[110:113], v[10:17], v[206:213], v[110:113]
	s_setprio 0
	s_barrier
	s_mov_b64 s[82:83], s[40:41]
	v_mov_b32_e32 v176, v180
	s_add_i32 s81, s81, s33
	ds_read_b128 v[182:185], v173 offset:16384
	ds_read_b128 v[186:189], v173 offset:17408
	ds_read_b128 v[190:193], v173 offset:18432
	ds_read_b128 v[194:197], v173 offset:19456
	ds_read_b128 v[198:201], v173 offset:20480
	ds_read_b128 v[202:205], v173 offset:21504
	ds_read_b128 v[206:209], v173 offset:22528
	ds_read_b128 v[210:213], v173 offset:23552
	s_mov_b32 m0, s81
	s_nop 0
	global_load_lds_dwordx4 v176, s[82:83]
	v_mov_b32_e32 v176, v181
	s_add_i32 m0, s81, 0x2000
	s_nop 0
	global_load_lds_dwordx4 v176, s[82:83]
	s_add_u32 s82, s40, 0xe0000
	s_addc_u32 s83, s41, 0
	v_mov_b32_e32 v176, v180
	s_add_i32 s81, s84, s33
	s_mov_b32 m0, s81
	s_nop 0
	global_load_lds_dwordx4 v176, s[82:83]
	v_mov_b32_e32 v176, v181
	s_add_i32 m0, s81, 0x2000
	s_nop 0
	global_load_lds_dwordx4 v176, s[82:83]
	s_waitcnt vmcnt(6)
	s_waitcnt lgkmcnt(0)
	s_barrier
	s_setprio 1
	s_waitcnt lgkmcnt(0)
	v_mfma_f32_16x16x128_f8f6f4 v[102:105], v[10:17], v[182:189], v[102:105]
	v_mfma_f32_16x16x128_f8f6f4 v[98:101], v[2:9], v[182:189], v[98:101]
	v_mfma_f32_16x16x128_f8f6f4 v[94:97], v[26:33], v[182:189], v[94:97]
	v_mfma_f32_16x16x128_f8f6f4 v[86:89], v[18:25], v[182:189], v[86:89]
	v_mfma_f32_16x16x128_f8f6f4 v[66:69], v[18:25], v[190:197], v[66:69]
	v_mfma_f32_16x16x128_f8f6f4 v[70:73], v[26:33], v[190:197], v[70:73]
	v_mfma_f32_16x16x128_f8f6f4 v[74:77], v[2:9], v[190:197], v[74:77]
	v_mfma_f32_16x16x128_f8f6f4 v[78:81], v[10:17], v[190:197], v[78:81]
	v_mfma_f32_16x16x128_f8f6f4 v[62:65], v[10:17], v[198:205], v[62:65]
	v_mfma_f32_16x16x128_f8f6f4 v[58:61], v[2:9], v[198:205], v[58:61]
	v_mfma_f32_16x16x128_f8f6f4 v[54:57], v[26:33], v[198:205], v[54:57]
	v_mfma_f32_16x16x128_f8f6f4 v[50:53], v[18:25], v[198:205], v[50:53]
	v_mfma_f32_16x16x128_f8f6f4 v[34:37], v[18:25], v[206:213], v[34:37]
	v_mfma_f32_16x16x128_f8f6f4 v[38:41], v[26:33], v[206:213], v[38:41]
	v_mfma_f32_16x16x128_f8f6f4 v[42:45], v[2:9], v[206:213], v[42:45]
	v_mfma_f32_16x16x128_f8f6f4 v[46:49], v[10:17], v[206:213], v[46:49]
	s_setprio 0
	s_barrier
	ds_read_b128 v[26:29], v174
	ds_read_b128 v[30:33], v174 offset:1024
	ds_read_b128 v[18:21], v174 offset:2048
	ds_read_b128 v[22:25], v174 offset:3072
	ds_read_b128 v[10:13], v175
	ds_read_b128 v[14:17], v175 offset:1024
	ds_read_b128 v[2:5], v175 offset:2048
	ds_read_b128 v[6:9], v175 offset:3072
	s_mov_b64 s[82:83], s[44:45]
	v_mov_b32_e32 v176, v180
	s_mov_b32 m0, s49
	ds_read_b128 v[182:185], v173 offset:32768
	ds_read_b128 v[186:189], v173 offset:33792
	ds_read_b128 v[190:193], v173 offset:34816
	ds_read_b128 v[194:197], v173 offset:35840
	ds_read_b128 v[198:201], v173 offset:36864
	ds_read_b128 v[202:205], v173 offset:37888
	ds_read_b128 v[206:209], v173 offset:38912
	ds_read_b128 v[210:213], v173 offset:39936
	s_add_u32 s44, s44, 0xe0000
	global_load_lds_dwordx4 v176, s[82:83]
	v_mov_b32_e32 v176, v181
	s_mov_b32 m0, s60
	s_addc_u32 s45, s45, 0
	global_load_lds_dwordx4 v176, s[82:83]
	v_mov_b32_e32 v176, v180
	s_mov_b32 m0, s61
	s_nop 0
	global_load_lds_dwordx4 v176, s[44:45]
	v_mov_b32_e32 v176, v181
	s_mov_b32 m0, s62
	s_nop 0
	global_load_lds_dwordx4 v176, s[44:45]
	s_waitcnt vmcnt(8)
	s_waitcnt lgkmcnt(0)
	s_barrier
	s_setprio 1
	s_waitcnt lgkmcnt(0)
	v_mfma_f32_16x16x128_f8f6f4 v[146:149], v[26:33], v[182:189], v[146:149]
	v_mfma_f32_16x16x128_f8f6f4 v[150:153], v[18:25], v[182:189], v[150:153]
	v_mfma_f32_16x16x128_f8f6f4 v[154:157], v[10:17], v[182:189], v[154:157]
	v_mfma_f32_16x16x128_f8f6f4 v[158:161], v[2:9], v[182:189], v[158:161]
	v_mfma_f32_16x16x128_f8f6f4 v[130:133], v[2:9], v[190:197], v[130:133]
	v_mfma_f32_16x16x128_f8f6f4 v[134:137], v[10:17], v[190:197], v[134:137]
	v_mfma_f32_16x16x128_f8f6f4 v[138:141], v[18:25], v[190:197], v[138:141]
	v_mfma_f32_16x16x128_f8f6f4 v[142:145], v[26:33], v[190:197], v[142:145]
	v_mfma_f32_16x16x128_f8f6f4 v[126:129], v[26:33], v[198:205], v[126:129]
	v_mfma_f32_16x16x128_f8f6f4 v[122:125], v[18:25], v[198:205], v[122:125]
	v_mfma_f32_16x16x128_f8f6f4 v[118:121], v[10:17], v[198:205], v[118:121]
	v_mfma_f32_16x16x128_f8f6f4 v[114:117], v[2:9], v[198:205], v[114:117]
	v_mfma_f32_16x16x128_f8f6f4 v[82:85], v[2:9], v[206:213], v[82:85]
	v_mfma_f32_16x16x128_f8f6f4 v[90:93], v[10:17], v[206:213], v[90:93]
	v_mfma_f32_16x16x128_f8f6f4 v[106:109], v[18:25], v[206:213], v[106:109]
	v_mfma_f32_16x16x128_f8f6f4 v[110:113], v[26:33], v[206:213], v[110:113]
	s_setprio 0
	s_barrier
	v_mov_b32_e32 v176, v180
	s_mov_b32 m0, s46
	ds_read_b128 v[182:185], v173 offset:49152
	ds_read_b128 v[186:189], v173 offset:50176
	ds_read_b128 v[190:193], v173 offset:51200
	ds_read_b128 v[194:197], v173 offset:52224
	ds_read_b128 v[198:201], v173 offset:53248
	ds_read_b128 v[202:205], v173 offset:54272
	ds_read_b128 v[206:209], v173 offset:55296
	ds_read_b128 v[210:213], v173 offset:56320
	s_add_u32 s40, s40, 0xe4000
	global_load_lds_dwordx4 v176, s[42:43]
	v_mov_b32_e32 v176, v181
	s_mov_b32 m0, s47
	s_addc_u32 s41, s41, 0
	global_load_lds_dwordx4 v176, s[42:43]
	v_mov_b32_e32 v176, v180
	s_mov_b32 m0, s76
	s_nop 0
	global_load_lds_dwordx4 v176, s[40:41]
	v_mov_b32_e32 v176, v181
	s_mov_b32 m0, s77
	s_nop 0
	global_load_lds_dwordx4 v176, s[40:41]
	s_waitcnt vmcnt(6)
	s_waitcnt lgkmcnt(0)
	s_barrier
	s_setprio 1
	s_waitcnt lgkmcnt(0)
	v_mfma_f32_16x16x128_f8f6f4 v[102:105], v[26:33], v[182:189], v[102:105]
	v_mfma_f32_16x16x128_f8f6f4 v[98:101], v[18:25], v[182:189], v[98:101]
	v_mfma_f32_16x16x128_f8f6f4 v[94:97], v[10:17], v[182:189], v[94:97]
	v_mfma_f32_16x16x128_f8f6f4 v[86:89], v[2:9], v[182:189], v[86:89]
	v_mfma_f32_16x16x128_f8f6f4 v[66:69], v[2:9], v[190:197], v[66:69]
	v_mfma_f32_16x16x128_f8f6f4 v[70:73], v[10:17], v[190:197], v[70:73]
	v_mfma_f32_16x16x128_f8f6f4 v[74:77], v[18:25], v[190:197], v[74:77]
	v_mfma_f32_16x16x128_f8f6f4 v[78:81], v[26:33], v[190:197], v[78:81]
	v_mfma_f32_16x16x128_f8f6f4 v[62:65], v[26:33], v[198:205], v[62:65]
	v_mfma_f32_16x16x128_f8f6f4 v[58:61], v[18:25], v[198:205], v[58:61]
	v_mfma_f32_16x16x128_f8f6f4 v[54:57], v[10:17], v[198:205], v[54:57]
	v_mfma_f32_16x16x128_f8f6f4 v[50:53], v[2:9], v[198:205], v[50:53]
	v_mfma_f32_16x16x128_f8f6f4 v[34:37], v[2:9], v[206:213], v[34:37]
	v_mfma_f32_16x16x128_f8f6f4 v[38:41], v[10:17], v[206:213], v[38:41]
	v_mfma_f32_16x16x128_f8f6f4 v[42:45], v[18:25], v[206:213], v[42:45]
	v_mfma_f32_16x16x128_f8f6f4 v[46:49], v[26:33], v[206:213], v[46:49]
	s_setprio 0
	s_barrier
	s_add_i32 s80, s80, 2
	s_add_u32 s78, s78, 0x8000
	s_addc_u32 s79, s79, 0
	s_cmp_gt_u32 s80, 53
	s_mov_b64 s[42:43], s[0:1]
	s_cbranch_scc0 .LBB0_1599
	s_and_b64 vcc, exec, s[8:9]
	s_cbranch_vccz .LBB0_1602
	s_barrier

.LBB0_1615:
	s_add_u32 s30, s16, 0x8000
	s_addc_u32 s31, s17, 0
	s_waitcnt vmcnt(8)
	s_add_u32 s38, s18, 0x8000
	s_waitcnt lgkmcnt(0)
	s_addc_u32 s39, s19, 0
	s_add_u32 s24, s18, 0xc000
	s_addc_u32 s25, s19, 0
	s_barrier
	s_setprio 1
	s_waitcnt lgkmcnt(0)
	v_mfma_f32_16x16x128_f8f6f4 v[146:149], v[2:9], v[58:65], 0
	v_mfma_f32_16x16x128_f8f6f4 v[150:153], v[10:17], v[58:65], 0
	v_mfma_f32_16x16x128_f8f6f4 v[154:157], v[18:25], v[58:65], 0
	v_mfma_f32_16x16x128_f8f6f4 v[158:161], v[26:33], v[58:65], 0
	v_mfma_f32_16x16x128_f8f6f4 v[130:133], v[26:33], v[50:57], 0
	v_mfma_f32_16x16x128_f8f6f4 v[134:137], v[18:25], v[50:57], 0
	v_mfma_f32_16x16x128_f8f6f4 v[138:141], v[10:17], v[50:57], 0
	v_mfma_f32_16x16x128_f8f6f4 v[142:145], v[2:9], v[50:57], 0
	v_mfma_f32_16x16x128_f8f6f4 v[126:129], v[2:9], v[42:49], 0
	v_mfma_f32_16x16x128_f8f6f4 v[122:125], v[10:17], v[42:49], 0
	v_mfma_f32_16x16x128_f8f6f4 v[118:121], v[18:25], v[42:49], 0
	v_mfma_f32_16x16x128_f8f6f4 v[114:117], v[26:33], v[42:49], 0
	v_mfma_f32_16x16x128_f8f6f4 v[98:101], v[26:33], v[34:41], 0
	v_mfma_f32_16x16x128_f8f6f4 v[102:105], v[18:25], v[34:41], 0
	v_mfma_f32_16x16x128_f8f6f4 v[106:109], v[10:17], v[34:41], 0
	v_mfma_f32_16x16x128_f8f6f4 v[110:113], v[2:9], v[34:41], 0
	s_setprio 0
	s_barrier
	v_mov_b32_e32 v50, v180
	s_mov_b32 m0, s43
	ds_read_b128 v[34:37], v193 offset:16384
	ds_read_b128 v[38:41], v193 offset:17408
	ds_read_b128 v[42:45], v193 offset:18432
	ds_read_b128 v[46:49], v193 offset:19456
	ds_read_b128 v[194:197], v193 offset:20480
	ds_read_b128 v[198:201], v193 offset:21504
	ds_read_b128 v[202:205], v193 offset:22528
	ds_read_b128 v[206:209], v193 offset:23552
	s_nop 0
	global_load_lds_dwordx4 v50, s[38:39]
	v_mov_b32_e32 v50, v181
	s_mov_b32 m0, s44
	s_nop 0
	global_load_lds_dwordx4 v50, s[38:39]
	s_add_u32 s38, s18, 0xe8000
	s_addc_u32 s39, s19, 0
	v_mov_b32_e32 v50, v180
	s_mov_b32 m0, s45
	s_nop 0
	global_load_lds_dwordx4 v50, s[38:39]
	v_mov_b32_e32 v50, v181
	s_mov_b32 m0, s46
	s_nop 0
	global_load_lds_dwordx4 v50, s[38:39]
	s_waitcnt vmcnt(6)
	s_waitcnt lgkmcnt(0)
	s_barrier
	s_setprio 1
	s_waitcnt lgkmcnt(0)
	v_mfma_f32_16x16x128_f8f6f4 v[94:97], v[2:9], v[34:41], 0
	v_mfma_f32_16x16x128_f8f6f4 v[90:93], v[10:17], v[34:41], 0
	v_mfma_f32_16x16x128_f8f6f4 v[86:89], v[18:25], v[34:41], 0
	v_mfma_f32_16x16x128_f8f6f4 v[82:85], v[26:33], v[34:41], 0
	v_mfma_f32_16x16x128_f8f6f4 v[66:69], v[26:33], v[42:49], 0
	v_mfma_f32_16x16x128_f8f6f4 v[70:73], v[18:25], v[42:49], 0
	v_mfma_f32_16x16x128_f8f6f4 v[74:77], v[10:17], v[42:49], 0
	v_mfma_f32_16x16x128_f8f6f4 v[78:81], v[2:9], v[42:49], 0
	v_mfma_f32_16x16x128_f8f6f4 v[62:65], v[2:9], v[194:201], 0
	v_mfma_f32_16x16x128_f8f6f4 v[58:61], v[10:17], v[194:201], 0
	v_mfma_f32_16x16x128_f8f6f4 v[54:57], v[18:25], v[194:201], 0
	v_mfma_f32_16x16x128_f8f6f4 v[50:53], v[26:33], v[194:201], 0
	v_mfma_f32_16x16x128_f8f6f4 v[34:37], v[26:33], v[202:209], 0
	v_mfma_f32_16x16x128_f8f6f4 v[38:41], v[18:25], v[202:209], 0
	v_mfma_f32_16x16x128_f8f6f4 v[42:45], v[10:17], v[202:209], 0
	v_mfma_f32_16x16x128_f8f6f4 v[46:49], v[2:9], v[202:209], 0
	s_setprio 0
	s_barrier
	v_add_u32_e32 v194, s62, v183
	v_add_u32_e32 v195, s63, v183
	ds_read_b128 v[26:29], v194
	ds_read_b128 v[30:33], v194 offset:1024
	ds_read_b128 v[18:21], v194 offset:2048
	ds_read_b128 v[22:25], v194 offset:3072
	ds_read_b128 v[10:13], v195
	ds_read_b128 v[14:17], v195 offset:1024
	ds_read_b128 v[2:5], v195 offset:2048
	ds_read_b128 v[6:9], v195 offset:3072
	v_mov_b32_e32 v228, v180
	s_mov_b32 m0, s42
	ds_read_b128 v[196:199], v193 offset:32768
	ds_read_b128 v[200:203], v193 offset:33792
	ds_read_b128 v[204:207], v193 offset:34816
	ds_read_b128 v[208:211], v193 offset:35840
	ds_read_b128 v[212:215], v193 offset:36864
	ds_read_b128 v[216:219], v193 offset:37888
	ds_read_b128 v[220:223], v193 offset:38912
	ds_read_b128 v[224:227], v193 offset:39936
	s_nop 0
	global_load_lds_dwordx4 v228, s[30:31]
	v_mov_b32_e32 v228, v181
	s_mov_b32 m0, s47
	s_nop 0
	global_load_lds_dwordx4 v228, s[30:31]
	s_add_u32 s30, s16, 0xe8000
	s_addc_u32 s31, s17, 0
	v_mov_b32_e32 v228, v180
	s_mov_b32 m0, s48
	s_nop 0
	global_load_lds_dwordx4 v228, s[30:31]
	v_mov_b32_e32 v228, v181
	s_mov_b32 m0, s49
	s_nop 0
	global_load_lds_dwordx4 v228, s[30:31]
	s_waitcnt vmcnt(8)
	s_waitcnt lgkmcnt(0)
	s_barrier
	s_setprio 1
	s_waitcnt lgkmcnt(0)
	v_mfma_f32_16x16x128_f8f6f4 v[146:149], v[26:33], v[196:203], v[146:149]
	v_mfma_f32_16x16x128_f8f6f4 v[150:153], v[18:25], v[196:203], v[150:153]
	v_mfma_f32_16x16x128_f8f6f4 v[154:157], v[10:17], v[196:203], v[154:157]
	v_mfma_f32_16x16x128_f8f6f4 v[158:161], v[2:9], v[196:203], v[158:161]
	v_mfma_f32_16x16x128_f8f6f4 v[130:133], v[2:9], v[204:211], v[130:133]
	v_mfma_f32_16x16x128_f8f6f4 v[134:137], v[10:17], v[204:211], v[134:137]
	v_mfma_f32_16x16x128_f8f6f4 v[138:141], v[18:25], v[204:211], v[138:141]
	v_mfma_f32_16x16x128_f8f6f4 v[142:145], v[26:33], v[204:211], v[142:145]
	v_mfma_f32_16x16x128_f8f6f4 v[126:129], v[26:33], v[212:219], v[126:129]
	v_mfma_f32_16x16x128_f8f6f4 v[122:125], v[18:25], v[212:219], v[122:125]
	v_mfma_f32_16x16x128_f8f6f4 v[118:121], v[10:17], v[212:219], v[118:121]
	v_mfma_f32_16x16x128_f8f6f4 v[114:117], v[2:9], v[212:219], v[114:117]
	v_mfma_f32_16x16x128_f8f6f4 v[98:101], v[2:9], v[220:227], v[98:101]
	v_mfma_f32_16x16x128_f8f6f4 v[102:105], v[10:17], v[220:227], v[102:105]
	v_mfma_f32_16x16x128_f8f6f4 v[106:109], v[18:25], v[220:227], v[106:109]
	v_mfma_f32_16x16x128_f8f6f4 v[110:113], v[26:33], v[220:227], v[110:113]
	s_setprio 0
	s_barrier
	v_mov_b32_e32 v228, v180
	s_mov_b32 m0, s64
	ds_read_b128 v[196:199], v193 offset:49152
	ds_read_b128 v[200:203], v193 offset:50176
	ds_read_b128 v[204:207], v193 offset:51200
	ds_read_b128 v[208:211], v193 offset:52224
	ds_read_b128 v[212:215], v193 offset:53248
	ds_read_b128 v[216:219], v193 offset:54272
	ds_read_b128 v[220:223], v193 offset:55296
	ds_read_b128 v[224:227], v193 offset:56320
	s_nop 0
	global_load_lds_dwordx4 v228, s[24:25]
	v_mov_b32_e32 v228, v181
	s_mov_b32 m0, s65
	s_nop 0
	global_load_lds_dwordx4 v228, s[24:25]
	s_add_u32 s24, s18, 0xec000
	s_addc_u32 s25, s19, 0
	v_mov_b32_e32 v228, v180
	s_mov_b32 m0, s66
	s_nop 0
	global_load_lds_dwordx4 v228, s[24:25]
	v_mov_b32_e32 v228, v181
	s_mov_b32 m0, s67
	s_nop 0
	global_load_lds_dwordx4 v228, s[24:25]
	s_waitcnt vmcnt(6)
	s_waitcnt lgkmcnt(0)
	s_barrier
	s_setprio 1
	s_waitcnt lgkmcnt(0)
	v_mfma_f32_16x16x128_f8f6f4 v[94:97], v[26:33], v[196:203], v[94:97]
	v_mfma_f32_16x16x128_f8f6f4 v[90:93], v[18:25], v[196:203], v[90:93]
	v_mfma_f32_16x16x128_f8f6f4 v[86:89], v[10:17], v[196:203], v[86:89]
	v_mfma_f32_16x16x128_f8f6f4 v[82:85], v[2:9], v[196:203], v[82:85]
	v_mfma_f32_16x16x128_f8f6f4 v[66:69], v[2:9], v[204:211], v[66:69]
	v_mfma_f32_16x16x128_f8f6f4 v[70:73], v[10:17], v[204:211], v[70:73]
	v_mfma_f32_16x16x128_f8f6f4 v[74:77], v[18:25], v[204:211], v[74:77]
	v_mfma_f32_16x16x128_f8f6f4 v[78:81], v[26:33], v[204:211], v[78:81]
	v_mfma_f32_16x16x128_f8f6f4 v[62:65], v[26:33], v[212:219], v[62:65]
	v_mfma_f32_16x16x128_f8f6f4 v[58:61], v[18:25], v[212:219], v[58:61]
	v_mfma_f32_16x16x128_f8f6f4 v[54:57], v[10:17], v[212:219], v[54:57]
	v_mfma_f32_16x16x128_f8f6f4 v[50:53], v[2:9], v[212:219], v[50:53]
	v_mfma_f32_16x16x128_f8f6f4 v[34:37], v[2:9], v[220:227], v[34:37]
	v_mfma_f32_16x16x128_f8f6f4 v[38:41], v[10:17], v[220:227], v[38:41]
	v_mfma_f32_16x16x128_f8f6f4 v[42:45], v[18:25], v[220:227], v[42:45]
	v_mfma_f32_16x16x128_f8f6f4 v[46:49], v[26:33], v[220:227], v[46:49]
	s_setprio 0
	s_barrier
	s_add_u32 s30, s18, 0x10000
	s_addc_u32 s31, s19, 0
	s_add_u32 s38, s16, 0x10000
	s_addc_u32 s39, s17, 0
	s_mov_b32 s71, 4
.LBB0_1616:
	s_add_i32 s74, 0, 0x10000
	s_cmp_eq_u32 s33, s71
	s_cselect_b32 s17, s7, s31
	s_cselect_b32 s16, s6, s30
	s_cselect_b32 s25, s5, s39
	s_cselect_b32 s24, s4, s38
	s_add_i32 s75, 0, 0x14000
	v_add_u32_e32 v6, s74, v183
	v_add_u32_e32 v22, s75, v183
	ds_read_b128 v[10:13], v6
	ds_read_b128 v[14:17], v6 offset:1024
	ds_read_b128 v[2:5], v6 offset:2048
	ds_read_b128 v[6:9], v6 offset:3072
	ds_read_b128 v[26:29], v22
	ds_read_b128 v[30:33], v22 offset:1024
	ds_read_b128 v[18:21], v22 offset:2048
	ds_read_b128 v[22:25], v22 offset:3072
	s_add_u32 s18, s38, 0xffffc000
	s_addc_u32 s19, s39, -1
	v_mov_b32_e32 v228, v180
	s_mov_b32 m0, s52
	ds_read_b128 v[196:199], v193
	ds_read_b128 v[200:203], v193 offset:1024
	ds_read_b128 v[204:207], v193 offset:2048
	ds_read_b128 v[208:211], v193 offset:3072
	ds_read_b128 v[212:215], v193 offset:4096
	ds_read_b128 v[216:219], v193 offset:5120
	ds_read_b128 v[220:223], v193 offset:6144
	ds_read_b128 v[224:227], v193 offset:7168
	s_nop 0
	global_load_lds_dwordx4 v228, s[18:19]
	v_mov_b32_e32 v228, v181
	s_mov_b32 m0, s53
	s_nop 0
	global_load_lds_dwordx4 v228, s[18:19]
	s_add_u32 s18, s38, 0xdc000
	s_addc_u32 s19, s39, 0
	v_mov_b32_e32 v228, v180
	s_mov_b32 m0, s60
	s_nop 0
	global_load_lds_dwordx4 v228, s[18:19]
	v_mov_b32_e32 v228, v181
	s_mov_b32 m0, s61
	s_nop 0
	global_load_lds_dwordx4 v228, s[18:19]
	s_waitcnt vmcnt(8)
	s_waitcnt lgkmcnt(0)
	s_add_u32 s18, s16, 0x4000
	s_addc_u32 s19, s17, 0
	s_barrier
	s_setprio 1
	s_waitcnt lgkmcnt(0)
	v_mfma_f32_16x16x128_f8f6f4 v[146:149], v[10:17], v[196:203], v[146:149]
	v_mfma_f32_16x16x128_f8f6f4 v[150:153], v[2:9], v[196:203], v[150:153]
	v_mfma_f32_16x16x128_f8f6f4 v[154:157], v[26:33], v[196:203], v[154:157]
	v_mfma_f32_16x16x128_f8f6f4 v[158:161], v[18:25], v[196:203], v[158:161]
	v_mfma_f32_16x16x128_f8f6f4 v[130:133], v[18:25], v[204:211], v[130:133]
	v_mfma_f32_16x16x128_f8f6f4 v[134:137], v[26:33], v[204:211], v[134:137]
	v_mfma_f32_16x16x128_f8f6f4 v[138:141], v[2:9], v[204:211], v[138:141]
	v_mfma_f32_16x16x128_f8f6f4 v[142:145], v[10:17], v[204:211], v[142:145]
	v_mfma_f32_16x16x128_f8f6f4 v[126:129], v[10:17], v[212:219], v[126:129]
	v_mfma_f32_16x16x128_f8f6f4 v[122:125], v[2:9], v[212:219], v[122:125]
	v_mfma_f32_16x16x128_f8f6f4 v[118:121], v[26:33], v[212:219], v[118:121]
	v_mfma_f32_16x16x128_f8f6f4 v[114:117], v[18:25], v[212:219], v[114:117]
	v_mfma_f32_16x16x128_f8f6f4 v[98:101], v[18:25], v[220:227], v[98:101]
	v_mfma_f32_16x16x128_f8f6f4 v[102:105], v[26:33], v[220:227], v[102:105]
	v_mfma_f32_16x16x128_f8f6f4 v[106:109], v[2:9], v[220:227], v[106:109]
	v_mfma_f32_16x16x128_f8f6f4 v[110:113], v[10:17], v[220:227], v[110:113]
	s_setprio 0
	s_barrier
	s_mov_b64 s[72:73], s[16:17]
	v_mov_b32_e32 v228, v180
	s_add_i32 s74, s74, s40
	ds_read_b128 v[196:199], v193 offset:16384
	ds_read_b128 v[200:203], v193 offset:17408
	ds_read_b128 v[204:207], v193 offset:18432
	ds_read_b128 v[208:211], v193 offset:19456
	ds_read_b128 v[212:215], v193 offset:20480
	ds_read_b128 v[216:219], v193 offset:21504
	ds_read_b128 v[220:223], v193 offset:22528
	ds_read_b128 v[224:227], v193 offset:23552
	s_mov_b32 m0, s74
	s_nop 0
	global_load_lds_dwordx4 v228, s[72:73]
	v_mov_b32_e32 v228, v181
	s_add_i32 m0, s74, 0x2000
	s_nop 0
	global_load_lds_dwordx4 v228, s[72:73]
	s_add_u32 s72, s16, 0xe0000
	s_addc_u32 s73, s17, 0
	v_mov_b32_e32 v228, v180
	s_add_i32 s74, s75, s40
	s_mov_b32 m0, s74
	s_nop 0
	global_load_lds_dwordx4 v228, s[72:73]
	v_mov_b32_e32 v228, v181
	s_add_i32 m0, s74, 0x2000
	s_nop 0
	global_load_lds_dwordx4 v228, s[72:73]
	s_waitcnt vmcnt(6)
	s_waitcnt lgkmcnt(0)
	s_barrier
	s_setprio 1
	s_waitcnt lgkmcnt(0)
	v_mfma_f32_16x16x128_f8f6f4 v[94:97], v[10:17], v[196:203], v[94:97]
	v_mfma_f32_16x16x128_f8f6f4 v[90:93], v[2:9], v[196:203], v[90:93]
	v_mfma_f32_16x16x128_f8f6f4 v[86:89], v[26:33], v[196:203], v[86:89]
	v_mfma_f32_16x16x128_f8f6f4 v[82:85], v[18:25], v[196:203], v[82:85]
	v_mfma_f32_16x16x128_f8f6f4 v[66:69], v[18:25], v[204:211], v[66:69]
	v_mfma_f32_16x16x128_f8f6f4 v[70:73], v[26:33], v[204:211], v[70:73]
	v_mfma_f32_16x16x128_f8f6f4 v[74:77], v[2:9], v[204:211], v[74:77]
	v_mfma_f32_16x16x128_f8f6f4 v[78:81], v[10:17], v[204:211], v[78:81]
	v_mfma_f32_16x16x128_f8f6f4 v[62:65], v[10:17], v[212:219], v[62:65]
	v_mfma_f32_16x16x128_f8f6f4 v[58:61], v[2:9], v[212:219], v[58:61]
	v_mfma_f32_16x16x128_f8f6f4 v[54:57], v[26:33], v[212:219], v[54:57]
	v_mfma_f32_16x16x128_f8f6f4 v[50:53], v[18:25], v[212:219], v[50:53]
	v_mfma_f32_16x16x128_f8f6f4 v[34:37], v[18:25], v[220:227], v[34:37]
	v_mfma_f32_16x16x128_f8f6f4 v[38:41], v[26:33], v[220:227], v[38:41]
	v_mfma_f32_16x16x128_f8f6f4 v[42:45], v[2:9], v[220:227], v[42:45]
	v_mfma_f32_16x16x128_f8f6f4 v[46:49], v[10:17], v[220:227], v[46:49]
	s_setprio 0
	s_barrier
	ds_read_b128 v[26:29], v194
	ds_read_b128 v[30:33], v194 offset:1024
	ds_read_b128 v[18:21], v194 offset:2048
	ds_read_b128 v[22:25], v194 offset:3072
	ds_read_b128 v[10:13], v195
	ds_read_b128 v[14:17], v195 offset:1024
	ds_read_b128 v[2:5], v195 offset:2048
	ds_read_b128 v[6:9], v195 offset:3072
	s_mov_b64 s[72:73], s[24:25]
	v_mov_b32_e32 v228, v180
	s_mov_b32 m0, s42
	ds_read_b128 v[196:199], v193 offset:32768
	ds_read_b128 v[200:203], v193 offset:33792
	ds_read_b128 v[204:207], v193 offset:34816
	ds_read_b128 v[208:211], v193 offset:35840
	ds_read_b128 v[212:215], v193 offset:36864
	ds_read_b128 v[216:219], v193 offset:37888
	ds_read_b128 v[220:223], v193 offset:38912
	ds_read_b128 v[224:227], v193 offset:39936
	s_add_u32 s24, s24, 0xe0000
	global_load_lds_dwordx4 v228, s[72:73]
	v_mov_b32_e32 v228, v181
	s_mov_b32 m0, s47
	s_addc_u32 s25, s25, 0
	global_load_lds_dwordx4 v228, s[72:73]
	v_mov_b32_e32 v228, v180
	s_mov_b32 m0, s48
	s_nop 0
	global_load_lds_dwordx4 v228, s[24:25]
	v_mov_b32_e32 v228, v181
	s_mov_b32 m0, s49
	s_nop 0
	global_load_lds_dwordx4 v228, s[24:25]
	s_waitcnt vmcnt(8)
	s_waitcnt lgkmcnt(0)
	s_barrier
	s_setprio 1
	s_waitcnt lgkmcnt(0)
	v_mfma_f32_16x16x128_f8f6f4 v[146:149], v[26:33], v[196:203], v[146:149]
	v_mfma_f32_16x16x128_f8f6f4 v[150:153], v[18:25], v[196:203], v[150:153]
	v_mfma_f32_16x16x128_f8f6f4 v[154:157], v[10:17], v[196:203], v[154:157]
	v_mfma_f32_16x16x128_f8f6f4 v[158:161], v[2:9], v[196:203], v[158:161]
	v_mfma_f32_16x16x128_f8f6f4 v[130:133], v[2:9], v[204:211], v[130:133]
	v_mfma_f32_16x16x128_f8f6f4 v[134:137], v[10:17], v[204:211], v[134:137]
	v_mfma_f32_16x16x128_f8f6f4 v[138:141], v[18:25], v[204:211], v[138:141]
	v_mfma_f32_16x16x128_f8f6f4 v[142:145], v[26:33], v[204:211], v[142:145]
	v_mfma_f32_16x16x128_f8f6f4 v[126:129], v[26:33], v[212:219], v[126:129]
	v_mfma_f32_16x16x128_f8f6f4 v[122:125], v[18:25], v[212:219], v[122:125]
	v_mfma_f32_16x16x128_f8f6f4 v[118:121], v[10:17], v[212:219], v[118:121]
	v_mfma_f32_16x16x128_f8f6f4 v[114:117], v[2:9], v[212:219], v[114:117]
	v_mfma_f32_16x16x128_f8f6f4 v[98:101], v[2:9], v[220:227], v[98:101]
	v_mfma_f32_16x16x128_f8f6f4 v[102:105], v[10:17], v[220:227], v[102:105]
	v_mfma_f32_16x16x128_f8f6f4 v[106:109], v[18:25], v[220:227], v[106:109]
	v_mfma_f32_16x16x128_f8f6f4 v[110:113], v[26:33], v[220:227], v[110:113]
	s_setprio 0
	s_barrier
	v_mov_b32_e32 v228, v180
	s_mov_b32 m0, s64
	ds_read_b128 v[196:199], v193 offset:49152
	ds_read_b128 v[200:203], v193 offset:50176
	ds_read_b128 v[204:207], v193 offset:51200
	ds_read_b128 v[208:211], v193 offset:52224
	ds_read_b128 v[212:215], v193 offset:53248
	ds_read_b128 v[216:219], v193 offset:54272
	ds_read_b128 v[220:223], v193 offset:55296
	ds_read_b128 v[224:227], v193 offset:56320
	s_add_u32 s16, s16, 0xe4000
	global_load_lds_dwordx4 v228, s[18:19]
	v_mov_b32_e32 v228, v181
	s_mov_b32 m0, s65
	s_addc_u32 s17, s17, 0
	global_load_lds_dwordx4 v228, s[18:19]
	v_mov_b32_e32 v228, v180
	s_mov_b32 m0, s66
	s_nop 0
	global_load_lds_dwordx4 v228, s[16:17]
	v_mov_b32_e32 v228, v181
	s_mov_b32 m0, s67
	s_nop 0
	global_load_lds_dwordx4 v228, s[16:17]
	s_waitcnt vmcnt(6)
	s_waitcnt lgkmcnt(0)
	s_barrier
	s_setprio 1
	s_waitcnt lgkmcnt(0)
	v_mfma_f32_16x16x128_f8f6f4 v[94:97], v[26:33], v[196:203], v[94:97]
	v_mfma_f32_16x16x128_f8f6f4 v[90:93], v[18:25], v[196:203], v[90:93]
	v_mfma_f32_16x16x128_f8f6f4 v[86:89], v[10:17], v[196:203], v[86:89]
	v_mfma_f32_16x16x128_f8f6f4 v[82:85], v[2:9], v[196:203], v[82:85]
	v_mfma_f32_16x16x128_f8f6f4 v[66:69], v[2:9], v[204:211], v[66:69]
	v_mfma_f32_16x16x128_f8f6f4 v[70:73], v[10:17], v[204:211], v[70:73]
	v_mfma_f32_16x16x128_f8f6f4 v[74:77], v[18:25], v[204:211], v[74:77]
	v_mfma_f32_16x16x128_f8f6f4 v[78:81], v[26:33], v[204:211], v[78:81]
	v_mfma_f32_16x16x128_f8f6f4 v[62:65], v[26:33], v[212:219], v[62:65]
	v_mfma_f32_16x16x128_f8f6f4 v[58:61], v[18:25], v[212:219], v[58:61]
	v_mfma_f32_16x16x128_f8f6f4 v[54:57], v[10:17], v[212:219], v[54:57]
	v_mfma_f32_16x16x128_f8f6f4 v[50:53], v[2:9], v[212:219], v[50:53]
	v_mfma_f32_16x16x128_f8f6f4 v[34:37], v[2:9], v[220:227], v[34:37]
	v_mfma_f32_16x16x128_f8f6f4 v[38:41], v[10:17], v[220:227], v[38:41]
	v_mfma_f32_16x16x128_f8f6f4 v[42:45], v[18:25], v[220:227], v[42:45]
	v_mfma_f32_16x16x128_f8f6f4 v[46:49], v[26:33], v[220:227], v[46:49]
	s_setprio 0
	s_barrier
	s_add_i32 s16, s71, 2
	s_add_u32 s30, s30, 0x8000
	s_addc_u32 s31, s31, 0
	s_add_u32 s38, s38, 0x8000
	s_addc_u32 s39, s39, 0
	s_cmp_ge_u32 s71, s51
	s_mov_b32 s71, s16
	s_cbranch_scc0 .LBB0_1616
	s_and_b64 vcc, exec, s[2:3]
	s_cbranch_vccz .LBB0_1619
	s_barrier
